# v13 + compute-segment edge trim: redundant post-barrier lgkmcnt wait removed, s_setprio 1 after the first MFMA, s_setprio 0 after the closing barrier (all GEMM K-loops)
# speedup vs baseline: 1.0126x; 1.0126x over previous
.LBB0_286:
	s_lshl_b32 s10, s51, 19
	s_add_u32 s10, s20, s10
	s_addc_u32 s11, s21, 0
	s_and_b64 s[16:17], s[4:5], exec
	s_cselect_b32 s54, s11, s31
	s_cselect_b32 s55, s10, s30
	s_lshl_b32 s14, s50, 19
	s_add_u32 s16, s15, s14
	s_addc_u32 s17, s26, 0
	s_and_b64 s[36:37], s[4:5], exec
	s_cselect_b32 s56, s17, s23
	s_cselect_b32 s57, s16, s22
	s_add_i32 s60, 0, 0x10000
	v_add_u32_e32 v198, s60, v196
	s_add_i32 s62, 0, 0x14000
	v_add_u32_e32 v199, s62, v196
	ds_read_b128 v[160:163], v198
	ds_read_b128 v[152:155], v198 offset:1024
	ds_read_b128 v[156:159], v198 offset:2048
	ds_read_b128 v[148:151], v198 offset:3072
	ds_read_b128 v[144:147], v199
	ds_read_b128 v[136:139], v199 offset:1024
	ds_read_b128 v[140:143], v199 offset:2048
	ds_read_b128 v[132:135], v199 offset:3072
	s_add_u32 s36, s30, 0x40080
	s_addc_u32 s37, s31, 0
	s_add_i32 s58, s41, 0xc000
	v_lshl_add_u64 v[174:175], s[36:37], 0, v[168:169]
	s_mov_b32 m0, s58
	s_add_i32 s59, s41, 0xe000
	ds_read_b128 v[178:181], v197
	ds_read_b128 v[182:185], v197 offset:1024
	ds_read_b128 v[190:193], v197 offset:2048
	ds_read_b128 v[200:203], v197 offset:3072
	ds_read_b128 v[204:207], v197 offset:4096
	ds_read_b128 v[208:211], v197 offset:5120
	ds_read_b128 v[212:215], v197 offset:6144
	ds_read_b128 v[216:219], v197 offset:7168
	global_load_lds_dwordx4 v[174:175], off
	v_lshl_add_u64 v[174:175], s[36:37], 0, v[166:167]
	s_mov_b32 m0, s59
	s_nop 0
	global_load_lds_dwordx4 v[174:175], off
	s_waitcnt vmcnt(8)
	s_waitcnt lgkmcnt(0)
	s_barrier
	v_mfma_f32_16x16x32_bf16 v[128:131], v[160:163], v[178:181], 0
	s_setprio 1
	v_mfma_f32_16x16x32_bf16 v[124:127], v[156:159], v[178:181], 0
	v_mfma_f32_16x16x32_bf16 v[116:119], v[156:159], v[190:193], 0
	v_mfma_f32_16x16x32_bf16 v[120:123], v[160:163], v[190:193], 0
	v_mfma_f32_16x16x32_bf16 v[112:115], v[160:163], v[204:207], 0
	v_mfma_f32_16x16x32_bf16 v[108:111], v[156:159], v[204:207], 0
	v_mfma_f32_16x16x32_bf16 v[100:103], v[156:159], v[212:215], 0
	v_mfma_f32_16x16x32_bf16 v[104:107], v[160:163], v[212:215], 0
	s_nop 0
	v_mfma_f32_16x16x32_bf16 v[128:131], v[152:155], v[182:185], v[128:131]
	v_mfma_f32_16x16x32_bf16 v[124:127], v[148:151], v[182:185], v[124:127]
	v_mfma_f32_16x16x32_bf16 v[116:119], v[148:151], v[200:203], v[116:119]
	v_mfma_f32_16x16x32_bf16 v[120:123], v[152:155], v[200:203], v[120:123]
	v_mfma_f32_16x16x32_bf16 v[112:115], v[152:155], v[208:211], v[112:115]
	v_mfma_f32_16x16x32_bf16 v[108:111], v[148:151], v[208:211], v[108:111]
	v_mfma_f32_16x16x32_bf16 v[100:103], v[148:151], v[216:219], v[100:103]
	v_mfma_f32_16x16x32_bf16 v[104:107], v[152:155], v[216:219], v[104:107]
	s_setprio 0
	s_setprio 1
	v_mfma_f32_16x16x32_bf16 v[96:99], v[144:147], v[178:181], 0
	v_mfma_f32_16x16x32_bf16 v[92:95], v[140:143], v[178:181], 0
	v_mfma_f32_16x16x32_bf16 v[84:87], v[140:143], v[190:193], 0
	v_mfma_f32_16x16x32_bf16 v[88:91], v[144:147], v[190:193], 0
	v_mfma_f32_16x16x32_bf16 v[80:83], v[144:147], v[204:207], 0
	v_mfma_f32_16x16x32_bf16 v[76:79], v[140:143], v[204:207], 0
	v_mfma_f32_16x16x32_bf16 v[68:71], v[140:143], v[212:215], 0
	v_mfma_f32_16x16x32_bf16 v[72:75], v[144:147], v[212:215], 0
	s_nop 0
	v_mfma_f32_16x16x32_bf16 v[96:99], v[136:139], v[182:185], v[96:99]
	v_mfma_f32_16x16x32_bf16 v[92:95], v[132:135], v[182:185], v[92:95]
	v_mfma_f32_16x16x32_bf16 v[84:87], v[132:135], v[200:203], v[84:87]
	v_mfma_f32_16x16x32_bf16 v[88:91], v[136:139], v[200:203], v[88:91]
	v_mfma_f32_16x16x32_bf16 v[80:83], v[136:139], v[208:211], v[80:83]
	v_mfma_f32_16x16x32_bf16 v[76:79], v[132:135], v[208:211], v[76:79]
	v_mfma_f32_16x16x32_bf16 v[68:71], v[132:135], v[216:219], v[68:71]
	v_mfma_f32_16x16x32_bf16 v[72:75], v[136:139], v[216:219], v[72:75]
	s_barrier
	s_setprio 0
	v_lshl_add_u64 v[174:175], s[22:23], 0, v[34:35]
	s_add_i32 s60, s60, s40
	v_lshl_add_u64 v[190:191], v[174:175], 0, s[28:29]
	s_mov_b32 m0, s60
	s_add_i32 s61, s60, 0x2000
	ds_read_b128 v[178:181], v197 offset:16384
	ds_read_b128 v[182:185], v197 offset:17408
	ds_read_b128 v[200:203], v197 offset:18432
	ds_read_b128 v[204:207], v197 offset:19456
	ds_read_b128 v[208:211], v197 offset:20480
	ds_read_b128 v[212:215], v197 offset:21504
	ds_read_b128 v[216:219], v197 offset:22528
	ds_read_b128 v[222:225], v197 offset:23552
	global_load_lds_dwordx4 v[190:191], off
	v_lshl_add_u64 v[190:191], s[22:23], 0, v[164:165]
	s_add_u32 s36, s22, 0x40100
	v_lshl_add_u64 v[192:193], v[190:191], 0, s[28:29]
	s_mov_b32 m0, s61
	s_addc_u32 s37, s23, 0
	s_add_i32 s62, s62, s40
	global_load_lds_dwordx4 v[192:193], off
	v_lshl_add_u64 v[192:193], s[36:37], 0, v[34:35]
	s_mov_b32 m0, s62
	s_add_i32 s63, s62, 0x2000
	global_load_lds_dwordx4 v[192:193], off
	v_lshl_add_u64 v[192:193], s[36:37], 0, v[164:165]
	s_mov_b32 m0, s63
	s_nop 0
	global_load_lds_dwordx4 v[192:193], off
	v_lshl_add_u64 v[192:193], s[30:31], 0, v[168:169]
	v_lshl_add_u64 v[194:195], v[192:193], 0, s[28:29]
	s_mov_b32 m0, s41
	s_nop 0
	global_load_lds_dwordx4 v[194:195], off
	v_lshl_add_u64 v[194:195], s[30:31], 0, v[166:167]
	v_lshl_add_u64 v[226:227], v[194:195], 0, s[28:29]
	s_mov_b32 m0, s42
	s_nop 0
	global_load_lds_dwordx4 v[226:227], off
	s_waitcnt vmcnt(8)
	s_waitcnt lgkmcnt(0)
	s_barrier
	v_mfma_f32_16x16x32_bf16 v[64:67], v[160:163], v[178:181], 0
	s_setprio 1
	v_mfma_f32_16x16x32_bf16 v[60:63], v[156:159], v[178:181], 0
	v_mfma_f32_16x16x32_bf16 v[52:55], v[156:159], v[200:203], 0
	v_mfma_f32_16x16x32_bf16 v[56:59], v[160:163], v[200:203], 0
	v_mfma_f32_16x16x32_bf16 v[48:51], v[160:163], v[208:211], 0
	v_mfma_f32_16x16x32_bf16 v[44:47], v[156:159], v[208:211], 0
	v_mfma_f32_16x16x32_bf16 v[36:39], v[156:159], v[216:219], 0
	v_mfma_f32_16x16x32_bf16 v[40:43], v[160:163], v[216:219], 0
	s_nop 0
	v_mfma_f32_16x16x32_bf16 v[64:67], v[152:155], v[182:185], v[64:67]
	v_mfma_f32_16x16x32_bf16 v[60:63], v[148:151], v[182:185], v[60:63]
	v_mfma_f32_16x16x32_bf16 v[52:55], v[148:151], v[204:207], v[52:55]
	v_mfma_f32_16x16x32_bf16 v[56:59], v[152:155], v[204:207], v[56:59]
	v_mfma_f32_16x16x32_bf16 v[48:51], v[152:155], v[212:215], v[48:51]
	v_mfma_f32_16x16x32_bf16 v[44:47], v[148:151], v[212:215], v[44:47]
	v_mfma_f32_16x16x32_bf16 v[36:39], v[148:151], v[222:225], v[36:39]
	v_mfma_f32_16x16x32_bf16 v[40:43], v[152:155], v[222:225], v[40:43]
	s_setprio 0
	s_setprio 1
	v_mfma_f32_16x16x32_bf16 v[30:33], v[144:147], v[178:181], 0
	v_mfma_f32_16x16x32_bf16 v[26:29], v[140:143], v[178:181], 0
	v_mfma_f32_16x16x32_bf16 v[18:21], v[140:143], v[200:203], 0
	v_mfma_f32_16x16x32_bf16 v[22:25], v[144:147], v[200:203], 0
	v_mfma_f32_16x16x32_bf16 v[14:17], v[144:147], v[208:211], 0
	v_mfma_f32_16x16x32_bf16 v[10:13], v[140:143], v[208:211], 0
	v_mfma_f32_16x16x32_bf16 v[2:5], v[140:143], v[216:219], 0
	v_mfma_f32_16x16x32_bf16 v[6:9], v[144:147], v[216:219], 0
	s_nop 0
	v_mfma_f32_16x16x32_bf16 v[30:33], v[136:139], v[182:185], v[30:33]
	v_mfma_f32_16x16x32_bf16 v[26:29], v[132:135], v[182:185], v[26:29]
	v_mfma_f32_16x16x32_bf16 v[18:21], v[132:135], v[204:207], v[18:21]
	v_mfma_f32_16x16x32_bf16 v[22:25], v[136:139], v[204:207], v[22:25]
	v_mfma_f32_16x16x32_bf16 v[14:17], v[136:139], v[212:215], v[14:17]
	v_mfma_f32_16x16x32_bf16 v[10:13], v[132:135], v[212:215], v[10:13]
	v_mfma_f32_16x16x32_bf16 v[2:5], v[132:135], v[222:225], v[2:5]
	v_mfma_f32_16x16x32_bf16 v[6:9], v[136:139], v[222:225], v[6:9]
	s_barrier
	s_setprio 0
	s_add_i32 s64, 0, 0x18000
	s_add_i32 s66, 0, 0x1c000
	v_add_u32_e32 v132, s64, v196
	v_add_u32_e32 v133, s66, v196
	ds_read_b128 v[134:137], v132
	ds_read_b128 v[138:141], v132 offset:1024
	ds_read_b128 v[142:145], v132 offset:2048
	ds_read_b128 v[146:149], v132 offset:3072
	ds_read_b128 v[150:153], v133
	ds_read_b128 v[154:157], v133 offset:1024
	ds_read_b128 v[158:161], v133 offset:2048
	ds_read_b128 v[178:181], v133 offset:3072
	s_add_u32 s36, s30, 0x40100
	s_addc_u32 s37, s31, 0
	s_mov_b32 m0, s43
	v_lshl_add_u64 v[162:163], s[36:37], 0, v[168:169]
	ds_read_b128 v[182:185], v197 offset:32768
	ds_read_b128 v[200:203], v197 offset:33792
	ds_read_b128 v[204:207], v197 offset:34816
	ds_read_b128 v[208:211], v197 offset:35840
	ds_read_b128 v[212:215], v197 offset:36864
	ds_read_b128 v[216:219], v197 offset:37888
	ds_read_b128 v[222:225], v197 offset:38912
	ds_read_b128 v[226:229], v197 offset:39936
	global_load_lds_dwordx4 v[162:163], off
	v_lshl_add_u64 v[162:163], s[36:37], 0, v[166:167]
	s_mov_b32 m0, s44
	s_nop 0
	global_load_lds_dwordx4 v[162:163], off
	s_waitcnt vmcnt(8)
	s_waitcnt lgkmcnt(0)
	s_barrier
	v_mfma_f32_16x16x32_bf16 v[128:131], v[134:137], v[182:185], v[128:131]
	s_setprio 1
	v_mfma_f32_16x16x32_bf16 v[124:127], v[142:145], v[182:185], v[124:127]
	v_mfma_f32_16x16x32_bf16 v[116:119], v[142:145], v[204:207], v[116:119]
	v_mfma_f32_16x16x32_bf16 v[120:123], v[134:137], v[204:207], v[120:123]
	v_mfma_f32_16x16x32_bf16 v[112:115], v[134:137], v[212:215], v[112:115]
	v_mfma_f32_16x16x32_bf16 v[108:111], v[142:145], v[212:215], v[108:111]
	v_mfma_f32_16x16x32_bf16 v[100:103], v[142:145], v[222:225], v[100:103]
	v_mfma_f32_16x16x32_bf16 v[104:107], v[134:137], v[222:225], v[104:107]
	v_mfma_f32_16x16x32_bf16 v[128:131], v[138:141], v[200:203], v[128:131]
	v_mfma_f32_16x16x32_bf16 v[124:127], v[146:149], v[200:203], v[124:127]
	v_mfma_f32_16x16x32_bf16 v[116:119], v[146:149], v[208:211], v[116:119]
	v_mfma_f32_16x16x32_bf16 v[120:123], v[138:141], v[208:211], v[120:123]
	v_mfma_f32_16x16x32_bf16 v[112:115], v[138:141], v[216:219], v[112:115]
	v_mfma_f32_16x16x32_bf16 v[108:111], v[146:149], v[216:219], v[108:111]
	v_mfma_f32_16x16x32_bf16 v[100:103], v[146:149], v[226:229], v[100:103]
	v_mfma_f32_16x16x32_bf16 v[104:107], v[138:141], v[226:229], v[104:107]
	s_setprio 0
	s_setprio 1
	v_mfma_f32_16x16x32_bf16 v[96:99], v[150:153], v[182:185], v[96:99]
	v_mfma_f32_16x16x32_bf16 v[92:95], v[158:161], v[182:185], v[92:95]
	v_mfma_f32_16x16x32_bf16 v[84:87], v[158:161], v[204:207], v[84:87]
	v_mfma_f32_16x16x32_bf16 v[88:91], v[150:153], v[204:207], v[88:91]
	v_mfma_f32_16x16x32_bf16 v[80:83], v[150:153], v[212:215], v[80:83]
	v_mfma_f32_16x16x32_bf16 v[76:79], v[158:161], v[212:215], v[76:79]
	v_mfma_f32_16x16x32_bf16 v[68:71], v[158:161], v[222:225], v[68:71]
	v_mfma_f32_16x16x32_bf16 v[72:75], v[150:153], v[222:225], v[72:75]
	v_mfma_f32_16x16x32_bf16 v[96:99], v[154:157], v[200:203], v[96:99]
	v_mfma_f32_16x16x32_bf16 v[92:95], v[178:181], v[200:203], v[92:95]
	v_mfma_f32_16x16x32_bf16 v[84:87], v[178:181], v[208:211], v[84:87]
	v_mfma_f32_16x16x32_bf16 v[88:91], v[154:157], v[208:211], v[88:91]
	v_mfma_f32_16x16x32_bf16 v[80:83], v[154:157], v[216:219], v[80:83]
	v_mfma_f32_16x16x32_bf16 v[76:79], v[178:181], v[216:219], v[76:79]
	v_mfma_f32_16x16x32_bf16 v[68:71], v[178:181], v[226:229], v[68:71]
	v_mfma_f32_16x16x32_bf16 v[72:75], v[154:157], v[226:229], v[72:75]
	s_barrier
	s_setprio 0
	s_add_i32 s64, s64, s40
	s_mov_b64 s[24:25], 0x180
	s_add_i32 s65, s64, 0x2000
	v_lshl_add_u64 v[162:163], v[174:175], 0, s[24:25]
	s_mov_b32 m0, s64
	s_add_u32 s36, s22, 0x40180
	ds_read_b128 v[182:185], v197 offset:49152
	ds_read_b128 v[200:203], v197 offset:50176
	ds_read_b128 v[204:207], v197 offset:51200
	ds_read_b128 v[208:211], v197 offset:52224
	ds_read_b128 v[212:215], v197 offset:53248
	ds_read_b128 v[216:219], v197 offset:54272
	ds_read_b128 v[222:225], v197 offset:55296
	ds_read_b128 v[226:229], v197 offset:56320
	global_load_lds_dwordx4 v[162:163], off
	v_lshl_add_u64 v[162:163], v[190:191], 0, s[24:25]
	s_mov_b32 m0, s65
	s_addc_u32 s37, s23, 0
	s_add_i32 s66, s66, s40
	global_load_lds_dwordx4 v[162:163], off
	v_lshl_add_u64 v[162:163], s[36:37], 0, v[34:35]
	s_mov_b32 m0, s66
	s_add_i32 s67, s66, 0x2000
	global_load_lds_dwordx4 v[162:163], off
	v_lshl_add_u64 v[162:163], s[36:37], 0, v[164:165]
	s_mov_b32 m0, s67
	s_nop 0
	global_load_lds_dwordx4 v[162:163], off
	v_lshl_add_u64 v[162:163], v[192:193], 0, s[24:25]
	s_mov_b32 m0, s47
	s_nop 0
	global_load_lds_dwordx4 v[162:163], off
	v_lshl_add_u64 v[162:163], v[194:195], 0, s[24:25]
	s_mov_b32 m0, s48
	s_nop 0
	global_load_lds_dwordx4 v[162:163], off
	s_waitcnt vmcnt(8)
	s_waitcnt lgkmcnt(0)
	s_barrier
	v_mfma_f32_16x16x32_bf16 v[64:67], v[134:137], v[182:185], v[64:67]
	s_setprio 1
	v_mfma_f32_16x16x32_bf16 v[60:63], v[142:145], v[182:185], v[60:63]
	v_mfma_f32_16x16x32_bf16 v[52:55], v[142:145], v[204:207], v[52:55]
	v_mfma_f32_16x16x32_bf16 v[56:59], v[134:137], v[204:207], v[56:59]
	v_mfma_f32_16x16x32_bf16 v[48:51], v[134:137], v[212:215], v[48:51]
	v_mfma_f32_16x16x32_bf16 v[44:47], v[142:145], v[212:215], v[44:47]
	v_mfma_f32_16x16x32_bf16 v[36:39], v[142:145], v[222:225], v[36:39]
	v_mfma_f32_16x16x32_bf16 v[40:43], v[134:137], v[222:225], v[40:43]
	v_mfma_f32_16x16x32_bf16 v[64:67], v[138:141], v[200:203], v[64:67]
	v_mfma_f32_16x16x32_bf16 v[60:63], v[146:149], v[200:203], v[60:63]
	v_mfma_f32_16x16x32_bf16 v[52:55], v[146:149], v[208:211], v[52:55]
	v_mfma_f32_16x16x32_bf16 v[56:59], v[138:141], v[208:211], v[56:59]
	v_mfma_f32_16x16x32_bf16 v[48:51], v[138:141], v[216:219], v[48:51]
	v_mfma_f32_16x16x32_bf16 v[44:47], v[146:149], v[216:219], v[44:47]
	v_mfma_f32_16x16x32_bf16 v[36:39], v[146:149], v[226:229], v[36:39]
	v_mfma_f32_16x16x32_bf16 v[40:43], v[138:141], v[226:229], v[40:43]
	s_setprio 0
	s_setprio 1
	v_mfma_f32_16x16x32_bf16 v[30:33], v[150:153], v[182:185], v[30:33]
	v_mfma_f32_16x16x32_bf16 v[26:29], v[158:161], v[182:185], v[26:29]
	v_mfma_f32_16x16x32_bf16 v[18:21], v[158:161], v[204:207], v[18:21]
	v_mfma_f32_16x16x32_bf16 v[22:25], v[150:153], v[204:207], v[22:25]
	v_mfma_f32_16x16x32_bf16 v[14:17], v[150:153], v[212:215], v[14:17]
	v_mfma_f32_16x16x32_bf16 v[10:13], v[158:161], v[212:215], v[10:13]
	v_mfma_f32_16x16x32_bf16 v[2:5], v[158:161], v[222:225], v[2:5]
	v_mfma_f32_16x16x32_bf16 v[6:9], v[150:153], v[222:225], v[6:9]
	v_mfma_f32_16x16x32_bf16 v[30:33], v[154:157], v[200:203], v[30:33]
	v_mfma_f32_16x16x32_bf16 v[26:29], v[178:181], v[200:203], v[26:29]
	v_mfma_f32_16x16x32_bf16 v[18:21], v[178:181], v[208:211], v[18:21]
	v_mfma_f32_16x16x32_bf16 v[22:25], v[154:157], v[208:211], v[22:25]
	v_mfma_f32_16x16x32_bf16 v[14:17], v[154:157], v[216:219], v[14:17]
	v_mfma_f32_16x16x32_bf16 v[10:13], v[178:181], v[216:219], v[10:13]
	v_mfma_f32_16x16x32_bf16 v[2:5], v[178:181], v[226:229], v[2:5]
	v_mfma_f32_16x16x32_bf16 v[6:9], v[154:157], v[226:229], v[6:9]
	s_barrier
	s_setprio 0
	s_add_u32 s30, s30, 0x40180
	s_addc_u32 s31, s31, 0
	s_add_u32 s68, s22, 0x200
	s_addc_u32 s69, s23, 0
	s_mov_b32 s70, 0
.LBB0_287:
	ds_read_b128 v[134:137], v198
	ds_read_b128 v[138:141], v198 offset:1024
	ds_read_b128 v[142:145], v198 offset:2048
	ds_read_b128 v[146:149], v198 offset:3072
	ds_read_b128 v[150:153], v199
	ds_read_b128 v[154:157], v199 offset:1024
	ds_read_b128 v[158:161], v199 offset:2048
	ds_read_b128 v[178:181], v199 offset:3072
	s_add_u32 s14, s30, 0xfffc0080
	s_addc_u32 s22, s31, -1
	s_cmp_eq_u32 s70, 12
	s_cselect_b32 s37, s54, s22
	s_cselect_b32 s36, s55, s14
	s_cselect_b32 s23, s56, s69
	s_cselect_b32 s22, s57, s68
	s_mov_b32 m0, s58
	v_lshl_add_u64 v[162:163], s[30:31], 0, v[170:171]
	ds_read_b128 v[182:185], v197
	ds_read_b128 v[190:193], v197 offset:1024
	ds_read_b128 v[200:203], v197 offset:2048
	ds_read_b128 v[204:207], v197 offset:3072
	ds_read_b128 v[208:211], v197 offset:4096
	ds_read_b128 v[212:215], v197 offset:5120
	ds_read_b128 v[216:219], v197 offset:6144
	ds_read_b128 v[222:225], v197 offset:7168
	global_load_lds_dwordx4 v[162:163], off
	v_lshl_add_u64 v[162:163], s[30:31], 0, v[172:173]
	s_mov_b32 m0, s59
	s_nop 0
	global_load_lds_dwordx4 v[162:163], off
	s_waitcnt vmcnt(8)
	s_waitcnt lgkmcnt(0)
	s_barrier
	v_mfma_f32_16x16x32_bf16 v[128:131], v[134:137], v[182:185], v[128:131]
	s_setprio 1
	v_mfma_f32_16x16x32_bf16 v[124:127], v[142:145], v[182:185], v[124:127]
	v_mfma_f32_16x16x32_bf16 v[116:119], v[142:145], v[200:203], v[116:119]
	v_mfma_f32_16x16x32_bf16 v[120:123], v[134:137], v[200:203], v[120:123]
	v_mfma_f32_16x16x32_bf16 v[112:115], v[134:137], v[208:211], v[112:115]
	v_mfma_f32_16x16x32_bf16 v[108:111], v[142:145], v[208:211], v[108:111]
	v_mfma_f32_16x16x32_bf16 v[100:103], v[142:145], v[216:219], v[100:103]
	v_mfma_f32_16x16x32_bf16 v[104:107], v[134:137], v[216:219], v[104:107]
	v_mfma_f32_16x16x32_bf16 v[128:131], v[138:141], v[190:193], v[128:131]
	v_mfma_f32_16x16x32_bf16 v[124:127], v[146:149], v[190:193], v[124:127]
	v_mfma_f32_16x16x32_bf16 v[116:119], v[146:149], v[204:207], v[116:119]
	v_mfma_f32_16x16x32_bf16 v[120:123], v[138:141], v[204:207], v[120:123]
	v_mfma_f32_16x16x32_bf16 v[112:115], v[138:141], v[212:215], v[112:115]
	v_mfma_f32_16x16x32_bf16 v[108:111], v[146:149], v[212:215], v[108:111]
	v_mfma_f32_16x16x32_bf16 v[100:103], v[146:149], v[222:225], v[100:103]
	v_mfma_f32_16x16x32_bf16 v[104:107], v[138:141], v[222:225], v[104:107]
	s_setprio 0
	s_setprio 1
	v_mfma_f32_16x16x32_bf16 v[96:99], v[150:153], v[182:185], v[96:99]
	v_mfma_f32_16x16x32_bf16 v[92:95], v[158:161], v[182:185], v[92:95]
	v_mfma_f32_16x16x32_bf16 v[84:87], v[158:161], v[200:203], v[84:87]
	v_mfma_f32_16x16x32_bf16 v[88:91], v[150:153], v[200:203], v[88:91]
	v_mfma_f32_16x16x32_bf16 v[80:83], v[150:153], v[208:211], v[80:83]
	v_mfma_f32_16x16x32_bf16 v[76:79], v[158:161], v[208:211], v[76:79]
	v_mfma_f32_16x16x32_bf16 v[68:71], v[158:161], v[216:219], v[68:71]
	v_mfma_f32_16x16x32_bf16 v[72:75], v[150:153], v[216:219], v[72:75]
	v_mfma_f32_16x16x32_bf16 v[96:99], v[154:157], v[190:193], v[96:99]
	v_mfma_f32_16x16x32_bf16 v[92:95], v[178:181], v[190:193], v[92:95]
	v_mfma_f32_16x16x32_bf16 v[84:87], v[178:181], v[204:207], v[84:87]
	v_mfma_f32_16x16x32_bf16 v[88:91], v[154:157], v[204:207], v[88:91]
	v_mfma_f32_16x16x32_bf16 v[80:83], v[154:157], v[212:215], v[80:83]
	v_mfma_f32_16x16x32_bf16 v[76:79], v[178:181], v[212:215], v[76:79]
	v_mfma_f32_16x16x32_bf16 v[68:71], v[178:181], v[222:225], v[68:71]
	v_mfma_f32_16x16x32_bf16 v[72:75], v[154:157], v[222:225], v[72:75]
	s_barrier
	s_setprio 0
	s_mov_b32 m0, s60
	v_lshl_add_u64 v[162:163], s[22:23], 0, v[34:35]
	s_add_u32 s72, s22, 0x40000
	ds_read_b128 v[182:185], v197 offset:16384
	ds_read_b128 v[190:193], v197 offset:17408
	ds_read_b128 v[200:203], v197 offset:18432
	ds_read_b128 v[204:207], v197 offset:19456
	ds_read_b128 v[208:211], v197 offset:20480
	ds_read_b128 v[212:215], v197 offset:21504
	ds_read_b128 v[216:219], v197 offset:22528
	ds_read_b128 v[222:225], v197 offset:23552
	global_load_lds_dwordx4 v[162:163], off
	v_lshl_add_u64 v[174:175], s[22:23], 0, v[164:165]
	s_mov_b32 m0, s61
	s_addc_u32 s73, s23, 0
	global_load_lds_dwordx4 v[174:175], off
	v_lshl_add_u64 v[194:195], s[72:73], 0, v[34:35]
	s_mov_b32 m0, s62
	v_lshl_add_u64 v[226:227], s[36:37], 0, v[166:167]
	global_load_lds_dwordx4 v[194:195], off
	v_lshl_add_u64 v[194:195], s[72:73], 0, v[164:165]
	s_mov_b32 m0, s63
	s_nop 0
	global_load_lds_dwordx4 v[194:195], off
	v_lshl_add_u64 v[194:195], s[36:37], 0, v[168:169]
	s_mov_b32 m0, s41
	s_nop 0
	global_load_lds_dwordx4 v[194:195], off
	s_mov_b32 m0, s42
	s_nop 0
	global_load_lds_dwordx4 v[226:227], off
	s_waitcnt vmcnt(8)
	s_waitcnt lgkmcnt(0)
	s_barrier
	v_mfma_f32_16x16x32_bf16 v[64:67], v[134:137], v[182:185], v[64:67]
	s_setprio 1
	v_mfma_f32_16x16x32_bf16 v[60:63], v[142:145], v[182:185], v[60:63]
	v_mfma_f32_16x16x32_bf16 v[52:55], v[142:145], v[200:203], v[52:55]
	v_mfma_f32_16x16x32_bf16 v[56:59], v[134:137], v[200:203], v[56:59]
	v_mfma_f32_16x16x32_bf16 v[48:51], v[134:137], v[208:211], v[48:51]
	v_mfma_f32_16x16x32_bf16 v[44:47], v[142:145], v[208:211], v[44:47]
	v_mfma_f32_16x16x32_bf16 v[36:39], v[142:145], v[216:219], v[36:39]
	v_mfma_f32_16x16x32_bf16 v[40:43], v[134:137], v[216:219], v[40:43]
	v_mfma_f32_16x16x32_bf16 v[64:67], v[138:141], v[190:193], v[64:67]
	v_mfma_f32_16x16x32_bf16 v[60:63], v[146:149], v[190:193], v[60:63]
	v_mfma_f32_16x16x32_bf16 v[52:55], v[146:149], v[204:207], v[52:55]
	v_mfma_f32_16x16x32_bf16 v[56:59], v[138:141], v[204:207], v[56:59]
	v_mfma_f32_16x16x32_bf16 v[48:51], v[138:141], v[212:215], v[48:51]
	v_mfma_f32_16x16x32_bf16 v[44:47], v[146:149], v[212:215], v[44:47]
	v_mfma_f32_16x16x32_bf16 v[36:39], v[146:149], v[222:225], v[36:39]
	v_mfma_f32_16x16x32_bf16 v[40:43], v[138:141], v[222:225], v[40:43]
	s_setprio 0
	s_setprio 1
	v_mfma_f32_16x16x32_bf16 v[30:33], v[150:153], v[182:185], v[30:33]
	v_mfma_f32_16x16x32_bf16 v[26:29], v[158:161], v[182:185], v[26:29]
	v_mfma_f32_16x16x32_bf16 v[18:21], v[158:161], v[200:203], v[18:21]
	v_mfma_f32_16x16x32_bf16 v[22:25], v[150:153], v[200:203], v[22:25]
	v_mfma_f32_16x16x32_bf16 v[14:17], v[150:153], v[208:211], v[14:17]
	v_mfma_f32_16x16x32_bf16 v[10:13], v[158:161], v[208:211], v[10:13]
	v_mfma_f32_16x16x32_bf16 v[2:5], v[158:161], v[216:219], v[2:5]
	v_mfma_f32_16x16x32_bf16 v[6:9], v[150:153], v[216:219], v[6:9]
	v_mfma_f32_16x16x32_bf16 v[30:33], v[154:157], v[190:193], v[30:33]
	v_mfma_f32_16x16x32_bf16 v[26:29], v[178:181], v[190:193], v[26:29]
	v_mfma_f32_16x16x32_bf16 v[18:21], v[178:181], v[204:207], v[18:21]
	v_mfma_f32_16x16x32_bf16 v[22:25], v[154:157], v[204:207], v[22:25]
	v_mfma_f32_16x16x32_bf16 v[14:17], v[154:157], v[212:215], v[14:17]
	v_mfma_f32_16x16x32_bf16 v[10:13], v[178:181], v[212:215], v[10:13]
	v_mfma_f32_16x16x32_bf16 v[2:5], v[178:181], v[222:225], v[2:5]
	v_mfma_f32_16x16x32_bf16 v[6:9], v[154:157], v[222:225], v[6:9]
	s_barrier
	s_setprio 0
	ds_read_b128 v[134:137], v132
	ds_read_b128 v[138:141], v132 offset:1024
	ds_read_b128 v[142:145], v132 offset:2048
	ds_read_b128 v[146:149], v132 offset:3072
	ds_read_b128 v[150:153], v133
	ds_read_b128 v[154:157], v133 offset:1024
	ds_read_b128 v[158:161], v133 offset:2048
	ds_read_b128 v[178:181], v133 offset:3072
	s_add_u32 s36, s36, 0x40000
	s_addc_u32 s37, s37, 0
	s_mov_b32 m0, s43
	v_lshl_add_u64 v[228:229], s[36:37], 0, v[168:169]
	ds_read_b128 v[182:185], v197 offset:32768
	ds_read_b128 v[190:193], v197 offset:33792
	ds_read_b128 v[200:203], v197 offset:34816
	ds_read_b128 v[204:207], v197 offset:35840
	ds_read_b128 v[208:211], v197 offset:36864
	ds_read_b128 v[212:215], v197 offset:37888
	ds_read_b128 v[216:219], v197 offset:38912
	ds_read_b128 v[222:225], v197 offset:39936
	global_load_lds_dwordx4 v[228:229], off
	v_lshl_add_u64 v[228:229], s[36:37], 0, v[166:167]
	s_mov_b32 m0, s44
	s_nop 0
	global_load_lds_dwordx4 v[228:229], off
	s_waitcnt vmcnt(8)
	s_waitcnt lgkmcnt(0)
	s_barrier
	v_mfma_f32_16x16x32_bf16 v[128:131], v[134:137], v[182:185], v[128:131]
	s_setprio 1
	v_mfma_f32_16x16x32_bf16 v[124:127], v[142:145], v[182:185], v[124:127]
	v_mfma_f32_16x16x32_bf16 v[116:119], v[142:145], v[200:203], v[116:119]
	v_mfma_f32_16x16x32_bf16 v[120:123], v[134:137], v[200:203], v[120:123]
	v_mfma_f32_16x16x32_bf16 v[112:115], v[134:137], v[208:211], v[112:115]
	v_mfma_f32_16x16x32_bf16 v[108:111], v[142:145], v[208:211], v[108:111]
	v_mfma_f32_16x16x32_bf16 v[100:103], v[142:145], v[216:219], v[100:103]
	v_mfma_f32_16x16x32_bf16 v[104:107], v[134:137], v[216:219], v[104:107]
	v_mfma_f32_16x16x32_bf16 v[128:131], v[138:141], v[190:193], v[128:131]
	v_mfma_f32_16x16x32_bf16 v[124:127], v[146:149], v[190:193], v[124:127]
	v_mfma_f32_16x16x32_bf16 v[116:119], v[146:149], v[204:207], v[116:119]
	v_mfma_f32_16x16x32_bf16 v[120:123], v[138:141], v[204:207], v[120:123]
	v_mfma_f32_16x16x32_bf16 v[112:115], v[138:141], v[212:215], v[112:115]
	v_mfma_f32_16x16x32_bf16 v[108:111], v[146:149], v[212:215], v[108:111]
	v_mfma_f32_16x16x32_bf16 v[100:103], v[146:149], v[222:225], v[100:103]
	v_mfma_f32_16x16x32_bf16 v[104:107], v[138:141], v[222:225], v[104:107]
	s_setprio 0
	s_setprio 1
	v_mfma_f32_16x16x32_bf16 v[96:99], v[150:153], v[182:185], v[96:99]
	v_mfma_f32_16x16x32_bf16 v[92:95], v[158:161], v[182:185], v[92:95]
	v_mfma_f32_16x16x32_bf16 v[84:87], v[158:161], v[200:203], v[84:87]
	v_mfma_f32_16x16x32_bf16 v[88:91], v[150:153], v[200:203], v[88:91]
	v_mfma_f32_16x16x32_bf16 v[80:83], v[150:153], v[208:211], v[80:83]
	v_mfma_f32_16x16x32_bf16 v[76:79], v[158:161], v[208:211], v[76:79]
	v_mfma_f32_16x16x32_bf16 v[68:71], v[158:161], v[216:219], v[68:71]
	v_mfma_f32_16x16x32_bf16 v[72:75], v[150:153], v[216:219], v[72:75]
	v_mfma_f32_16x16x32_bf16 v[96:99], v[154:157], v[190:193], v[96:99]
	v_mfma_f32_16x16x32_bf16 v[92:95], v[178:181], v[190:193], v[92:95]
	v_mfma_f32_16x16x32_bf16 v[84:87], v[178:181], v[204:207], v[84:87]
	v_mfma_f32_16x16x32_bf16 v[88:91], v[154:157], v[204:207], v[88:91]
	v_mfma_f32_16x16x32_bf16 v[80:83], v[154:157], v[212:215], v[80:83]
	v_mfma_f32_16x16x32_bf16 v[76:79], v[178:181], v[212:215], v[76:79]
	v_mfma_f32_16x16x32_bf16 v[68:71], v[178:181], v[222:225], v[68:71]
	v_mfma_f32_16x16x32_bf16 v[72:75], v[154:157], v[222:225], v[72:75]
	s_barrier
	s_setprio 0
	s_mov_b32 m0, s64
	v_lshl_add_u64 v[162:163], v[162:163], 0, s[18:19]
	s_add_u32 s22, s22, 0x40080
	ds_read_b128 v[182:185], v197 offset:49152
	ds_read_b128 v[190:193], v197 offset:50176
	ds_read_b128 v[200:203], v197 offset:51200
	ds_read_b128 v[204:207], v197 offset:52224
	ds_read_b128 v[208:211], v197 offset:53248
	ds_read_b128 v[212:215], v197 offset:54272
	ds_read_b128 v[216:219], v197 offset:55296
	ds_read_b128 v[222:225], v197 offset:56320
	global_load_lds_dwordx4 v[162:163], off
	v_lshl_add_u64 v[162:163], v[174:175], 0, s[18:19]
	s_mov_b32 m0, s65
	s_addc_u32 s23, s23, 0
	global_load_lds_dwordx4 v[162:163], off
	v_lshl_add_u64 v[162:163], s[22:23], 0, v[34:35]
	s_mov_b32 m0, s66
	s_nop 0
	global_load_lds_dwordx4 v[162:163], off
	v_lshl_add_u64 v[162:163], s[22:23], 0, v[164:165]
	s_mov_b32 m0, s67
	s_nop 0
	global_load_lds_dwordx4 v[162:163], off
	v_lshl_add_u64 v[162:163], v[194:195], 0, s[18:19]
	s_mov_b32 m0, s47
	s_nop 0
	global_load_lds_dwordx4 v[162:163], off
	v_lshl_add_u64 v[162:163], v[226:227], 0, s[18:19]
	s_mov_b32 m0, s48
	s_nop 0
	global_load_lds_dwordx4 v[162:163], off
	s_waitcnt vmcnt(8)
	s_waitcnt lgkmcnt(0)
	s_barrier
	v_mfma_f32_16x16x32_bf16 v[64:67], v[134:137], v[182:185], v[64:67]
	s_setprio 1
	v_mfma_f32_16x16x32_bf16 v[60:63], v[142:145], v[182:185], v[60:63]
	v_mfma_f32_16x16x32_bf16 v[52:55], v[142:145], v[200:203], v[52:55]
	v_mfma_f32_16x16x32_bf16 v[56:59], v[134:137], v[200:203], v[56:59]
	v_mfma_f32_16x16x32_bf16 v[48:51], v[134:137], v[208:211], v[48:51]
	v_mfma_f32_16x16x32_bf16 v[44:47], v[142:145], v[208:211], v[44:47]
	v_mfma_f32_16x16x32_bf16 v[36:39], v[142:145], v[216:219], v[36:39]
	v_mfma_f32_16x16x32_bf16 v[40:43], v[134:137], v[216:219], v[40:43]
	v_mfma_f32_16x16x32_bf16 v[64:67], v[138:141], v[190:193], v[64:67]
	v_mfma_f32_16x16x32_bf16 v[60:63], v[146:149], v[190:193], v[60:63]
	v_mfma_f32_16x16x32_bf16 v[52:55], v[146:149], v[204:207], v[52:55]
	v_mfma_f32_16x16x32_bf16 v[56:59], v[138:141], v[204:207], v[56:59]
	v_mfma_f32_16x16x32_bf16 v[48:51], v[138:141], v[212:215], v[48:51]
	v_mfma_f32_16x16x32_bf16 v[44:47], v[146:149], v[212:215], v[44:47]
	v_mfma_f32_16x16x32_bf16 v[36:39], v[146:149], v[222:225], v[36:39]
	v_mfma_f32_16x16x32_bf16 v[40:43], v[138:141], v[222:225], v[40:43]
	s_setprio 0
	s_setprio 1
	v_mfma_f32_16x16x32_bf16 v[30:33], v[150:153], v[182:185], v[30:33]
	v_mfma_f32_16x16x32_bf16 v[26:29], v[158:161], v[182:185], v[26:29]
	v_mfma_f32_16x16x32_bf16 v[18:21], v[158:161], v[200:203], v[18:21]
	v_mfma_f32_16x16x32_bf16 v[22:25], v[150:153], v[200:203], v[22:25]
	v_mfma_f32_16x16x32_bf16 v[14:17], v[150:153], v[208:211], v[14:17]
	v_mfma_f32_16x16x32_bf16 v[10:13], v[158:161], v[208:211], v[10:13]
	v_mfma_f32_16x16x32_bf16 v[2:5], v[158:161], v[216:219], v[2:5]
	v_mfma_f32_16x16x32_bf16 v[6:9], v[150:153], v[216:219], v[6:9]
	v_mfma_f32_16x16x32_bf16 v[30:33], v[154:157], v[190:193], v[30:33]
	v_mfma_f32_16x16x32_bf16 v[26:29], v[178:181], v[190:193], v[26:29]
	v_mfma_f32_16x16x32_bf16 v[18:21], v[178:181], v[204:207], v[18:21]
	v_mfma_f32_16x16x32_bf16 v[22:25], v[154:157], v[204:207], v[22:25]
	v_mfma_f32_16x16x32_bf16 v[14:17], v[154:157], v[212:215], v[14:17]
	v_mfma_f32_16x16x32_bf16 v[10:13], v[178:181], v[212:215], v[10:13]
	v_mfma_f32_16x16x32_bf16 v[2:5], v[178:181], v[222:225], v[2:5]
	v_mfma_f32_16x16x32_bf16 v[6:9], v[154:157], v[222:225], v[6:9]
	s_barrier
	s_setprio 0
	s_add_i32 s70, s70, 2
	s_add_u32 s30, s30, 0x100
	s_addc_u32 s31, s31, 0
	s_add_u32 s68, s68, 0x100
	s_addc_u32 s69, s69, 0
	s_cmp_gt_u32 s70, 13
	s_cbranch_scc0 .LBB0_287
	s_and_b64 vcc, exec, s[8:9]
	s_cbranch_vccz .LBB0_290
	s_barrier

.LBB0_540:
	s_lshl_b32 s14, s55, 19
	v_readlane_b32 s16, v253, 53
	v_readlane_b32 s17, v253, 54
	s_add_u32 s16, s16, s14
	s_addc_u32 s17, s17, 0
	s_and_b64 s[22:23], s[4:5], exec
	s_cselect_b32 s58, s17, s37
	s_cselect_b32 s59, s16, s36
	s_lshl_b32 s14, s54, 19
	s_add_u32 s22, s15, s14
	s_addc_u32 s23, s26, 0
	s_and_b64 s[40:41], s[4:5], exec
	s_cselect_b32 s60, s23, s31
	s_cselect_b32 s61, s22, s30
	s_add_i32 s64, 0, 0x10000
	v_add_u32_e32 v172, s64, v222
	s_add_i32 s66, 0, 0x14000
	v_add_u32_e32 v173, s66, v222
	ds_read_b128 v[160:163], v172
	ds_read_b128 v[152:155], v172 offset:1024
	ds_read_b128 v[156:159], v172 offset:2048
	ds_read_b128 v[148:151], v172 offset:3072
	ds_read_b128 v[144:147], v173
	ds_read_b128 v[136:139], v173 offset:1024
	ds_read_b128 v[140:143], v173 offset:2048
	ds_read_b128 v[132:135], v173 offset:3072
	s_add_u32 s40, s36, 0x40080
	s_addc_u32 s41, s37, 0
	s_add_i32 s62, s43, 0xc000
	v_lshl_add_u64 v[174:175], s[40:41], 0, v[194:195]
	s_mov_b32 m0, s62
	s_add_i32 s63, s43, 0xe000
	ds_read_b128 v[164:167], v223
	ds_read_b128 v[168:171], v223 offset:1024
	ds_read_b128 v[178:181], v223 offset:2048
	ds_read_b128 v[182:185], v223 offset:3072
	ds_read_b128 v[200:203], v223 offset:4096
	ds_read_b128 v[204:207], v223 offset:5120
	ds_read_b128 v[208:211], v223 offset:6144
	ds_read_b128 v[212:215], v223 offset:7168
	global_load_lds_dwordx4 v[174:175], off
	v_lshl_add_u64 v[174:175], s[40:41], 0, v[192:193]
	s_mov_b32 m0, s63
	s_nop 0
	global_load_lds_dwordx4 v[174:175], off
	s_waitcnt vmcnt(8)
	s_waitcnt lgkmcnt(0)
	s_barrier
	v_mfma_f32_16x16x32_bf16 v[128:131], v[160:163], v[164:167], 0
	s_setprio 1
	v_mfma_f32_16x16x32_bf16 v[124:127], v[156:159], v[164:167], 0
	v_mfma_f32_16x16x32_bf16 v[116:119], v[156:159], v[178:181], 0
	v_mfma_f32_16x16x32_bf16 v[120:123], v[160:163], v[178:181], 0
	v_mfma_f32_16x16x32_bf16 v[112:115], v[160:163], v[200:203], 0
	v_mfma_f32_16x16x32_bf16 v[108:111], v[156:159], v[200:203], 0
	v_mfma_f32_16x16x32_bf16 v[100:103], v[156:159], v[208:211], 0
	v_mfma_f32_16x16x32_bf16 v[104:107], v[160:163], v[208:211], 0
	s_nop 0
	v_mfma_f32_16x16x32_bf16 v[128:131], v[152:155], v[168:171], v[128:131]
	v_mfma_f32_16x16x32_bf16 v[124:127], v[148:151], v[168:171], v[124:127]
	v_mfma_f32_16x16x32_bf16 v[116:119], v[148:151], v[182:185], v[116:119]
	v_mfma_f32_16x16x32_bf16 v[120:123], v[152:155], v[182:185], v[120:123]
	v_mfma_f32_16x16x32_bf16 v[112:115], v[152:155], v[204:207], v[112:115]
	v_mfma_f32_16x16x32_bf16 v[108:111], v[148:151], v[204:207], v[108:111]
	v_mfma_f32_16x16x32_bf16 v[100:103], v[148:151], v[212:215], v[100:103]
	v_mfma_f32_16x16x32_bf16 v[104:107], v[152:155], v[212:215], v[104:107]
	s_setprio 0
	s_setprio 1
	v_mfma_f32_16x16x32_bf16 v[96:99], v[144:147], v[164:167], 0
	v_mfma_f32_16x16x32_bf16 v[92:95], v[140:143], v[164:167], 0
	v_mfma_f32_16x16x32_bf16 v[84:87], v[140:143], v[178:181], 0
	v_mfma_f32_16x16x32_bf16 v[88:91], v[144:147], v[178:181], 0
	v_mfma_f32_16x16x32_bf16 v[80:83], v[144:147], v[200:203], 0
	v_mfma_f32_16x16x32_bf16 v[76:79], v[140:143], v[200:203], 0
	v_mfma_f32_16x16x32_bf16 v[68:71], v[140:143], v[208:211], 0
	v_mfma_f32_16x16x32_bf16 v[72:75], v[144:147], v[208:211], 0
	s_nop 0
	v_mfma_f32_16x16x32_bf16 v[96:99], v[136:139], v[168:171], v[96:99]
	v_mfma_f32_16x16x32_bf16 v[92:95], v[132:135], v[168:171], v[92:95]
	v_mfma_f32_16x16x32_bf16 v[84:87], v[132:135], v[182:185], v[84:87]
	v_mfma_f32_16x16x32_bf16 v[88:91], v[136:139], v[182:185], v[88:91]
	v_mfma_f32_16x16x32_bf16 v[80:83], v[136:139], v[204:207], v[80:83]
	v_mfma_f32_16x16x32_bf16 v[76:79], v[132:135], v[204:207], v[76:79]
	v_mfma_f32_16x16x32_bf16 v[68:71], v[132:135], v[212:215], v[68:71]
	v_mfma_f32_16x16x32_bf16 v[72:75], v[136:139], v[212:215], v[72:75]
	s_barrier
	s_setprio 0
	v_lshl_add_u64 v[164:165], s[30:31], 0, v[34:35]
	s_add_i32 s64, s64, s42
	v_lshl_add_u64 v[166:167], v[164:165], 0, s[28:29]
	s_mov_b32 m0, s64
	s_add_i32 s65, s64, 0x2000
	ds_read_b128 v[178:181], v223 offset:16384
	ds_read_b128 v[182:185], v223 offset:17408
	ds_read_b128 v[200:203], v223 offset:18432
	ds_read_b128 v[204:207], v223 offset:19456
	ds_read_b128 v[208:211], v223 offset:20480
	ds_read_b128 v[212:215], v223 offset:21504
	ds_read_b128 v[216:219], v223 offset:22528
	ds_read_b128 v[224:227], v223 offset:23552
	global_load_lds_dwordx4 v[166:167], off
	v_lshl_add_u64 v[166:167], s[30:31], 0, v[190:191]
	s_add_u32 s40, s30, 0x40100
	v_lshl_add_u64 v[168:169], v[166:167], 0, s[28:29]
	s_mov_b32 m0, s65
	s_addc_u32 s41, s31, 0
	s_add_i32 s66, s66, s42
	global_load_lds_dwordx4 v[168:169], off
	v_lshl_add_u64 v[168:169], s[40:41], 0, v[34:35]
	s_mov_b32 m0, s66
	s_add_i32 s67, s66, 0x2000
	global_load_lds_dwordx4 v[168:169], off
	v_lshl_add_u64 v[168:169], s[40:41], 0, v[190:191]
	s_mov_b32 m0, s67
	s_nop 0
	global_load_lds_dwordx4 v[168:169], off
	v_lshl_add_u64 v[168:169], s[36:37], 0, v[194:195]
	v_lshl_add_u64 v[170:171], v[168:169], 0, s[28:29]
	s_mov_b32 m0, s43
	s_nop 0
	global_load_lds_dwordx4 v[170:171], off
	v_lshl_add_u64 v[170:171], s[36:37], 0, v[192:193]
	v_lshl_add_u64 v[174:175], v[170:171], 0, s[28:29]
	s_mov_b32 m0, s44
	s_nop 0
	global_load_lds_dwordx4 v[174:175], off
	s_waitcnt vmcnt(8)
	s_waitcnt lgkmcnt(0)
	s_barrier
	v_mfma_f32_16x16x32_bf16 v[64:67], v[160:163], v[178:181], 0
	s_setprio 1
	v_mfma_f32_16x16x32_bf16 v[60:63], v[156:159], v[178:181], 0
	v_mfma_f32_16x16x32_bf16 v[52:55], v[156:159], v[200:203], 0
	v_mfma_f32_16x16x32_bf16 v[56:59], v[160:163], v[200:203], 0
	v_mfma_f32_16x16x32_bf16 v[48:51], v[160:163], v[208:211], 0
	v_mfma_f32_16x16x32_bf16 v[44:47], v[156:159], v[208:211], 0
	v_mfma_f32_16x16x32_bf16 v[36:39], v[156:159], v[216:219], 0
	v_mfma_f32_16x16x32_bf16 v[40:43], v[160:163], v[216:219], 0
	s_nop 0
	v_mfma_f32_16x16x32_bf16 v[64:67], v[152:155], v[182:185], v[64:67]
	v_mfma_f32_16x16x32_bf16 v[60:63], v[148:151], v[182:185], v[60:63]
	v_mfma_f32_16x16x32_bf16 v[52:55], v[148:151], v[204:207], v[52:55]
	v_mfma_f32_16x16x32_bf16 v[56:59], v[152:155], v[204:207], v[56:59]
	v_mfma_f32_16x16x32_bf16 v[48:51], v[152:155], v[212:215], v[48:51]
	v_mfma_f32_16x16x32_bf16 v[44:47], v[148:151], v[212:215], v[44:47]
	v_mfma_f32_16x16x32_bf16 v[36:39], v[148:151], v[224:227], v[36:39]
	v_mfma_f32_16x16x32_bf16 v[40:43], v[152:155], v[224:227], v[40:43]
	s_setprio 0
	s_setprio 1
	v_mfma_f32_16x16x32_bf16 v[30:33], v[144:147], v[178:181], 0
	v_mfma_f32_16x16x32_bf16 v[26:29], v[140:143], v[178:181], 0
	v_mfma_f32_16x16x32_bf16 v[18:21], v[140:143], v[200:203], 0
	v_mfma_f32_16x16x32_bf16 v[22:25], v[144:147], v[200:203], 0
	v_mfma_f32_16x16x32_bf16 v[14:17], v[144:147], v[208:211], 0
	v_mfma_f32_16x16x32_bf16 v[10:13], v[140:143], v[208:211], 0
	v_mfma_f32_16x16x32_bf16 v[2:5], v[140:143], v[216:219], 0
	v_mfma_f32_16x16x32_bf16 v[6:9], v[144:147], v[216:219], 0
	s_nop 0
	v_mfma_f32_16x16x32_bf16 v[30:33], v[136:139], v[182:185], v[30:33]
	v_mfma_f32_16x16x32_bf16 v[26:29], v[132:135], v[182:185], v[26:29]
	v_mfma_f32_16x16x32_bf16 v[18:21], v[132:135], v[204:207], v[18:21]
	v_mfma_f32_16x16x32_bf16 v[22:25], v[136:139], v[204:207], v[22:25]
	v_mfma_f32_16x16x32_bf16 v[14:17], v[136:139], v[212:215], v[14:17]
	v_mfma_f32_16x16x32_bf16 v[10:13], v[132:135], v[212:215], v[10:13]
	v_mfma_f32_16x16x32_bf16 v[2:5], v[132:135], v[224:227], v[2:5]
	v_mfma_f32_16x16x32_bf16 v[6:9], v[136:139], v[224:227], v[6:9]
	s_barrier
	s_setprio 0
	s_add_i32 s68, 0, 0x18000
	s_add_i32 s70, 0, 0x1c000
	v_add_u32_e32 v132, s68, v222
	v_add_u32_e32 v133, s70, v222
	ds_read_b128 v[134:137], v132
	ds_read_b128 v[138:141], v132 offset:1024
	ds_read_b128 v[142:145], v132 offset:2048
	ds_read_b128 v[146:149], v132 offset:3072
	ds_read_b128 v[150:153], v133
	ds_read_b128 v[154:157], v133 offset:1024
	ds_read_b128 v[158:161], v133 offset:2048
	ds_read_b128 v[178:181], v133 offset:3072
	s_add_u32 s40, s36, 0x40100
	s_addc_u32 s41, s37, 0
	s_mov_b32 m0, s45
	v_lshl_add_u64 v[162:163], s[40:41], 0, v[194:195]
	ds_read_b128 v[182:185], v223 offset:32768
	ds_read_b128 v[200:203], v223 offset:33792
	ds_read_b128 v[204:207], v223 offset:34816
	ds_read_b128 v[208:211], v223 offset:35840
	ds_read_b128 v[212:215], v223 offset:36864
	ds_read_b128 v[216:219], v223 offset:37888
	ds_read_b128 v[224:227], v223 offset:38912
	ds_read_b128 v[228:231], v223 offset:39936
	global_load_lds_dwordx4 v[162:163], off
	v_lshl_add_u64 v[162:163], s[40:41], 0, v[192:193]
	s_mov_b32 m0, s46
	s_nop 0
	global_load_lds_dwordx4 v[162:163], off
	s_waitcnt vmcnt(8)
	s_waitcnt lgkmcnt(0)
	s_barrier
	v_mfma_f32_16x16x32_bf16 v[128:131], v[134:137], v[182:185], v[128:131]
	s_setprio 1
	v_mfma_f32_16x16x32_bf16 v[124:127], v[142:145], v[182:185], v[124:127]
	v_mfma_f32_16x16x32_bf16 v[116:119], v[142:145], v[204:207], v[116:119]
	v_mfma_f32_16x16x32_bf16 v[120:123], v[134:137], v[204:207], v[120:123]
	v_mfma_f32_16x16x32_bf16 v[112:115], v[134:137], v[212:215], v[112:115]
	v_mfma_f32_16x16x32_bf16 v[108:111], v[142:145], v[212:215], v[108:111]
	v_mfma_f32_16x16x32_bf16 v[100:103], v[142:145], v[224:227], v[100:103]
	v_mfma_f32_16x16x32_bf16 v[104:107], v[134:137], v[224:227], v[104:107]
	v_mfma_f32_16x16x32_bf16 v[128:131], v[138:141], v[200:203], v[128:131]
	v_mfma_f32_16x16x32_bf16 v[124:127], v[146:149], v[200:203], v[124:127]
	v_mfma_f32_16x16x32_bf16 v[116:119], v[146:149], v[208:211], v[116:119]
	v_mfma_f32_16x16x32_bf16 v[120:123], v[138:141], v[208:211], v[120:123]
	v_mfma_f32_16x16x32_bf16 v[112:115], v[138:141], v[216:219], v[112:115]
	v_mfma_f32_16x16x32_bf16 v[108:111], v[146:149], v[216:219], v[108:111]
	v_mfma_f32_16x16x32_bf16 v[100:103], v[146:149], v[228:231], v[100:103]
	v_mfma_f32_16x16x32_bf16 v[104:107], v[138:141], v[228:231], v[104:107]
	s_setprio 0
	s_setprio 1
	v_mfma_f32_16x16x32_bf16 v[96:99], v[150:153], v[182:185], v[96:99]
	v_mfma_f32_16x16x32_bf16 v[92:95], v[158:161], v[182:185], v[92:95]
	v_mfma_f32_16x16x32_bf16 v[84:87], v[158:161], v[204:207], v[84:87]
	v_mfma_f32_16x16x32_bf16 v[88:91], v[150:153], v[204:207], v[88:91]
	v_mfma_f32_16x16x32_bf16 v[80:83], v[150:153], v[212:215], v[80:83]
	v_mfma_f32_16x16x32_bf16 v[76:79], v[158:161], v[212:215], v[76:79]
	v_mfma_f32_16x16x32_bf16 v[68:71], v[158:161], v[224:227], v[68:71]
	v_mfma_f32_16x16x32_bf16 v[72:75], v[150:153], v[224:227], v[72:75]
	v_mfma_f32_16x16x32_bf16 v[96:99], v[154:157], v[200:203], v[96:99]
	v_mfma_f32_16x16x32_bf16 v[92:95], v[178:181], v[200:203], v[92:95]
	v_mfma_f32_16x16x32_bf16 v[84:87], v[178:181], v[208:211], v[84:87]
	v_mfma_f32_16x16x32_bf16 v[88:91], v[154:157], v[208:211], v[88:91]
	v_mfma_f32_16x16x32_bf16 v[80:83], v[154:157], v[216:219], v[80:83]
	v_mfma_f32_16x16x32_bf16 v[76:79], v[178:181], v[216:219], v[76:79]
	v_mfma_f32_16x16x32_bf16 v[68:71], v[178:181], v[228:231], v[68:71]
	v_mfma_f32_16x16x32_bf16 v[72:75], v[154:157], v[228:231], v[72:75]
	s_barrier
	s_setprio 0
	s_add_i32 s68, s68, s42
	s_mov_b64 s[24:25], 0x180
	s_add_i32 s69, s68, 0x2000
	v_lshl_add_u64 v[162:163], v[164:165], 0, s[24:25]
	s_mov_b32 m0, s68
	s_add_u32 s40, s30, 0x40180
	ds_read_b128 v[182:185], v223 offset:49152
	ds_read_b128 v[200:203], v223 offset:50176
	ds_read_b128 v[204:207], v223 offset:51200
	ds_read_b128 v[208:211], v223 offset:52224
	ds_read_b128 v[212:215], v223 offset:53248
	ds_read_b128 v[216:219], v223 offset:54272
	ds_read_b128 v[224:227], v223 offset:55296
	ds_read_b128 v[228:231], v223 offset:56320
	global_load_lds_dwordx4 v[162:163], off
	v_lshl_add_u64 v[162:163], v[166:167], 0, s[24:25]
	s_mov_b32 m0, s69
	s_addc_u32 s41, s31, 0
	s_add_i32 s70, s70, s42
	global_load_lds_dwordx4 v[162:163], off
	v_lshl_add_u64 v[162:163], s[40:41], 0, v[34:35]
	s_mov_b32 m0, s70
	s_add_i32 s71, s70, 0x2000
	global_load_lds_dwordx4 v[162:163], off
	v_lshl_add_u64 v[162:163], s[40:41], 0, v[190:191]
	s_mov_b32 m0, s71
	s_nop 0
	global_load_lds_dwordx4 v[162:163], off
	v_lshl_add_u64 v[162:163], v[168:169], 0, s[24:25]
	s_mov_b32 m0, s51
	s_nop 0
	global_load_lds_dwordx4 v[162:163], off
	v_lshl_add_u64 v[162:163], v[170:171], 0, s[24:25]
	s_mov_b32 m0, s52
	s_nop 0
	global_load_lds_dwordx4 v[162:163], off
	s_waitcnt vmcnt(8)
	s_waitcnt lgkmcnt(0)
	s_barrier
	v_mfma_f32_16x16x32_bf16 v[64:67], v[134:137], v[182:185], v[64:67]
	s_setprio 1
	v_mfma_f32_16x16x32_bf16 v[60:63], v[142:145], v[182:185], v[60:63]
	v_mfma_f32_16x16x32_bf16 v[52:55], v[142:145], v[204:207], v[52:55]
	v_mfma_f32_16x16x32_bf16 v[56:59], v[134:137], v[204:207], v[56:59]
	v_mfma_f32_16x16x32_bf16 v[48:51], v[134:137], v[212:215], v[48:51]
	v_mfma_f32_16x16x32_bf16 v[44:47], v[142:145], v[212:215], v[44:47]
	v_mfma_f32_16x16x32_bf16 v[36:39], v[142:145], v[224:227], v[36:39]
	v_mfma_f32_16x16x32_bf16 v[40:43], v[134:137], v[224:227], v[40:43]
	v_mfma_f32_16x16x32_bf16 v[64:67], v[138:141], v[200:203], v[64:67]
	v_mfma_f32_16x16x32_bf16 v[60:63], v[146:149], v[200:203], v[60:63]
	v_mfma_f32_16x16x32_bf16 v[52:55], v[146:149], v[208:211], v[52:55]
	v_mfma_f32_16x16x32_bf16 v[56:59], v[138:141], v[208:211], v[56:59]
	v_mfma_f32_16x16x32_bf16 v[48:51], v[138:141], v[216:219], v[48:51]
	v_mfma_f32_16x16x32_bf16 v[44:47], v[146:149], v[216:219], v[44:47]
	v_mfma_f32_16x16x32_bf16 v[36:39], v[146:149], v[228:231], v[36:39]
	v_mfma_f32_16x16x32_bf16 v[40:43], v[138:141], v[228:231], v[40:43]
	s_setprio 0
	s_setprio 1
	v_mfma_f32_16x16x32_bf16 v[30:33], v[150:153], v[182:185], v[30:33]
	v_mfma_f32_16x16x32_bf16 v[26:29], v[158:161], v[182:185], v[26:29]
	v_mfma_f32_16x16x32_bf16 v[18:21], v[158:161], v[204:207], v[18:21]
	v_mfma_f32_16x16x32_bf16 v[22:25], v[150:153], v[204:207], v[22:25]
	v_mfma_f32_16x16x32_bf16 v[14:17], v[150:153], v[212:215], v[14:17]
	v_mfma_f32_16x16x32_bf16 v[10:13], v[158:161], v[212:215], v[10:13]
	v_mfma_f32_16x16x32_bf16 v[2:5], v[158:161], v[224:227], v[2:5]
	v_mfma_f32_16x16x32_bf16 v[6:9], v[150:153], v[224:227], v[6:9]
	v_mfma_f32_16x16x32_bf16 v[30:33], v[154:157], v[200:203], v[30:33]
	v_mfma_f32_16x16x32_bf16 v[26:29], v[178:181], v[200:203], v[26:29]
	v_mfma_f32_16x16x32_bf16 v[18:21], v[178:181], v[208:211], v[18:21]
	v_mfma_f32_16x16x32_bf16 v[22:25], v[154:157], v[208:211], v[22:25]
	v_mfma_f32_16x16x32_bf16 v[14:17], v[154:157], v[216:219], v[14:17]
	v_mfma_f32_16x16x32_bf16 v[10:13], v[178:181], v[216:219], v[10:13]
	v_mfma_f32_16x16x32_bf16 v[2:5], v[178:181], v[228:231], v[2:5]
	v_mfma_f32_16x16x32_bf16 v[6:9], v[154:157], v[228:231], v[6:9]
	s_barrier
	s_setprio 0
	s_add_u32 s36, s36, 0x40180
	s_addc_u32 s37, s37, 0
	s_add_u32 s72, s30, 0x200
	s_addc_u32 s73, s31, 0
	s_mov_b32 s74, 0
.LBB0_541:
	ds_read_b128 v[134:137], v172
	ds_read_b128 v[138:141], v172 offset:1024
	ds_read_b128 v[142:145], v172 offset:2048
	ds_read_b128 v[146:149], v172 offset:3072
	ds_read_b128 v[150:153], v173
	ds_read_b128 v[154:157], v173 offset:1024
	ds_read_b128 v[158:161], v173 offset:2048
	ds_read_b128 v[162:165], v173 offset:3072
	s_add_u32 s14, s36, 0xfffc0080
	s_addc_u32 s30, s37, -1
	s_cmp_eq_u32 s74, 12
	s_cselect_b32 s41, s58, s30
	s_cselect_b32 s40, s59, s14
	s_cselect_b32 s31, s60, s73
	s_cselect_b32 s30, s61, s72
	s_mov_b32 m0, s62
	v_lshl_add_u64 v[170:171], s[36:37], 0, v[196:197]
	ds_read_b128 v[166:169], v223
	ds_read_b128 v[178:181], v223 offset:1024
	ds_read_b128 v[182:185], v223 offset:2048
	ds_read_b128 v[200:203], v223 offset:3072
	ds_read_b128 v[204:207], v223 offset:4096
	ds_read_b128 v[208:211], v223 offset:5120
	ds_read_b128 v[212:215], v223 offset:6144
	ds_read_b128 v[216:219], v223 offset:7168
	global_load_lds_dwordx4 v[170:171], off
	v_lshl_add_u64 v[170:171], s[36:37], 0, v[198:199]
	s_mov_b32 m0, s63
	s_nop 0
	global_load_lds_dwordx4 v[170:171], off
	s_waitcnt vmcnt(8)
	s_waitcnt lgkmcnt(0)
	s_barrier
	v_mfma_f32_16x16x32_bf16 v[128:131], v[134:137], v[166:169], v[128:131]
	s_setprio 1
	v_mfma_f32_16x16x32_bf16 v[124:127], v[142:145], v[166:169], v[124:127]
	v_mfma_f32_16x16x32_bf16 v[116:119], v[142:145], v[182:185], v[116:119]
	v_mfma_f32_16x16x32_bf16 v[120:123], v[134:137], v[182:185], v[120:123]
	v_mfma_f32_16x16x32_bf16 v[112:115], v[134:137], v[204:207], v[112:115]
	v_mfma_f32_16x16x32_bf16 v[108:111], v[142:145], v[204:207], v[108:111]
	v_mfma_f32_16x16x32_bf16 v[100:103], v[142:145], v[212:215], v[100:103]
	v_mfma_f32_16x16x32_bf16 v[104:107], v[134:137], v[212:215], v[104:107]
	v_mfma_f32_16x16x32_bf16 v[128:131], v[138:141], v[178:181], v[128:131]
	v_mfma_f32_16x16x32_bf16 v[124:127], v[146:149], v[178:181], v[124:127]
	v_mfma_f32_16x16x32_bf16 v[116:119], v[146:149], v[200:203], v[116:119]
	v_mfma_f32_16x16x32_bf16 v[120:123], v[138:141], v[200:203], v[120:123]
	v_mfma_f32_16x16x32_bf16 v[112:115], v[138:141], v[208:211], v[112:115]
	v_mfma_f32_16x16x32_bf16 v[108:111], v[146:149], v[208:211], v[108:111]
	v_mfma_f32_16x16x32_bf16 v[100:103], v[146:149], v[216:219], v[100:103]
	v_mfma_f32_16x16x32_bf16 v[104:107], v[138:141], v[216:219], v[104:107]
	s_setprio 0
	s_setprio 1
	v_mfma_f32_16x16x32_bf16 v[96:99], v[150:153], v[166:169], v[96:99]
	v_mfma_f32_16x16x32_bf16 v[92:95], v[158:161], v[166:169], v[92:95]
	v_mfma_f32_16x16x32_bf16 v[84:87], v[158:161], v[182:185], v[84:87]
	v_mfma_f32_16x16x32_bf16 v[88:91], v[150:153], v[182:185], v[88:91]
	v_mfma_f32_16x16x32_bf16 v[80:83], v[150:153], v[204:207], v[80:83]
	v_mfma_f32_16x16x32_bf16 v[76:79], v[158:161], v[204:207], v[76:79]
	v_mfma_f32_16x16x32_bf16 v[68:71], v[158:161], v[212:215], v[68:71]
	v_mfma_f32_16x16x32_bf16 v[72:75], v[150:153], v[212:215], v[72:75]
	v_mfma_f32_16x16x32_bf16 v[96:99], v[154:157], v[178:181], v[96:99]
	v_mfma_f32_16x16x32_bf16 v[92:95], v[162:165], v[178:181], v[92:95]
	v_mfma_f32_16x16x32_bf16 v[84:87], v[162:165], v[200:203], v[84:87]
	v_mfma_f32_16x16x32_bf16 v[88:91], v[154:157], v[200:203], v[88:91]
	v_mfma_f32_16x16x32_bf16 v[80:83], v[154:157], v[208:211], v[80:83]
	v_mfma_f32_16x16x32_bf16 v[76:79], v[162:165], v[208:211], v[76:79]
	v_mfma_f32_16x16x32_bf16 v[68:71], v[162:165], v[216:219], v[68:71]
	v_mfma_f32_16x16x32_bf16 v[72:75], v[154:157], v[216:219], v[72:75]
	s_barrier
	s_setprio 0
	s_mov_b32 m0, s64
	v_lshl_add_u64 v[170:171], s[30:31], 0, v[34:35]
	s_add_u32 s76, s30, 0x40000
	ds_read_b128 v[166:169], v223 offset:16384
	ds_read_b128 v[178:181], v223 offset:17408
	ds_read_b128 v[182:185], v223 offset:18432
	ds_read_b128 v[200:203], v223 offset:19456
	ds_read_b128 v[204:207], v223 offset:20480
	ds_read_b128 v[208:211], v223 offset:21504
	ds_read_b128 v[212:215], v223 offset:22528
	ds_read_b128 v[216:219], v223 offset:23552
	global_load_lds_dwordx4 v[170:171], off
	v_lshl_add_u64 v[174:175], s[30:31], 0, v[190:191]
	s_mov_b32 m0, s65
	s_addc_u32 s77, s31, 0
	global_load_lds_dwordx4 v[174:175], off
	v_lshl_add_u64 v[224:225], s[76:77], 0, v[34:35]
	s_mov_b32 m0, s66
	v_lshl_add_u64 v[226:227], s[40:41], 0, v[192:193]
	global_load_lds_dwordx4 v[224:225], off
	v_lshl_add_u64 v[224:225], s[76:77], 0, v[190:191]
	s_mov_b32 m0, s67
	s_nop 0
	global_load_lds_dwordx4 v[224:225], off
	v_lshl_add_u64 v[224:225], s[40:41], 0, v[194:195]
	s_mov_b32 m0, s43
	s_nop 0
	global_load_lds_dwordx4 v[224:225], off
	s_mov_b32 m0, s44
	s_nop 0
	global_load_lds_dwordx4 v[226:227], off
	s_waitcnt vmcnt(8)
	s_waitcnt lgkmcnt(0)
	s_barrier
	v_mfma_f32_16x16x32_bf16 v[64:67], v[134:137], v[166:169], v[64:67]
	s_setprio 1
	v_mfma_f32_16x16x32_bf16 v[60:63], v[142:145], v[166:169], v[60:63]
	v_mfma_f32_16x16x32_bf16 v[52:55], v[142:145], v[182:185], v[52:55]
	v_mfma_f32_16x16x32_bf16 v[56:59], v[134:137], v[182:185], v[56:59]
	v_mfma_f32_16x16x32_bf16 v[48:51], v[134:137], v[204:207], v[48:51]
	v_mfma_f32_16x16x32_bf16 v[44:47], v[142:145], v[204:207], v[44:47]
	v_mfma_f32_16x16x32_bf16 v[36:39], v[142:145], v[212:215], v[36:39]
	v_mfma_f32_16x16x32_bf16 v[40:43], v[134:137], v[212:215], v[40:43]
	v_mfma_f32_16x16x32_bf16 v[64:67], v[138:141], v[178:181], v[64:67]
	v_mfma_f32_16x16x32_bf16 v[60:63], v[146:149], v[178:181], v[60:63]
	v_mfma_f32_16x16x32_bf16 v[52:55], v[146:149], v[200:203], v[52:55]
	v_mfma_f32_16x16x32_bf16 v[56:59], v[138:141], v[200:203], v[56:59]
	v_mfma_f32_16x16x32_bf16 v[48:51], v[138:141], v[208:211], v[48:51]
	v_mfma_f32_16x16x32_bf16 v[44:47], v[146:149], v[208:211], v[44:47]
	v_mfma_f32_16x16x32_bf16 v[36:39], v[146:149], v[216:219], v[36:39]
	v_mfma_f32_16x16x32_bf16 v[40:43], v[138:141], v[216:219], v[40:43]
	s_setprio 0
	s_setprio 1
	v_mfma_f32_16x16x32_bf16 v[30:33], v[150:153], v[166:169], v[30:33]
	v_mfma_f32_16x16x32_bf16 v[26:29], v[158:161], v[166:169], v[26:29]
	v_mfma_f32_16x16x32_bf16 v[18:21], v[158:161], v[182:185], v[18:21]
	v_mfma_f32_16x16x32_bf16 v[22:25], v[150:153], v[182:185], v[22:25]
	v_mfma_f32_16x16x32_bf16 v[14:17], v[150:153], v[204:207], v[14:17]
	v_mfma_f32_16x16x32_bf16 v[10:13], v[158:161], v[204:207], v[10:13]
	v_mfma_f32_16x16x32_bf16 v[2:5], v[158:161], v[212:215], v[2:5]
	v_mfma_f32_16x16x32_bf16 v[6:9], v[150:153], v[212:215], v[6:9]
	v_mfma_f32_16x16x32_bf16 v[30:33], v[154:157], v[178:181], v[30:33]
	v_mfma_f32_16x16x32_bf16 v[26:29], v[162:165], v[178:181], v[26:29]
	v_mfma_f32_16x16x32_bf16 v[18:21], v[162:165], v[200:203], v[18:21]
	v_mfma_f32_16x16x32_bf16 v[22:25], v[154:157], v[200:203], v[22:25]
	v_mfma_f32_16x16x32_bf16 v[14:17], v[154:157], v[208:211], v[14:17]
	v_mfma_f32_16x16x32_bf16 v[10:13], v[162:165], v[208:211], v[10:13]
	v_mfma_f32_16x16x32_bf16 v[2:5], v[162:165], v[216:219], v[2:5]
	v_mfma_f32_16x16x32_bf16 v[6:9], v[154:157], v[216:219], v[6:9]
	s_barrier
	s_setprio 0
	ds_read_b128 v[134:137], v132
	ds_read_b128 v[138:141], v132 offset:1024
	ds_read_b128 v[142:145], v132 offset:2048
	ds_read_b128 v[146:149], v132 offset:3072
	ds_read_b128 v[150:153], v133
	ds_read_b128 v[154:157], v133 offset:1024
	ds_read_b128 v[158:161], v133 offset:2048
	ds_read_b128 v[162:165], v133 offset:3072
	s_add_u32 s40, s40, 0x40000
	s_addc_u32 s41, s41, 0
	s_mov_b32 m0, s45
	v_lshl_add_u64 v[228:229], s[40:41], 0, v[194:195]
	ds_read_b128 v[166:169], v223 offset:32768
	ds_read_b128 v[178:181], v223 offset:33792
	ds_read_b128 v[182:185], v223 offset:34816
	ds_read_b128 v[200:203], v223 offset:35840
	ds_read_b128 v[204:207], v223 offset:36864
	ds_read_b128 v[208:211], v223 offset:37888
	ds_read_b128 v[212:215], v223 offset:38912
	ds_read_b128 v[216:219], v223 offset:39936
	global_load_lds_dwordx4 v[228:229], off
	v_lshl_add_u64 v[228:229], s[40:41], 0, v[192:193]
	s_mov_b32 m0, s46
	s_nop 0
	global_load_lds_dwordx4 v[228:229], off
	s_waitcnt vmcnt(8)
	s_waitcnt lgkmcnt(0)
	s_barrier
	v_mfma_f32_16x16x32_bf16 v[128:131], v[134:137], v[166:169], v[128:131]
	s_setprio 1
	v_mfma_f32_16x16x32_bf16 v[124:127], v[142:145], v[166:169], v[124:127]
	v_mfma_f32_16x16x32_bf16 v[116:119], v[142:145], v[182:185], v[116:119]
	v_mfma_f32_16x16x32_bf16 v[120:123], v[134:137], v[182:185], v[120:123]
	v_mfma_f32_16x16x32_bf16 v[112:115], v[134:137], v[204:207], v[112:115]
	v_mfma_f32_16x16x32_bf16 v[108:111], v[142:145], v[204:207], v[108:111]
	v_mfma_f32_16x16x32_bf16 v[100:103], v[142:145], v[212:215], v[100:103]
	v_mfma_f32_16x16x32_bf16 v[104:107], v[134:137], v[212:215], v[104:107]
	v_mfma_f32_16x16x32_bf16 v[128:131], v[138:141], v[178:181], v[128:131]
	v_mfma_f32_16x16x32_bf16 v[124:127], v[146:149], v[178:181], v[124:127]
	v_mfma_f32_16x16x32_bf16 v[116:119], v[146:149], v[200:203], v[116:119]
	v_mfma_f32_16x16x32_bf16 v[120:123], v[138:141], v[200:203], v[120:123]
	v_mfma_f32_16x16x32_bf16 v[112:115], v[138:141], v[208:211], v[112:115]
	v_mfma_f32_16x16x32_bf16 v[108:111], v[146:149], v[208:211], v[108:111]
	v_mfma_f32_16x16x32_bf16 v[100:103], v[146:149], v[216:219], v[100:103]
	v_mfma_f32_16x16x32_bf16 v[104:107], v[138:141], v[216:219], v[104:107]
	s_setprio 0
	s_setprio 1
	v_mfma_f32_16x16x32_bf16 v[96:99], v[150:153], v[166:169], v[96:99]
	v_mfma_f32_16x16x32_bf16 v[92:95], v[158:161], v[166:169], v[92:95]
	v_mfma_f32_16x16x32_bf16 v[84:87], v[158:161], v[182:185], v[84:87]
	v_mfma_f32_16x16x32_bf16 v[88:91], v[150:153], v[182:185], v[88:91]
	v_mfma_f32_16x16x32_bf16 v[80:83], v[150:153], v[204:207], v[80:83]
	v_mfma_f32_16x16x32_bf16 v[76:79], v[158:161], v[204:207], v[76:79]
	v_mfma_f32_16x16x32_bf16 v[68:71], v[158:161], v[212:215], v[68:71]
	v_mfma_f32_16x16x32_bf16 v[72:75], v[150:153], v[212:215], v[72:75]
	v_mfma_f32_16x16x32_bf16 v[96:99], v[154:157], v[178:181], v[96:99]
	v_mfma_f32_16x16x32_bf16 v[92:95], v[162:165], v[178:181], v[92:95]
	v_mfma_f32_16x16x32_bf16 v[84:87], v[162:165], v[200:203], v[84:87]
	v_mfma_f32_16x16x32_bf16 v[88:91], v[154:157], v[200:203], v[88:91]
	v_mfma_f32_16x16x32_bf16 v[80:83], v[154:157], v[208:211], v[80:83]
	v_mfma_f32_16x16x32_bf16 v[76:79], v[162:165], v[208:211], v[76:79]
	v_mfma_f32_16x16x32_bf16 v[68:71], v[162:165], v[216:219], v[68:71]
	v_mfma_f32_16x16x32_bf16 v[72:75], v[154:157], v[216:219], v[72:75]
	s_barrier
	s_setprio 0
	s_mov_b32 m0, s68
	v_lshl_add_u64 v[170:171], v[170:171], 0, s[18:19]
	s_add_u32 s30, s30, 0x40080
	ds_read_b128 v[166:169], v223 offset:49152
	ds_read_b128 v[178:181], v223 offset:50176
	ds_read_b128 v[182:185], v223 offset:51200
	ds_read_b128 v[200:203], v223 offset:52224
	ds_read_b128 v[204:207], v223 offset:53248
	ds_read_b128 v[208:211], v223 offset:54272
	ds_read_b128 v[212:215], v223 offset:55296
	ds_read_b128 v[216:219], v223 offset:56320
	global_load_lds_dwordx4 v[170:171], off
	v_lshl_add_u64 v[170:171], v[174:175], 0, s[18:19]
	s_mov_b32 m0, s69
	s_addc_u32 s31, s31, 0
	global_load_lds_dwordx4 v[170:171], off
	v_lshl_add_u64 v[170:171], s[30:31], 0, v[34:35]
	s_mov_b32 m0, s70
	s_nop 0
	global_load_lds_dwordx4 v[170:171], off
	v_lshl_add_u64 v[170:171], s[30:31], 0, v[190:191]
	s_mov_b32 m0, s71
	s_nop 0
	global_load_lds_dwordx4 v[170:171], off
	v_lshl_add_u64 v[170:171], v[224:225], 0, s[18:19]
	s_mov_b32 m0, s51
	s_nop 0
	global_load_lds_dwordx4 v[170:171], off
	v_lshl_add_u64 v[170:171], v[226:227], 0, s[18:19]
	s_mov_b32 m0, s52
	s_nop 0
	global_load_lds_dwordx4 v[170:171], off
	s_waitcnt vmcnt(8)
	s_waitcnt lgkmcnt(0)
	s_barrier
	v_mfma_f32_16x16x32_bf16 v[64:67], v[134:137], v[166:169], v[64:67]
	s_setprio 1
	v_mfma_f32_16x16x32_bf16 v[60:63], v[142:145], v[166:169], v[60:63]
	v_mfma_f32_16x16x32_bf16 v[52:55], v[142:145], v[182:185], v[52:55]
	v_mfma_f32_16x16x32_bf16 v[56:59], v[134:137], v[182:185], v[56:59]
	v_mfma_f32_16x16x32_bf16 v[48:51], v[134:137], v[204:207], v[48:51]
	v_mfma_f32_16x16x32_bf16 v[44:47], v[142:145], v[204:207], v[44:47]
	v_mfma_f32_16x16x32_bf16 v[36:39], v[142:145], v[212:215], v[36:39]
	v_mfma_f32_16x16x32_bf16 v[40:43], v[134:137], v[212:215], v[40:43]
	v_mfma_f32_16x16x32_bf16 v[64:67], v[138:141], v[178:181], v[64:67]
	v_mfma_f32_16x16x32_bf16 v[60:63], v[146:149], v[178:181], v[60:63]
	v_mfma_f32_16x16x32_bf16 v[52:55], v[146:149], v[200:203], v[52:55]
	v_mfma_f32_16x16x32_bf16 v[56:59], v[138:141], v[200:203], v[56:59]
	v_mfma_f32_16x16x32_bf16 v[48:51], v[138:141], v[208:211], v[48:51]
	v_mfma_f32_16x16x32_bf16 v[44:47], v[146:149], v[208:211], v[44:47]
	v_mfma_f32_16x16x32_bf16 v[36:39], v[146:149], v[216:219], v[36:39]
	v_mfma_f32_16x16x32_bf16 v[40:43], v[138:141], v[216:219], v[40:43]
	s_setprio 0
	s_setprio 1
	v_mfma_f32_16x16x32_bf16 v[30:33], v[150:153], v[166:169], v[30:33]
	v_mfma_f32_16x16x32_bf16 v[26:29], v[158:161], v[166:169], v[26:29]
	v_mfma_f32_16x16x32_bf16 v[18:21], v[158:161], v[182:185], v[18:21]
	v_mfma_f32_16x16x32_bf16 v[22:25], v[150:153], v[182:185], v[22:25]
	v_mfma_f32_16x16x32_bf16 v[14:17], v[150:153], v[204:207], v[14:17]
	v_mfma_f32_16x16x32_bf16 v[10:13], v[158:161], v[204:207], v[10:13]
	v_mfma_f32_16x16x32_bf16 v[2:5], v[158:161], v[212:215], v[2:5]
	v_mfma_f32_16x16x32_bf16 v[6:9], v[150:153], v[212:215], v[6:9]
	v_mfma_f32_16x16x32_bf16 v[30:33], v[154:157], v[178:181], v[30:33]
	v_mfma_f32_16x16x32_bf16 v[26:29], v[162:165], v[178:181], v[26:29]
	v_mfma_f32_16x16x32_bf16 v[18:21], v[162:165], v[200:203], v[18:21]
	v_mfma_f32_16x16x32_bf16 v[22:25], v[154:157], v[200:203], v[22:25]
	v_mfma_f32_16x16x32_bf16 v[14:17], v[154:157], v[208:211], v[14:17]
	v_mfma_f32_16x16x32_bf16 v[10:13], v[162:165], v[208:211], v[10:13]
	v_mfma_f32_16x16x32_bf16 v[2:5], v[162:165], v[216:219], v[2:5]
	v_mfma_f32_16x16x32_bf16 v[6:9], v[154:157], v[216:219], v[6:9]
	s_barrier
	s_setprio 0
	s_add_i32 s74, s74, 2
	s_add_u32 s36, s36, 0x100
	s_addc_u32 s37, s37, 0
	s_add_u32 s72, s72, 0x100
	s_addc_u32 s73, s73, 0
	s_cmp_gt_u32 s74, 13
	s_cbranch_scc0 .LBB0_541
	v_readlane_b32 s74, v255, 3
	s_and_b64 vcc, exec, s[10:11]
	v_readlane_b32 s75, v255, 4
	s_mov_b32 s58, 0x19b00000
	v_readlane_b32 s59, v255, 10
	s_mov_b32 s60, 0xff61b1e6
	s_mov_b64 s[62:63], 0x800
	s_mov_b32 s64, 0x3b000000
	s_cbranch_vccz .LBB0_544
	s_barrier

.LBB0_819:
	s_add_u32 s81, s30, 0x200
	s_addc_u32 s82, s31, 0
	s_add_i32 s55, 0, 0x14000
	s_add_i32 s52, 0, 0x10000
	v_add_u32_e32 v199, s55, v167
	v_add_u32_e32 v200, s52, v167
	ds_read_b128 v[10:13], v199
	ds_read_b128 v[14:17], v199 offset:1024
	ds_read_b128 v[2:5], v199 offset:2048
	ds_read_b128 v[6:9], v199 offset:3072
	ds_read_b128 v[22:25], v200 offset:3072
	ds_read_b128 v[18:21], v200 offset:2048
	ds_read_b128 v[30:33], v200 offset:1024
	ds_read_b128 v[26:29], v200
	s_lshl_b32 s14, s80, 10
	s_add_i32 s83, s14, 0
	s_add_i32 s83, s83, 0x20400
	v_mov_b32_e32 v191, v35
	v_mov_b32_e32 v175, v35
	s_add_i32 s84, s69, 0xc000
	v_readlane_b32 s26, v253, 28
	s_mov_b32 m0, s84
	v_readlane_b32 s27, v253, 29
	s_add_i32 s53, s69, 0xe000
	ds_read_b128 v[202:205], v169
	ds_read_b128 v[206:209], v169 offset:1024
	ds_read_b128 v[222:225], v169 offset:2048
	ds_read_b128 v[226:229], v169 offset:3072
	ds_read_b128 v[230:233], v169 offset:4096
	ds_read_b128 v[234:237], v169 offset:5120
	ds_read_b128 v[238:241], v169 offset:6144
	ds_read_b128 v[242:245], v169 offset:7168
	global_load_lds_dwordx4 v190, s[26:27]
	s_mov_b32 m0, s53
	s_nop 0
	global_load_lds_dwordx4 v174, s[26:27]
	s_waitcnt vmcnt(8)
	s_waitcnt lgkmcnt(0)
	s_barrier
	v_mfma_f32_16x16x128_f8f6f4 v[160:163], v[26:33], v[202:209], 0
	s_setprio 1
	v_mfma_f32_16x16x128_f8f6f4 v[156:159], v[18:25], v[202:209], 0
	v_mfma_f32_16x16x128_f8f6f4 v[148:151], v[18:25], v[222:229], 0
	v_mfma_f32_16x16x128_f8f6f4 v[152:155], v[26:33], v[222:229], 0
	v_mfma_f32_16x16x128_f8f6f4 v[144:147], v[26:33], v[230:237], 0
	v_mfma_f32_16x16x128_f8f6f4 v[140:143], v[18:25], v[230:237], 0
	v_mfma_f32_16x16x128_f8f6f4 v[132:135], v[18:25], v[238:245], 0
	v_mfma_f32_16x16x128_f8f6f4 v[136:139], v[26:33], v[238:245], 0
	s_setprio 0
	s_setprio 1
	v_mfma_f32_16x16x128_f8f6f4 v[128:131], v[10:17], v[202:209], 0
	v_mfma_f32_16x16x128_f8f6f4 v[124:127], v[2:9], v[202:209], 0
	v_mfma_f32_16x16x128_f8f6f4 v[116:119], v[2:9], v[222:229], 0
	v_mfma_f32_16x16x128_f8f6f4 v[120:123], v[10:17], v[222:229], 0
	v_mfma_f32_16x16x128_f8f6f4 v[112:115], v[10:17], v[230:237], 0
	v_mfma_f32_16x16x128_f8f6f4 v[108:111], v[2:9], v[230:237], 0
	v_mfma_f32_16x16x128_f8f6f4 v[100:103], v[2:9], v[238:245], 0
	v_mfma_f32_16x16x128_f8f6f4 v[104:107], v[10:17], v[238:245], 0
	s_barrier
	s_setprio 0
	s_add_i32 s52, s52, s68
	v_lshl_add_u64 v[194:195], s[30:31], 0, v[170:171]
	s_add_i32 s85, s52, 0x2000
	v_lshl_add_u64 v[178:179], v[194:195], 0, s[28:29]
	s_mov_b32 m0, s52
	v_lshl_add_u64 v[196:197], s[30:31], 0, v[172:173]
	s_add_u32 s36, s30, 0x20100
	ds_read_b128 v[202:205], v169 offset:16384
	ds_read_b128 v[206:209], v169 offset:17408
	ds_read_b128 v[222:225], v169 offset:18432
	ds_read_b128 v[226:229], v169 offset:19456
	ds_read_b128 v[230:233], v169 offset:20480
	ds_read_b128 v[234:237], v169 offset:21504
	ds_read_b128 v[238:241], v169 offset:22528
	ds_read_b128 v[242:245], v169 offset:23552
	global_load_lds_dwordx4 v[178:179], off
	v_lshl_add_u64 v[178:179], v[196:197], 0, s[28:29]
	s_mov_b32 m0, s85
	s_addc_u32 s37, s31, 0
	s_add_i32 s55, s55, s68
	global_load_lds_dwordx4 v[178:179], off
	v_lshl_add_u64 v[178:179], s[36:37], 0, v[170:171]
	s_mov_b32 m0, s55
	s_add_i32 s65, s55, 0x2000
	global_load_lds_dwordx4 v[178:179], off
	v_lshl_add_u64 v[178:179], s[36:37], 0, v[172:173]
	s_mov_b32 m0, s65
	v_readlane_b32 s26, v253, 37
	global_load_lds_dwordx4 v[178:179], off
	s_mov_b32 m0, s69
	v_readlane_b32 s27, v253, 38
	s_nop 4
	global_load_lds_dwordx4 v34, s[26:27]
	s_mov_b32 m0, s70
	s_nop 0
	global_load_lds_dwordx4 v192, s[26:27]
	s_waitcnt vmcnt(8)
	s_waitcnt lgkmcnt(0)
	s_barrier
	v_mfma_f32_16x16x128_f8f6f4 v[96:99], v[26:33], v[202:209], 0
	s_setprio 1
	v_mfma_f32_16x16x128_f8f6f4 v[92:95], v[18:25], v[202:209], 0
	v_mfma_f32_16x16x128_f8f6f4 v[84:87], v[18:25], v[222:229], 0
	v_mfma_f32_16x16x128_f8f6f4 v[88:91], v[26:33], v[222:229], 0
	v_mfma_f32_16x16x128_f8f6f4 v[80:83], v[26:33], v[230:237], 0
	v_mfma_f32_16x16x128_f8f6f4 v[76:79], v[18:25], v[230:237], 0
	v_mfma_f32_16x16x128_f8f6f4 v[68:71], v[18:25], v[238:245], 0
	v_mfma_f32_16x16x128_f8f6f4 v[72:75], v[26:33], v[238:245], 0
	s_setprio 0
	s_setprio 1
	v_mfma_f32_16x16x128_f8f6f4 v[64:67], v[10:17], v[202:209], 0
	v_mfma_f32_16x16x128_f8f6f4 v[60:63], v[2:9], v[202:209], 0
	v_mfma_f32_16x16x128_f8f6f4 v[52:55], v[2:9], v[222:229], 0
	v_mfma_f32_16x16x128_f8f6f4 v[56:59], v[10:17], v[222:229], 0
	v_mfma_f32_16x16x128_f8f6f4 v[48:51], v[10:17], v[230:237], 0
	v_mfma_f32_16x16x128_f8f6f4 v[44:47], v[2:9], v[230:237], 0
	v_mfma_f32_16x16x128_f8f6f4 v[36:39], v[2:9], v[238:245], 0
	v_mfma_f32_16x16x128_f8f6f4 v[40:43], v[10:17], v[238:245], 0
	s_barrier
	s_setprio 0
	s_add_i32 s54, 0, 0x18000
	s_add_i32 s51, 0, 0x1c000
	v_add_u32_e32 v201, s54, v167
	v_add_u32_e32 v202, s51, v167
	ds_read_b128 v[26:29], v201
	ds_read_b128 v[30:33], v201 offset:1024
	ds_read_b128 v[18:21], v201 offset:2048
	ds_read_b128 v[22:25], v201 offset:3072
	ds_read_b128 v[10:13], v202
	ds_read_b128 v[14:17], v202 offset:1024
	ds_read_b128 v[2:5], v202 offset:2048
	ds_read_b128 v[6:9], v202 offset:3072
	s_mov_b32 m0, s71
	ds_read_b128 v[204:207], v169 offset:32768
	ds_read_b128 v[208:211], v169 offset:33792
	ds_read_b128 v[222:225], v169 offset:34816
	ds_read_b128 v[226:229], v169 offset:35840
	ds_read_b128 v[230:233], v169 offset:36864
	ds_read_b128 v[234:237], v169 offset:37888
	ds_read_b128 v[238:241], v169 offset:38912
	ds_read_b128 v[242:245], v169 offset:39936
	global_load_lds_dwordx4 v189, s[26:27]
	s_mov_b32 m0, s72
	s_nop 0
	global_load_lds_dwordx4 v198, s[26:27]
	s_waitcnt vmcnt(8)
	s_waitcnt lgkmcnt(0)
	s_barrier
	v_mfma_f32_16x16x128_f8f6f4 v[160:163], v[26:33], v[204:211], v[160:163]
	s_setprio 1
	v_mfma_f32_16x16x128_f8f6f4 v[156:159], v[18:25], v[204:211], v[156:159]
	v_mfma_f32_16x16x128_f8f6f4 v[148:151], v[18:25], v[222:229], v[148:151]
	v_mfma_f32_16x16x128_f8f6f4 v[152:155], v[26:33], v[222:229], v[152:155]
	v_mfma_f32_16x16x128_f8f6f4 v[144:147], v[26:33], v[230:237], v[144:147]
	v_mfma_f32_16x16x128_f8f6f4 v[140:143], v[18:25], v[230:237], v[140:143]
	v_mfma_f32_16x16x128_f8f6f4 v[132:135], v[18:25], v[238:245], v[132:135]
	v_mfma_f32_16x16x128_f8f6f4 v[136:139], v[26:33], v[238:245], v[136:139]
	s_setprio 0
	s_setprio 1
	v_mfma_f32_16x16x128_f8f6f4 v[128:131], v[10:17], v[204:211], v[128:131]
	v_mfma_f32_16x16x128_f8f6f4 v[124:127], v[2:9], v[204:211], v[124:127]
	v_mfma_f32_16x16x128_f8f6f4 v[116:119], v[2:9], v[222:229], v[116:119]
	v_mfma_f32_16x16x128_f8f6f4 v[120:123], v[10:17], v[222:229], v[120:123]
	v_mfma_f32_16x16x128_f8f6f4 v[112:115], v[10:17], v[230:237], v[112:115]
	v_mfma_f32_16x16x128_f8f6f4 v[108:111], v[2:9], v[230:237], v[108:111]
	v_mfma_f32_16x16x128_f8f6f4 v[100:103], v[2:9], v[238:245], v[100:103]
	v_mfma_f32_16x16x128_f8f6f4 v[104:107], v[10:17], v[238:245], v[104:107]
	s_barrier
	s_setprio 0
	s_add_i32 s54, s54, s68
	s_mov_b64 s[26:27], 0x180
	s_add_i32 s50, s54, 0x2000
	v_lshl_add_u64 v[178:179], v[194:195], 0, s[26:27]
	s_mov_b32 m0, s54
	s_add_u32 s30, s30, 0x20180
	ds_read_b128 v[204:207], v169 offset:49152
	ds_read_b128 v[208:211], v169 offset:50176
	ds_read_b128 v[222:225], v169 offset:51200
	ds_read_b128 v[226:229], v169 offset:52224
	ds_read_b128 v[230:233], v169 offset:53248
	ds_read_b128 v[234:237], v169 offset:54272
	ds_read_b128 v[238:241], v169 offset:55296
	ds_read_b128 v[242:245], v169 offset:56320
	global_load_lds_dwordx4 v[178:179], off
	v_lshl_add_u64 v[178:179], v[196:197], 0, s[26:27]
	s_mov_b32 m0, s50
	s_addc_u32 s31, s31, 0
	s_add_i32 s51, s51, s68
	global_load_lds_dwordx4 v[178:179], off
	v_lshl_add_u64 v[178:179], s[30:31], 0, v[170:171]
	s_mov_b32 m0, s51
	s_add_i32 s64, s51, 0x2000
	global_load_lds_dwordx4 v[178:179], off
	v_lshl_add_u64 v[178:179], s[30:31], 0, v[172:173]
	s_mov_b32 m0, s64
	v_readlane_b32 s26, v253, 39
	global_load_lds_dwordx4 v[178:179], off
	s_mov_b32 m0, s75
	v_readlane_b32 s27, v253, 40
	s_nop 4
	global_load_lds_dwordx4 v34, s[26:27]
	s_mov_b32 m0, s76
	s_nop 0
	global_load_lds_dwordx4 v192, s[26:27]
	s_waitcnt vmcnt(8)
	s_waitcnt lgkmcnt(0)
	s_barrier
	v_mfma_f32_16x16x128_f8f6f4 v[96:99], v[26:33], v[204:211], v[96:99]
	s_setprio 1
	v_mfma_f32_16x16x128_f8f6f4 v[92:95], v[18:25], v[204:211], v[92:95]
	v_mfma_f32_16x16x128_f8f6f4 v[84:87], v[18:25], v[222:229], v[84:87]
	v_mfma_f32_16x16x128_f8f6f4 v[88:91], v[26:33], v[222:229], v[88:91]
	v_mfma_f32_16x16x128_f8f6f4 v[80:83], v[26:33], v[230:237], v[80:83]
	v_mfma_f32_16x16x128_f8f6f4 v[76:79], v[18:25], v[230:237], v[76:79]
	v_mfma_f32_16x16x128_f8f6f4 v[68:71], v[18:25], v[238:245], v[68:71]
	v_mfma_f32_16x16x128_f8f6f4 v[72:75], v[26:33], v[238:245], v[72:75]
	s_setprio 0
	s_setprio 1
	v_mfma_f32_16x16x128_f8f6f4 v[64:67], v[10:17], v[204:211], v[64:67]
	v_mfma_f32_16x16x128_f8f6f4 v[60:63], v[2:9], v[204:211], v[60:63]
	v_mfma_f32_16x16x128_f8f6f4 v[52:55], v[2:9], v[222:229], v[52:55]
	v_mfma_f32_16x16x128_f8f6f4 v[56:59], v[10:17], v[222:229], v[56:59]
	v_mfma_f32_16x16x128_f8f6f4 v[48:51], v[10:17], v[230:237], v[48:51]
	v_mfma_f32_16x16x128_f8f6f4 v[44:47], v[2:9], v[230:237], v[44:47]
	v_mfma_f32_16x16x128_f8f6f4 v[36:39], v[2:9], v[238:245], v[36:39]
	v_mfma_f32_16x16x128_f8f6f4 v[40:43], v[10:17], v[238:245], v[40:43]
	s_barrier
	s_setprio 0
	v_lshl_add_u64 v[18:19], s[26:27], 0, v[174:175]
	v_lshl_add_u64 v[20:21], s[26:27], 0, v[190:191]
	s_mov_b32 s63, 0
	s_mov_b64 s[30:31], 0
	s_branch .LBB0_821
.LBB0_820:
	ds_read_b128 v[204:207], v200
	ds_read_b128 v[208:211], v200 offset:1024
	ds_read_b128 v[222:225], v200 offset:2048
	ds_read_b128 v[226:229], v200 offset:3072
	ds_read_b128 v[10:13], v199
	ds_read_b128 v[14:17], v199 offset:1024
	ds_read_b128 v[2:5], v199 offset:2048
	ds_read_b128 v[6:9], v199 offset:3072
	s_add_u32 s14, s30, 0x200
	s_addc_u32 s86, s31, 0
	s_and_b64 s[40:41], s[36:37], exec
	s_cselect_b32 s14, 0, s14
	s_cselect_b32 s41, 0, s86
	s_add_u32 s40, s20, s14
	s_addc_u32 s41, s21, s41
	s_add_u32 s14, s81, s30
	s_addc_u32 s86, s82, s31
	s_and_b64 s[36:37], s[36:37], exec
	s_cselect_b32 s37, s23, s86
	s_cselect_b32 s36, s22, s14
	s_mov_b32 m0, s84
	v_lshl_add_u64 v[30:31], v[20:21], 0, s[30:31]
	ds_read_b128 v[22:25], v169
	ds_read_b128 v[26:29], v169 offset:1024
	ds_read_b128 v[230:233], v169 offset:2048
	ds_read_b128 v[234:237], v169 offset:3072
	ds_read_b128 v[238:241], v169 offset:4096
	ds_read_b128 v[242:245], v169 offset:5120
	ds_read_b128 v[178:181], v169 offset:6144
	ds_read_b128 v[182:185], v169 offset:7168
	global_load_lds_dwordx4 v[30:31], off
	v_lshl_add_u64 v[30:31], v[18:19], 0, s[30:31]
	s_mov_b32 m0, s53
	s_nop 0
	global_load_lds_dwordx4 v[30:31], off
	s_waitcnt vmcnt(8)
	s_waitcnt lgkmcnt(0)
	s_barrier
	v_mfma_f32_16x16x128_f8f6f4 v[160:163], v[204:211], v[22:29], v[160:163]
	s_setprio 1
	v_mfma_f32_16x16x128_f8f6f4 v[156:159], v[222:229], v[22:29], v[156:159]
	v_mfma_f32_16x16x128_f8f6f4 v[148:151], v[222:229], v[230:237], v[148:151]
	v_mfma_f32_16x16x128_f8f6f4 v[152:155], v[204:211], v[230:237], v[152:155]
	v_mfma_f32_16x16x128_f8f6f4 v[144:147], v[204:211], v[238:245], v[144:147]
	v_mfma_f32_16x16x128_f8f6f4 v[140:143], v[222:229], v[238:245], v[140:143]
	v_mfma_f32_16x16x128_f8f6f4 v[132:135], v[222:229], v[178:185], v[132:135]
	v_mfma_f32_16x16x128_f8f6f4 v[136:139], v[204:211], v[178:185], v[136:139]
	s_setprio 0
	s_setprio 1
	v_mfma_f32_16x16x128_f8f6f4 v[128:131], v[10:17], v[22:29], v[128:131]
	v_mfma_f32_16x16x128_f8f6f4 v[124:127], v[2:9], v[22:29], v[124:127]
	v_mfma_f32_16x16x128_f8f6f4 v[116:119], v[2:9], v[230:237], v[116:119]
	v_mfma_f32_16x16x128_f8f6f4 v[120:123], v[10:17], v[230:237], v[120:123]
	v_mfma_f32_16x16x128_f8f6f4 v[112:115], v[10:17], v[238:245], v[112:115]
	v_mfma_f32_16x16x128_f8f6f4 v[108:111], v[2:9], v[238:245], v[108:111]
	v_mfma_f32_16x16x128_f8f6f4 v[100:103], v[2:9], v[178:185], v[100:103]
	v_mfma_f32_16x16x128_f8f6f4 v[104:107], v[10:17], v[178:185], v[104:107]
	s_barrier
	s_setprio 0
	s_mov_b32 m0, s52
	v_lshl_add_u64 v[22:23], s[36:37], 0, v[170:171]
	s_add_u32 s86, s36, 0x20000
	ds_read_b128 v[178:181], v169 offset:16384
	ds_read_b128 v[182:185], v169 offset:17408
	ds_read_b128 v[230:233], v169 offset:18432
	ds_read_b128 v[234:237], v169 offset:19456
	ds_read_b128 v[238:241], v169 offset:20480
	ds_read_b128 v[242:245], v169 offset:21504
	ds_read_b128 v[212:215], v169 offset:22528
	ds_read_b128 v[216:219], v169 offset:23552
	global_load_lds_dwordx4 v[22:23], off
	v_lshl_add_u64 v[24:25], s[36:37], 0, v[172:173]
	s_mov_b32 m0, s85
	s_addc_u32 s87, s37, 0
	global_load_lds_dwordx4 v[24:25], off
	v_lshl_add_u64 v[26:27], s[86:87], 0, v[170:171]
	s_mov_b32 m0, s55
	v_mov_b32_e32 v193, v35
	global_load_lds_dwordx4 v[26:27], off
	v_lshl_add_u64 v[26:27], s[86:87], 0, v[172:173]
	s_mov_b32 m0, s65
	v_lshl_add_u64 v[28:29], s[40:41], 0, v[34:35]
	global_load_lds_dwordx4 v[26:27], off
	s_mov_b32 m0, s69
	v_lshl_add_u64 v[26:27], s[40:41], 0, v[192:193]
	global_load_lds_dwordx4 v34, s[40:41]
	s_mov_b32 m0, s70
	s_nop 0
	global_load_lds_dwordx4 v192, s[40:41]
	s_waitcnt vmcnt(8)
	s_waitcnt lgkmcnt(0)
	s_barrier
	v_mfma_f32_16x16x128_f8f6f4 v[96:99], v[204:211], v[178:185], v[96:99]
	s_setprio 1
	v_mfma_f32_16x16x128_f8f6f4 v[92:95], v[222:229], v[178:185], v[92:95]
	v_mfma_f32_16x16x128_f8f6f4 v[84:87], v[222:229], v[230:237], v[84:87]
	v_mfma_f32_16x16x128_f8f6f4 v[88:91], v[204:211], v[230:237], v[88:91]
	v_mfma_f32_16x16x128_f8f6f4 v[80:83], v[204:211], v[238:245], v[80:83]
	v_mfma_f32_16x16x128_f8f6f4 v[76:79], v[222:229], v[238:245], v[76:79]
	v_mfma_f32_16x16x128_f8f6f4 v[68:71], v[222:229], v[212:219], v[68:71]
	v_mfma_f32_16x16x128_f8f6f4 v[72:75], v[204:211], v[212:219], v[72:75]
	s_setprio 0
	s_setprio 1
	v_mfma_f32_16x16x128_f8f6f4 v[64:67], v[10:17], v[178:185], v[64:67]
	v_mfma_f32_16x16x128_f8f6f4 v[60:63], v[2:9], v[178:185], v[60:63]
	v_mfma_f32_16x16x128_f8f6f4 v[52:55], v[2:9], v[230:237], v[52:55]
	v_mfma_f32_16x16x128_f8f6f4 v[56:59], v[10:17], v[230:237], v[56:59]
	v_mfma_f32_16x16x128_f8f6f4 v[48:51], v[10:17], v[238:245], v[48:51]
	v_mfma_f32_16x16x128_f8f6f4 v[44:47], v[2:9], v[238:245], v[44:47]
	v_mfma_f32_16x16x128_f8f6f4 v[36:39], v[2:9], v[212:219], v[36:39]
	v_mfma_f32_16x16x128_f8f6f4 v[40:43], v[10:17], v[212:219], v[40:43]
	s_barrier
	s_setprio 0
	ds_read_b128 v[178:181], v201
	ds_read_b128 v[182:185], v201 offset:1024
	ds_read_b128 v[204:207], v201 offset:2048
	ds_read_b128 v[208:211], v201 offset:3072
	ds_read_b128 v[10:13], v202
	ds_read_b128 v[14:17], v202 offset:1024
	ds_read_b128 v[2:5], v202 offset:2048
	ds_read_b128 v[6:9], v202 offset:3072
	s_mov_b32 m0, s71
	ds_read_b128 v[212:215], v169 offset:32768
	ds_read_b128 v[216:219], v169 offset:33792
	ds_read_b128 v[222:225], v169 offset:34816
	ds_read_b128 v[226:229], v169 offset:35840
	ds_read_b128 v[230:233], v169 offset:36864
	ds_read_b128 v[234:237], v169 offset:37888
	ds_read_b128 v[238:241], v169 offset:38912
	ds_read_b128 v[242:245], v169 offset:39936
	global_load_lds_dwordx4 v189, s[40:41]
	s_mov_b32 m0, s72
	s_nop 0
	global_load_lds_dwordx4 v198, s[40:41]
	s_waitcnt vmcnt(8)
	s_waitcnt lgkmcnt(0)
	s_barrier
	v_mfma_f32_16x16x128_f8f6f4 v[160:163], v[178:185], v[212:219], v[160:163]
	s_setprio 1
	v_mfma_f32_16x16x128_f8f6f4 v[156:159], v[204:211], v[212:219], v[156:159]
	v_mfma_f32_16x16x128_f8f6f4 v[148:151], v[204:211], v[222:229], v[148:151]
	v_mfma_f32_16x16x128_f8f6f4 v[152:155], v[178:185], v[222:229], v[152:155]
	v_mfma_f32_16x16x128_f8f6f4 v[144:147], v[178:185], v[230:237], v[144:147]
	v_mfma_f32_16x16x128_f8f6f4 v[140:143], v[204:211], v[230:237], v[140:143]
	v_mfma_f32_16x16x128_f8f6f4 v[132:135], v[204:211], v[238:245], v[132:135]
	v_mfma_f32_16x16x128_f8f6f4 v[136:139], v[178:185], v[238:245], v[136:139]
	s_setprio 0
	s_setprio 1
	v_mfma_f32_16x16x128_f8f6f4 v[128:131], v[10:17], v[212:219], v[128:131]
	v_mfma_f32_16x16x128_f8f6f4 v[124:127], v[2:9], v[212:219], v[124:127]
	v_mfma_f32_16x16x128_f8f6f4 v[116:119], v[2:9], v[222:229], v[116:119]
	v_mfma_f32_16x16x128_f8f6f4 v[120:123], v[10:17], v[222:229], v[120:123]
	v_mfma_f32_16x16x128_f8f6f4 v[112:115], v[10:17], v[230:237], v[112:115]
	v_mfma_f32_16x16x128_f8f6f4 v[108:111], v[2:9], v[230:237], v[108:111]
	v_mfma_f32_16x16x128_f8f6f4 v[100:103], v[2:9], v[238:245], v[100:103]
	v_mfma_f32_16x16x128_f8f6f4 v[104:107], v[10:17], v[238:245], v[104:107]
	s_barrier
	s_setprio 0
	s_mov_b32 m0, s54
	v_lshl_add_u64 v[22:23], v[22:23], 0, s[18:19]
	s_add_u32 s36, s36, 0x20080
	ds_read_b128 v[212:215], v169 offset:49152
	ds_read_b128 v[216:219], v169 offset:50176
	ds_read_b128 v[222:225], v169 offset:51200
	ds_read_b128 v[226:229], v169 offset:52224
	ds_read_b128 v[230:233], v169 offset:53248
	ds_read_b128 v[234:237], v169 offset:54272
	ds_read_b128 v[238:241], v169 offset:55296
	ds_read_b128 v[242:245], v169 offset:56320
	global_load_lds_dwordx4 v[22:23], off
	v_lshl_add_u64 v[22:23], v[24:25], 0, s[18:19]
	s_mov_b32 m0, s50
	s_addc_u32 s37, s37, 0
	global_load_lds_dwordx4 v[22:23], off
	v_lshl_add_u64 v[22:23], s[36:37], 0, v[170:171]
	s_mov_b32 m0, s51
	s_nop 0
	global_load_lds_dwordx4 v[22:23], off
	v_lshl_add_u64 v[22:23], s[36:37], 0, v[172:173]
	s_mov_b32 m0, s64
	s_nop 0
	global_load_lds_dwordx4 v[22:23], off
	v_lshl_add_u64 v[22:23], v[28:29], 0, s[18:19]
	s_mov_b32 m0, s75
	s_nop 0
	global_load_lds_dwordx4 v[22:23], off
	v_lshl_add_u64 v[22:23], v[26:27], 0, s[18:19]
	s_mov_b32 m0, s76
	s_nop 0
	global_load_lds_dwordx4 v[22:23], off
	s_waitcnt vmcnt(8)
	s_waitcnt lgkmcnt(0)
	s_barrier
	v_mfma_f32_16x16x128_f8f6f4 v[96:99], v[178:185], v[212:219], v[96:99]
	s_setprio 1
	v_mfma_f32_16x16x128_f8f6f4 v[92:95], v[204:211], v[212:219], v[92:95]
	v_mfma_f32_16x16x128_f8f6f4 v[84:87], v[204:211], v[222:229], v[84:87]
	v_mfma_f32_16x16x128_f8f6f4 v[88:91], v[178:185], v[222:229], v[88:91]
	v_mfma_f32_16x16x128_f8f6f4 v[80:83], v[178:185], v[230:237], v[80:83]
	v_mfma_f32_16x16x128_f8f6f4 v[76:79], v[204:211], v[230:237], v[76:79]
	v_mfma_f32_16x16x128_f8f6f4 v[68:71], v[204:211], v[238:245], v[68:71]
	v_mfma_f32_16x16x128_f8f6f4 v[72:75], v[178:185], v[238:245], v[72:75]
	s_setprio 0
	s_setprio 1
	v_mfma_f32_16x16x128_f8f6f4 v[64:67], v[10:17], v[212:219], v[64:67]
	v_mfma_f32_16x16x128_f8f6f4 v[60:63], v[2:9], v[212:219], v[60:63]
	v_mfma_f32_16x16x128_f8f6f4 v[52:55], v[2:9], v[222:229], v[52:55]
	v_mfma_f32_16x16x128_f8f6f4 v[56:59], v[10:17], v[222:229], v[56:59]
	v_mfma_f32_16x16x128_f8f6f4 v[48:51], v[10:17], v[230:237], v[48:51]
	v_mfma_f32_16x16x128_f8f6f4 v[44:47], v[2:9], v[230:237], v[44:47]
	v_mfma_f32_16x16x128_f8f6f4 v[36:39], v[2:9], v[238:245], v[36:39]
	v_mfma_f32_16x16x128_f8f6f4 v[40:43], v[10:17], v[238:245], v[40:43]
	s_barrier
	s_setprio 0
	s_add_i32 s63, s63, 2
	s_add_u32 s30, s30, 0x100
	s_addc_u32 s31, s31, 0
	s_cmp_gt_u32 s63, 5
	s_cbranch_scc1 .LBB0_823

.LBB0_899:
	s_mul_i32 s14, s81, 0xe0000
	s_add_u32 s40, s44, s14
	s_addc_u32 s41, s45, 0
	s_and_b64 s[6:7], s[6:7], exec
	s_cselect_b32 s52, s41, s43
	s_cselect_b32 s53, s40, s42
	s_add_i32 s54, 0, 0x10000
	s_add_i32 s65, 0, 0x14000
	v_add_u32_e32 v34, s54, v167
	v_add_u32_e32 v206, s65, v167
	ds_read_b128 v[26:29], v34
	ds_read_b128 v[30:33], v34 offset:1024
	ds_read_b128 v[18:21], v34 offset:2048
	ds_read_b128 v[22:25], v34 offset:3072
	ds_read_b128 v[10:13], v206
	ds_read_b128 v[14:17], v206 offset:1024
	ds_read_b128 v[2:5], v206 offset:2048
	ds_read_b128 v[6:9], v206 offset:3072
	s_add_u32 s6, s42, 0x70080
	s_addc_u32 s7, s43, 0
	s_add_i32 s84, s72, 0xc000
	v_lshl_add_u64 v[216:217], s[6:7], 0, v[174:175]
	s_mov_b32 m0, s84
	s_add_i32 s85, s72, 0xe000
	ds_read_b128 v[178:181], v189
	ds_read_b128 v[182:185], v189 offset:1024
	ds_read_b128 v[198:201], v189 offset:2048
	ds_read_b128 v[202:205], v189 offset:3072
	ds_read_b128 v[208:211], v189 offset:4096
	ds_read_b128 v[212:215], v189 offset:5120
	ds_read_b128 v[222:225], v189 offset:6144
	ds_read_b128 v[226:229], v189 offset:7168
	global_load_lds_dwordx4 v[216:217], off
	v_lshl_add_u64 v[216:217], s[6:7], 0, v[170:171]
	s_mov_b32 m0, s85
	s_nop 0
	global_load_lds_dwordx4 v[216:217], off
	s_waitcnt vmcnt(8)
	s_waitcnt lgkmcnt(0)
	s_barrier
	v_mfma_f32_16x16x128_f8f6f4 v[160:163], v[26:33], v[178:185], 0
	s_setprio 1
	v_mfma_f32_16x16x128_f8f6f4 v[156:159], v[18:25], v[178:185], 0
	v_mfma_f32_16x16x128_f8f6f4 v[148:151], v[18:25], v[198:205], 0
	v_mfma_f32_16x16x128_f8f6f4 v[152:155], v[26:33], v[198:205], 0
	v_mfma_f32_16x16x128_f8f6f4 v[144:147], v[26:33], v[208:215], 0
	v_mfma_f32_16x16x128_f8f6f4 v[140:143], v[18:25], v[208:215], 0
	v_mfma_f32_16x16x128_f8f6f4 v[132:135], v[18:25], v[222:229], 0
	v_mfma_f32_16x16x128_f8f6f4 v[136:139], v[26:33], v[222:229], 0
	s_setprio 0
	s_setprio 1
	v_mfma_f32_16x16x128_f8f6f4 v[128:131], v[10:17], v[178:185], 0
	v_mfma_f32_16x16x128_f8f6f4 v[124:127], v[2:9], v[178:185], 0
	v_mfma_f32_16x16x128_f8f6f4 v[116:119], v[2:9], v[198:205], 0
	v_mfma_f32_16x16x128_f8f6f4 v[120:123], v[10:17], v[198:205], 0
	v_mfma_f32_16x16x128_f8f6f4 v[112:115], v[10:17], v[208:215], 0
	v_mfma_f32_16x16x128_f8f6f4 v[108:111], v[2:9], v[208:215], 0
	v_mfma_f32_16x16x128_f8f6f4 v[100:103], v[2:9], v[222:229], 0
	v_mfma_f32_16x16x128_f8f6f4 v[104:107], v[10:17], v[222:229], 0
	s_barrier
	s_setprio 0
	v_lshl_add_u64 v[198:199], v[196:197], 0, v[172:173]
	s_add_i32 s54, s54, s71
	v_lshl_add_u64 v[200:201], v[198:199], 0, s[28:29]
	s_mov_b32 m0, s54
	ds_read_b128 v[178:181], v189 offset:16384
	ds_read_b128 v[182:185], v189 offset:17408
	ds_read_b128 v[208:211], v189 offset:18432
	ds_read_b128 v[212:215], v189 offset:19456
	ds_read_b128 v[222:225], v189 offset:20480
	ds_read_b128 v[226:229], v189 offset:21504
	ds_read_b128 v[230:233], v189 offset:22528
	ds_read_b128 v[234:237], v189 offset:23552
	global_load_lds_dwordx4 v[200:201], off
	v_lshl_add_u64 v[200:201], v[196:197], 0, v[168:169]
	s_add_i32 s55, s54, 0x2000
	v_lshl_add_u64 v[202:203], v[200:201], 0, s[28:29]
	s_mov_b32 m0, s55
	s_mov_b64 s[6:7], 0x70100
	global_load_lds_dwordx4 v[202:203], off
	v_lshl_add_u64 v[202:203], v[196:197], 0, s[6:7]
	s_add_i32 s65, s65, s71
	v_lshl_add_u64 v[204:205], v[202:203], 0, v[172:173]
	s_mov_b32 m0, s65
	s_add_i32 s67, s65, 0x2000
	global_load_lds_dwordx4 v[204:205], off
	v_lshl_add_u64 v[202:203], v[202:203], 0, v[168:169]
	s_mov_b32 m0, s67
	s_nop 0
	global_load_lds_dwordx4 v[202:203], off
	v_lshl_add_u64 v[202:203], s[42:43], 0, v[174:175]
	v_lshl_add_u64 v[204:205], v[202:203], 0, s[28:29]
	s_mov_b32 m0, s72
	s_nop 0
	global_load_lds_dwordx4 v[204:205], off
	v_lshl_add_u64 v[204:205], s[42:43], 0, v[170:171]
	v_lshl_add_u64 v[216:217], v[204:205], 0, s[28:29]
	s_mov_b32 m0, s73
	s_nop 0
	global_load_lds_dwordx4 v[216:217], off
	s_waitcnt vmcnt(8)
	s_waitcnt lgkmcnt(0)
	s_barrier
	v_mfma_f32_16x16x128_f8f6f4 v[96:99], v[26:33], v[178:185], 0
	s_setprio 1
	v_mfma_f32_16x16x128_f8f6f4 v[92:95], v[18:25], v[178:185], 0
	v_mfma_f32_16x16x128_f8f6f4 v[84:87], v[18:25], v[208:215], 0
	v_mfma_f32_16x16x128_f8f6f4 v[88:91], v[26:33], v[208:215], 0
	v_mfma_f32_16x16x128_f8f6f4 v[80:83], v[26:33], v[222:229], 0
	v_mfma_f32_16x16x128_f8f6f4 v[76:79], v[18:25], v[222:229], 0
	v_mfma_f32_16x16x128_f8f6f4 v[68:71], v[18:25], v[230:237], 0
	v_mfma_f32_16x16x128_f8f6f4 v[72:75], v[26:33], v[230:237], 0
	s_setprio 0
	s_setprio 1
	v_mfma_f32_16x16x128_f8f6f4 v[64:67], v[10:17], v[178:185], 0
	v_mfma_f32_16x16x128_f8f6f4 v[60:63], v[2:9], v[178:185], 0
	v_mfma_f32_16x16x128_f8f6f4 v[52:55], v[2:9], v[208:215], 0
	v_mfma_f32_16x16x128_f8f6f4 v[56:59], v[10:17], v[208:215], 0
	v_mfma_f32_16x16x128_f8f6f4 v[48:51], v[10:17], v[222:229], 0
	v_mfma_f32_16x16x128_f8f6f4 v[44:47], v[2:9], v[222:229], 0
	v_mfma_f32_16x16x128_f8f6f4 v[36:39], v[2:9], v[230:237], 0
	v_mfma_f32_16x16x128_f8f6f4 v[40:43], v[10:17], v[230:237], 0
	s_barrier
	s_setprio 0
	s_add_i32 s50, 0, 0x18000
	s_add_i32 s63, 0, 0x1c000
	v_add_u32_e32 v207, s50, v167
	v_add_u32_e32 v208, s63, v167
	ds_read_b128 v[26:29], v207
	ds_read_b128 v[30:33], v207 offset:1024
	ds_read_b128 v[18:21], v207 offset:2048
	ds_read_b128 v[22:25], v207 offset:3072
	ds_read_b128 v[10:13], v208
	ds_read_b128 v[14:17], v208 offset:1024
	ds_read_b128 v[2:5], v208 offset:2048
	ds_read_b128 v[6:9], v208 offset:3072
	s_add_u32 s6, s42, 0x70100
	s_addc_u32 s7, s43, 0
	s_mov_b32 m0, s74
	v_lshl_add_u64 v[218:219], s[6:7], 0, v[174:175]
	ds_read_b128 v[178:181], v189 offset:32768
	ds_read_b128 v[182:185], v189 offset:33792
	ds_read_b128 v[210:213], v189 offset:34816
	ds_read_b128 v[214:217], v189 offset:35840
	ds_read_b128 v[222:225], v189 offset:36864
	ds_read_b128 v[226:229], v189 offset:37888
	ds_read_b128 v[230:233], v189 offset:38912
	ds_read_b128 v[234:237], v189 offset:39936
	global_load_lds_dwordx4 v[218:219], off
	v_lshl_add_u64 v[218:219], s[6:7], 0, v[170:171]
	s_mov_b32 m0, s75
	s_nop 0
	global_load_lds_dwordx4 v[218:219], off
	s_waitcnt vmcnt(8)
	s_waitcnt lgkmcnt(0)
	s_barrier
	v_mfma_f32_16x16x128_f8f6f4 v[160:163], v[26:33], v[178:185], v[160:163]
	s_setprio 1
	v_mfma_f32_16x16x128_f8f6f4 v[156:159], v[18:25], v[178:185], v[156:159]
	v_mfma_f32_16x16x128_f8f6f4 v[148:151], v[18:25], v[210:217], v[148:151]
	v_mfma_f32_16x16x128_f8f6f4 v[152:155], v[26:33], v[210:217], v[152:155]
	v_mfma_f32_16x16x128_f8f6f4 v[144:147], v[26:33], v[222:229], v[144:147]
	v_mfma_f32_16x16x128_f8f6f4 v[140:143], v[18:25], v[222:229], v[140:143]
	v_mfma_f32_16x16x128_f8f6f4 v[132:135], v[18:25], v[230:237], v[132:135]
	v_mfma_f32_16x16x128_f8f6f4 v[136:139], v[26:33], v[230:237], v[136:139]
	s_setprio 0
	s_setprio 1
	v_mfma_f32_16x16x128_f8f6f4 v[128:131], v[10:17], v[178:185], v[128:131]
	v_mfma_f32_16x16x128_f8f6f4 v[124:127], v[2:9], v[178:185], v[124:127]
	v_mfma_f32_16x16x128_f8f6f4 v[116:119], v[2:9], v[210:217], v[116:119]
	v_mfma_f32_16x16x128_f8f6f4 v[120:123], v[10:17], v[210:217], v[120:123]
	v_mfma_f32_16x16x128_f8f6f4 v[112:115], v[10:17], v[222:229], v[112:115]
	v_mfma_f32_16x16x128_f8f6f4 v[108:111], v[2:9], v[222:229], v[108:111]
	v_mfma_f32_16x16x128_f8f6f4 v[100:103], v[2:9], v[230:237], v[100:103]
	v_mfma_f32_16x16x128_f8f6f4 v[104:107], v[10:17], v[230:237], v[104:107]
	s_barrier
	s_setprio 0
	s_mov_b64 s[6:7], 0x180
	s_add_i32 s50, s50, s71
	v_lshl_add_u64 v[198:199], v[198:199], 0, s[6:7]
	s_mov_b32 m0, s50
	s_add_i32 s51, s50, 0x2000
	ds_read_b128 v[178:181], v189 offset:49152
	ds_read_b128 v[182:185], v189 offset:50176
	ds_read_b128 v[210:213], v189 offset:51200
	ds_read_b128 v[214:217], v189 offset:52224
	ds_read_b128 v[222:225], v189 offset:53248
	ds_read_b128 v[226:229], v189 offset:54272
	ds_read_b128 v[230:233], v189 offset:55296
	ds_read_b128 v[234:237], v189 offset:56320
	global_load_lds_dwordx4 v[198:199], off
	v_lshl_add_u64 v[198:199], v[200:201], 0, s[6:7]
	s_mov_b32 m0, s51
	s_add_i32 s63, s63, s71
	global_load_lds_dwordx4 v[198:199], off
	v_lshl_add_u64 v[198:199], v[196:197], 0, s[26:27]
	v_lshl_add_u64 v[200:201], v[198:199], 0, v[172:173]
	s_mov_b32 m0, s63
	s_add_i32 s64, s63, 0x2000
	global_load_lds_dwordx4 v[200:201], off
	v_lshl_add_u64 v[198:199], v[198:199], 0, v[168:169]
	s_mov_b32 m0, s64
	s_nop 0
	global_load_lds_dwordx4 v[198:199], off
	v_lshl_add_u64 v[198:199], v[202:203], 0, s[6:7]
	s_mov_b32 m0, s77
	s_nop 0
	global_load_lds_dwordx4 v[198:199], off
	v_lshl_add_u64 v[198:199], v[204:205], 0, s[6:7]
	s_mov_b32 m0, s78
	s_nop 0
	global_load_lds_dwordx4 v[198:199], off
	s_waitcnt vmcnt(8)
	s_waitcnt lgkmcnt(0)
	s_barrier
	v_mfma_f32_16x16x128_f8f6f4 v[96:99], v[26:33], v[178:185], v[96:99]
	s_setprio 1
	v_mfma_f32_16x16x128_f8f6f4 v[92:95], v[18:25], v[178:185], v[92:95]
	v_mfma_f32_16x16x128_f8f6f4 v[84:87], v[18:25], v[210:217], v[84:87]
	v_mfma_f32_16x16x128_f8f6f4 v[88:91], v[26:33], v[210:217], v[88:91]
	v_mfma_f32_16x16x128_f8f6f4 v[80:83], v[26:33], v[222:229], v[80:83]
	v_mfma_f32_16x16x128_f8f6f4 v[76:79], v[18:25], v[222:229], v[76:79]
	v_mfma_f32_16x16x128_f8f6f4 v[68:71], v[18:25], v[230:237], v[68:71]
	v_mfma_f32_16x16x128_f8f6f4 v[72:75], v[26:33], v[230:237], v[72:75]
	s_setprio 0
	s_setprio 1
	v_mfma_f32_16x16x128_f8f6f4 v[64:67], v[10:17], v[178:185], v[64:67]
	v_mfma_f32_16x16x128_f8f6f4 v[60:63], v[2:9], v[178:185], v[60:63]
	v_mfma_f32_16x16x128_f8f6f4 v[52:55], v[2:9], v[210:217], v[52:55]
	v_mfma_f32_16x16x128_f8f6f4 v[56:59], v[10:17], v[210:217], v[56:59]
	v_mfma_f32_16x16x128_f8f6f4 v[48:51], v[10:17], v[222:229], v[48:51]
	v_mfma_f32_16x16x128_f8f6f4 v[44:47], v[2:9], v[222:229], v[44:47]
	v_mfma_f32_16x16x128_f8f6f4 v[36:39], v[2:9], v[230:237], v[36:39]
	v_mfma_f32_16x16x128_f8f6f4 v[40:43], v[10:17], v[230:237], v[40:43]
	s_barrier
	s_setprio 0
	s_mov_b64 s[6:7], 0x200
	v_lshl_add_u64 v[18:19], v[196:197], 0, s[6:7]
	s_mov_b32 s86, 0
.LBB0_900:
	ds_read_b128 v[2:5], v34
	ds_read_b128 v[6:9], v34 offset:1024
	ds_read_b128 v[10:13], v34 offset:2048
	ds_read_b128 v[14:17], v34 offset:3072
	ds_read_b128 v[178:181], v206
	ds_read_b128 v[182:185], v206 offset:1024
	ds_read_b128 v[196:199], v206 offset:2048
	ds_read_b128 v[200:203], v206 offset:3072
	s_add_u32 s6, s42, 0x200
	s_addc_u32 s7, s43, 0
	s_cmp_eq_u32 s86, 24
	s_cselect_b64 vcc, -1, 0
	s_cselect_b32 s7, s52, s7
	s_cselect_b32 s6, s53, s6
	v_cndmask_b32_e32 v21, v19, v195, vcc
	v_cndmask_b32_e32 v20, v18, v194, vcc
	s_mov_b32 m0, s84
	v_lshl_add_u64 v[30:31], s[42:43], 0, v[190:191]
	ds_read_b128 v[22:25], v189
	ds_read_b128 v[26:29], v189 offset:1024
	ds_read_b128 v[210:213], v189 offset:2048
	ds_read_b128 v[214:217], v189 offset:3072
	ds_read_b128 v[222:225], v189 offset:4096
	ds_read_b128 v[226:229], v189 offset:5120
	ds_read_b128 v[230:233], v189 offset:6144
	ds_read_b128 v[234:237], v189 offset:7168
	global_load_lds_dwordx4 v[30:31], off
	v_lshl_add_u64 v[30:31], s[42:43], 0, v[192:193]
	s_mov_b32 m0, s85
	s_nop 0
	global_load_lds_dwordx4 v[30:31], off
	s_waitcnt vmcnt(8)
	s_waitcnt lgkmcnt(0)
	s_barrier
	v_mfma_f32_16x16x128_f8f6f4 v[160:163], v[2:9], v[22:29], v[160:163]
	s_setprio 1
	v_mfma_f32_16x16x128_f8f6f4 v[156:159], v[10:17], v[22:29], v[156:159]
	v_mfma_f32_16x16x128_f8f6f4 v[148:151], v[10:17], v[210:217], v[148:151]
	v_mfma_f32_16x16x128_f8f6f4 v[152:155], v[2:9], v[210:217], v[152:155]
	v_mfma_f32_16x16x128_f8f6f4 v[144:147], v[2:9], v[222:229], v[144:147]
	v_mfma_f32_16x16x128_f8f6f4 v[140:143], v[10:17], v[222:229], v[140:143]
	v_mfma_f32_16x16x128_f8f6f4 v[132:135], v[10:17], v[230:237], v[132:135]
	v_mfma_f32_16x16x128_f8f6f4 v[136:139], v[2:9], v[230:237], v[136:139]
	s_setprio 0
	s_setprio 1
	v_mfma_f32_16x16x128_f8f6f4 v[128:131], v[178:185], v[22:29], v[128:131]
	v_mfma_f32_16x16x128_f8f6f4 v[124:127], v[196:203], v[22:29], v[124:127]
	v_mfma_f32_16x16x128_f8f6f4 v[116:119], v[196:203], v[210:217], v[116:119]
	v_mfma_f32_16x16x128_f8f6f4 v[120:123], v[178:185], v[210:217], v[120:123]
	v_mfma_f32_16x16x128_f8f6f4 v[112:115], v[178:185], v[222:229], v[112:115]
	v_mfma_f32_16x16x128_f8f6f4 v[108:111], v[196:203], v[222:229], v[108:111]
	v_mfma_f32_16x16x128_f8f6f4 v[100:103], v[196:203], v[230:237], v[100:103]
	v_mfma_f32_16x16x128_f8f6f4 v[104:107], v[178:185], v[230:237], v[104:107]
	s_barrier
	s_setprio 0
	s_mov_b32 m0, s54
	v_lshl_add_u64 v[22:23], v[20:21], 0, v[172:173]
	ds_read_b128 v[210:213], v189 offset:16384
	ds_read_b128 v[214:217], v189 offset:17408
	ds_read_b128 v[222:225], v189 offset:18432
	ds_read_b128 v[226:229], v189 offset:19456
	ds_read_b128 v[230:233], v189 offset:20480
	ds_read_b128 v[234:237], v189 offset:21504
	ds_read_b128 v[238:241], v189 offset:22528
	ds_read_b128 v[242:245], v189 offset:23552
	global_load_lds_dwordx4 v[22:23], off
	v_lshl_add_u64 v[24:25], v[20:21], 0, v[168:169]
	s_mov_b32 m0, s55
	v_lshl_add_u64 v[26:27], v[20:21], 0, s[2:3]
	global_load_lds_dwordx4 v[24:25], off
	v_lshl_add_u64 v[28:29], v[26:27], 0, v[172:173]
	s_mov_b32 m0, s65
	v_lshl_add_u64 v[26:27], v[26:27], 0, v[168:169]
	global_load_lds_dwordx4 v[28:29], off
	s_mov_b32 m0, s67
	v_lshl_add_u64 v[28:29], s[6:7], 0, v[170:171]
	global_load_lds_dwordx4 v[26:27], off
	v_lshl_add_u64 v[26:27], s[6:7], 0, v[174:175]
	s_mov_b32 m0, s72
	s_nop 0
	global_load_lds_dwordx4 v[26:27], off
	s_mov_b32 m0, s73
	s_nop 0
	global_load_lds_dwordx4 v[28:29], off
	s_waitcnt vmcnt(8)
	s_waitcnt lgkmcnt(0)
	s_barrier
	v_mfma_f32_16x16x128_f8f6f4 v[96:99], v[2:9], v[210:217], v[96:99]
	s_setprio 1
	v_mfma_f32_16x16x128_f8f6f4 v[92:95], v[10:17], v[210:217], v[92:95]
	v_mfma_f32_16x16x128_f8f6f4 v[84:87], v[10:17], v[222:229], v[84:87]
	v_mfma_f32_16x16x128_f8f6f4 v[88:91], v[2:9], v[222:229], v[88:91]
	v_mfma_f32_16x16x128_f8f6f4 v[80:83], v[2:9], v[230:237], v[80:83]
	v_mfma_f32_16x16x128_f8f6f4 v[76:79], v[10:17], v[230:237], v[76:79]
	v_mfma_f32_16x16x128_f8f6f4 v[68:71], v[10:17], v[238:245], v[68:71]
	v_mfma_f32_16x16x128_f8f6f4 v[72:75], v[2:9], v[238:245], v[72:75]
	s_setprio 0
	s_setprio 1
	v_mfma_f32_16x16x128_f8f6f4 v[64:67], v[178:185], v[210:217], v[64:67]
	v_mfma_f32_16x16x128_f8f6f4 v[60:63], v[196:203], v[210:217], v[60:63]
	v_mfma_f32_16x16x128_f8f6f4 v[52:55], v[196:203], v[222:229], v[52:55]
	v_mfma_f32_16x16x128_f8f6f4 v[56:59], v[178:185], v[222:229], v[56:59]
	v_mfma_f32_16x16x128_f8f6f4 v[48:51], v[178:185], v[230:237], v[48:51]
	v_mfma_f32_16x16x128_f8f6f4 v[44:47], v[196:203], v[230:237], v[44:47]
	v_mfma_f32_16x16x128_f8f6f4 v[36:39], v[196:203], v[238:245], v[36:39]
	v_mfma_f32_16x16x128_f8f6f4 v[40:43], v[178:185], v[238:245], v[40:43]
	s_barrier
	s_setprio 0
	ds_read_b128 v[178:181], v207
	ds_read_b128 v[182:185], v207 offset:1024
	ds_read_b128 v[196:199], v207 offset:2048
	ds_read_b128 v[200:203], v207 offset:3072
	ds_read_b128 v[10:13], v208
	ds_read_b128 v[14:17], v208 offset:1024
	ds_read_b128 v[2:5], v208 offset:2048
	ds_read_b128 v[6:9], v208 offset:3072
	s_add_u32 s6, s6, 0x70000
	s_addc_u32 s7, s7, 0
	s_mov_b32 m0, s74
	v_lshl_add_u64 v[30:31], s[6:7], 0, v[174:175]
	ds_read_b128 v[210:213], v189 offset:32768
	ds_read_b128 v[214:217], v189 offset:33792
	ds_read_b128 v[222:225], v189 offset:34816
	ds_read_b128 v[226:229], v189 offset:35840
	ds_read_b128 v[230:233], v189 offset:36864
	ds_read_b128 v[234:237], v189 offset:37888
	ds_read_b128 v[238:241], v189 offset:38912
	ds_read_b128 v[242:245], v189 offset:39936
	global_load_lds_dwordx4 v[30:31], off
	v_lshl_add_u64 v[30:31], s[6:7], 0, v[170:171]
	s_mov_b32 m0, s75
	s_nop 0
	global_load_lds_dwordx4 v[30:31], off
	s_waitcnt vmcnt(8)
	s_waitcnt lgkmcnt(0)
	s_barrier
	v_mfma_f32_16x16x128_f8f6f4 v[160:163], v[178:185], v[210:217], v[160:163]
	s_setprio 1
	v_mfma_f32_16x16x128_f8f6f4 v[156:159], v[196:203], v[210:217], v[156:159]
	v_mfma_f32_16x16x128_f8f6f4 v[148:151], v[196:203], v[222:229], v[148:151]
	v_mfma_f32_16x16x128_f8f6f4 v[152:155], v[178:185], v[222:229], v[152:155]
	v_mfma_f32_16x16x128_f8f6f4 v[144:147], v[178:185], v[230:237], v[144:147]
	v_mfma_f32_16x16x128_f8f6f4 v[140:143], v[196:203], v[230:237], v[140:143]
	v_mfma_f32_16x16x128_f8f6f4 v[132:135], v[196:203], v[238:245], v[132:135]
	v_mfma_f32_16x16x128_f8f6f4 v[136:139], v[178:185], v[238:245], v[136:139]
	s_setprio 0
	s_setprio 1
	v_mfma_f32_16x16x128_f8f6f4 v[128:131], v[10:17], v[210:217], v[128:131]
	v_mfma_f32_16x16x128_f8f6f4 v[124:127], v[2:9], v[210:217], v[124:127]
	v_mfma_f32_16x16x128_f8f6f4 v[116:119], v[2:9], v[222:229], v[116:119]
	v_mfma_f32_16x16x128_f8f6f4 v[120:123], v[10:17], v[222:229], v[120:123]
	v_mfma_f32_16x16x128_f8f6f4 v[112:115], v[10:17], v[230:237], v[112:115]
	v_mfma_f32_16x16x128_f8f6f4 v[108:111], v[2:9], v[230:237], v[108:111]
	v_mfma_f32_16x16x128_f8f6f4 v[100:103], v[2:9], v[238:245], v[100:103]
	v_mfma_f32_16x16x128_f8f6f4 v[104:107], v[10:17], v[238:245], v[104:107]
	s_barrier
	s_setprio 0
	s_mov_b32 m0, s50
	v_lshl_add_u64 v[22:23], v[22:23], 0, s[18:19]
	ds_read_b128 v[210:213], v189 offset:49152
	ds_read_b128 v[214:217], v189 offset:50176
	ds_read_b128 v[222:225], v189 offset:51200
	ds_read_b128 v[226:229], v189 offset:52224
	ds_read_b128 v[230:233], v189 offset:53248
	ds_read_b128 v[234:237], v189 offset:54272
	ds_read_b128 v[238:241], v189 offset:55296
	ds_read_b128 v[242:245], v189 offset:56320
	global_load_lds_dwordx4 v[22:23], off
	v_lshl_add_u64 v[22:23], v[24:25], 0, s[18:19]
	s_mov_b32 m0, s51
	v_lshl_add_u64 v[20:21], v[20:21], 0, s[34:35]
	global_load_lds_dwordx4 v[22:23], off
	v_lshl_add_u64 v[22:23], v[20:21], 0, v[172:173]
	s_mov_b32 m0, s63
	v_lshl_add_u64 v[20:21], v[20:21], 0, v[168:169]
	global_load_lds_dwordx4 v[22:23], off
	s_mov_b32 m0, s64
	s_nop 0
	global_load_lds_dwordx4 v[20:21], off
	v_lshl_add_u64 v[20:21], v[26:27], 0, s[18:19]
	s_mov_b32 m0, s77
	s_nop 0
	global_load_lds_dwordx4 v[20:21], off
	v_lshl_add_u64 v[20:21], v[28:29], 0, s[18:19]
	s_mov_b32 m0, s78
	s_nop 0
	global_load_lds_dwordx4 v[20:21], off
	s_waitcnt vmcnt(8)
	s_waitcnt lgkmcnt(0)
	s_barrier
	v_mfma_f32_16x16x128_f8f6f4 v[96:99], v[178:185], v[210:217], v[96:99]
	s_setprio 1
	v_mfma_f32_16x16x128_f8f6f4 v[92:95], v[196:203], v[210:217], v[92:95]
	v_mfma_f32_16x16x128_f8f6f4 v[84:87], v[196:203], v[222:229], v[84:87]
	v_mfma_f32_16x16x128_f8f6f4 v[88:91], v[178:185], v[222:229], v[88:91]
	v_mfma_f32_16x16x128_f8f6f4 v[80:83], v[178:185], v[230:237], v[80:83]
	v_mfma_f32_16x16x128_f8f6f4 v[76:79], v[196:203], v[230:237], v[76:79]
	v_mfma_f32_16x16x128_f8f6f4 v[68:71], v[196:203], v[238:245], v[68:71]
	v_mfma_f32_16x16x128_f8f6f4 v[72:75], v[178:185], v[238:245], v[72:75]
	s_setprio 0
	s_setprio 1
	v_mfma_f32_16x16x128_f8f6f4 v[64:67], v[10:17], v[210:217], v[64:67]
	v_mfma_f32_16x16x128_f8f6f4 v[60:63], v[2:9], v[210:217], v[60:63]
	v_mfma_f32_16x16x128_f8f6f4 v[52:55], v[2:9], v[222:229], v[52:55]
	v_mfma_f32_16x16x128_f8f6f4 v[56:59], v[10:17], v[222:229], v[56:59]
	v_mfma_f32_16x16x128_f8f6f4 v[48:51], v[10:17], v[230:237], v[48:51]
	v_mfma_f32_16x16x128_f8f6f4 v[44:47], v[2:9], v[230:237], v[44:47]
	v_mfma_f32_16x16x128_f8f6f4 v[36:39], v[2:9], v[238:245], v[36:39]
	v_mfma_f32_16x16x128_f8f6f4 v[40:43], v[10:17], v[238:245], v[40:43]
	s_barrier
	s_setprio 0
	s_add_i32 s86, s86, 2
	s_add_u32 s42, s42, 0x100
	s_addc_u32 s43, s43, 0
	s_cmp_gt_u32 s86, 25
	v_lshl_add_u64 v[18:19], v[18:19], 0, s[28:29]
	s_cbranch_scc0 .LBB0_900
	s_and_b64 vcc, exec, s[36:37]
	s_mov_b64 s[84:85], s[24:25]
	s_cbranch_vccz .LBB0_903
	s_barrier

.LBB0_953:
	s_add_u32 s95, s30, 0x200
	s_addc_u32 s96, s31, 0
	s_add_i32 s65, 0, 0x14000
	s_add_i32 s67, 0, 0x10000
	v_add_u32_e32 v199, s65, v167
	v_add_u32_e32 v200, s67, v167
	ds_read_b128 v[10:13], v199
	ds_read_b128 v[14:17], v199 offset:1024
	ds_read_b128 v[2:5], v199 offset:2048
	ds_read_b128 v[6:9], v199 offset:3072
	ds_read_b128 v[22:25], v200 offset:3072
	ds_read_b128 v[18:21], v200 offset:2048
	ds_read_b128 v[30:33], v200 offset:1024
	ds_read_b128 v[26:29], v200
	s_lshl_b32 s14, s94, 10
	s_add_i32 s97, s14, 0
	s_add_i32 s97, s97, 0x20400
	v_mov_b32_e32 v191, v35
	v_mov_b32_e32 v175, v35
	s_add_i32 s83, s52, 0xc000
	v_readlane_b32 s26, v253, 28
	s_mov_b32 m0, s83
	v_readlane_b32 s27, v253, 29
	s_add_i32 s53, s52, 0xe000
	ds_read_b128 v[178:181], v169
	ds_read_b128 v[182:185], v169 offset:1024
	ds_read_b128 v[202:205], v169 offset:2048
	ds_read_b128 v[206:209], v169 offset:3072
	ds_read_b128 v[210:213], v169 offset:4096
	ds_read_b128 v[214:217], v169 offset:5120
	ds_read_b128 v[222:225], v169 offset:6144
	ds_read_b128 v[226:229], v169 offset:7168
	global_load_lds_dwordx4 v190, s[26:27]
	s_mov_b32 m0, s53
	s_nop 0
	global_load_lds_dwordx4 v174, s[26:27]
	s_waitcnt vmcnt(8)
	s_waitcnt lgkmcnt(0)
	s_barrier
	v_mfma_f32_16x16x128_f8f6f4 v[160:163], v[26:33], v[178:185], 0
	s_setprio 1
	v_mfma_f32_16x16x128_f8f6f4 v[156:159], v[18:25], v[178:185], 0
	v_mfma_f32_16x16x128_f8f6f4 v[148:151], v[18:25], v[202:209], 0
	v_mfma_f32_16x16x128_f8f6f4 v[152:155], v[26:33], v[202:209], 0
	v_mfma_f32_16x16x128_f8f6f4 v[144:147], v[26:33], v[210:217], 0
	v_mfma_f32_16x16x128_f8f6f4 v[140:143], v[18:25], v[210:217], 0
	v_mfma_f32_16x16x128_f8f6f4 v[132:135], v[18:25], v[222:229], 0
	v_mfma_f32_16x16x128_f8f6f4 v[136:139], v[26:33], v[222:229], 0
	s_setprio 0
	s_setprio 1
	v_mfma_f32_16x16x128_f8f6f4 v[128:131], v[10:17], v[178:185], 0
	v_mfma_f32_16x16x128_f8f6f4 v[124:127], v[2:9], v[178:185], 0
	v_mfma_f32_16x16x128_f8f6f4 v[116:119], v[2:9], v[202:209], 0
	v_mfma_f32_16x16x128_f8f6f4 v[120:123], v[10:17], v[202:209], 0
	v_mfma_f32_16x16x128_f8f6f4 v[112:115], v[10:17], v[210:217], 0
	v_mfma_f32_16x16x128_f8f6f4 v[108:111], v[2:9], v[210:217], 0
	v_mfma_f32_16x16x128_f8f6f4 v[100:103], v[2:9], v[222:229], 0
	v_mfma_f32_16x16x128_f8f6f4 v[104:107], v[10:17], v[222:229], 0
	s_barrier
	s_setprio 0
	v_lshl_add_u64 v[194:195], s[30:31], 0, v[170:171]
	s_add_i32 s67, s67, s82
	v_lshl_add_u64 v[196:197], v[194:195], 0, s[28:29]
	s_mov_b32 m0, s67
	s_add_i32 s55, s67, 0x2000
	ds_read_b128 v[178:181], v169 offset:16384
	ds_read_b128 v[182:185], v169 offset:17408
	ds_read_b128 v[202:205], v169 offset:18432
	ds_read_b128 v[206:209], v169 offset:19456
	ds_read_b128 v[210:213], v169 offset:20480
	ds_read_b128 v[214:217], v169 offset:21504
	ds_read_b128 v[222:225], v169 offset:22528
	ds_read_b128 v[226:229], v169 offset:23552
	global_load_lds_dwordx4 v[196:197], off
	v_lshl_add_u64 v[196:197], s[30:31], 0, v[172:173]
	s_add_u32 s46, s30, 0x20100
	v_lshl_add_u64 v[218:219], v[196:197], 0, s[28:29]
	s_mov_b32 m0, s55
	s_addc_u32 s47, s31, 0
	s_add_i32 s65, s65, s82
	global_load_lds_dwordx4 v[218:219], off
	v_lshl_add_u64 v[218:219], s[46:47], 0, v[170:171]
	s_mov_b32 m0, s65
	s_add_i32 s54, s65, 0x2000
	global_load_lds_dwordx4 v[218:219], off
	v_lshl_add_u64 v[218:219], s[46:47], 0, v[172:173]
	s_mov_b32 m0, s54
	v_readlane_b32 s26, v253, 37
	global_load_lds_dwordx4 v[218:219], off
	s_mov_b32 m0, s52
	v_readlane_b32 s27, v253, 38
	s_nop 4
	global_load_lds_dwordx4 v34, s[26:27]
	s_mov_b32 m0, s84
	s_nop 0
	global_load_lds_dwordx4 v192, s[26:27]
	s_waitcnt vmcnt(8)
	s_waitcnt lgkmcnt(0)
	s_barrier
	v_mfma_f32_16x16x128_f8f6f4 v[96:99], v[26:33], v[178:185], 0
	s_setprio 1
	v_mfma_f32_16x16x128_f8f6f4 v[92:95], v[18:25], v[178:185], 0
	v_mfma_f32_16x16x128_f8f6f4 v[84:87], v[18:25], v[202:209], 0
	v_mfma_f32_16x16x128_f8f6f4 v[88:91], v[26:33], v[202:209], 0
	v_mfma_f32_16x16x128_f8f6f4 v[80:83], v[26:33], v[210:217], 0
	v_mfma_f32_16x16x128_f8f6f4 v[76:79], v[18:25], v[210:217], 0
	v_mfma_f32_16x16x128_f8f6f4 v[68:71], v[18:25], v[222:229], 0
	v_mfma_f32_16x16x128_f8f6f4 v[72:75], v[26:33], v[222:229], 0
	s_setprio 0
	s_setprio 1
	v_mfma_f32_16x16x128_f8f6f4 v[64:67], v[10:17], v[178:185], 0
	v_mfma_f32_16x16x128_f8f6f4 v[60:63], v[2:9], v[178:185], 0
	v_mfma_f32_16x16x128_f8f6f4 v[52:55], v[2:9], v[202:209], 0
	v_mfma_f32_16x16x128_f8f6f4 v[56:59], v[10:17], v[202:209], 0
	v_mfma_f32_16x16x128_f8f6f4 v[48:51], v[10:17], v[210:217], 0
	v_mfma_f32_16x16x128_f8f6f4 v[44:47], v[2:9], v[210:217], 0
	v_mfma_f32_16x16x128_f8f6f4 v[36:39], v[2:9], v[222:229], 0
	v_mfma_f32_16x16x128_f8f6f4 v[40:43], v[10:17], v[222:229], 0
	s_barrier
	s_setprio 0
	s_add_i32 s50, 0, 0x18000
	s_add_i32 s64, 0, 0x1c000
	v_add_u32_e32 v201, s50, v167
	v_add_u32_e32 v202, s64, v167
	ds_read_b128 v[26:29], v201
	ds_read_b128 v[30:33], v201 offset:1024
	ds_read_b128 v[18:21], v201 offset:2048
	ds_read_b128 v[22:25], v201 offset:3072
	ds_read_b128 v[10:13], v202
	ds_read_b128 v[14:17], v202 offset:1024
	ds_read_b128 v[2:5], v202 offset:2048
	ds_read_b128 v[6:9], v202 offset:3072
	s_mov_b32 m0, s85
	ds_read_b128 v[178:181], v169 offset:32768
	ds_read_b128 v[182:185], v169 offset:33792
	ds_read_b128 v[204:207], v169 offset:34816
	ds_read_b128 v[208:211], v169 offset:35840
	ds_read_b128 v[212:215], v169 offset:36864
	ds_read_b128 v[216:219], v169 offset:37888
	ds_read_b128 v[222:225], v169 offset:38912
	ds_read_b128 v[226:229], v169 offset:39936
	global_load_lds_dwordx4 v189, s[26:27]
	s_mov_b32 m0, s86
	s_nop 0
	global_load_lds_dwordx4 v198, s[26:27]
	s_waitcnt vmcnt(8)
	s_waitcnt lgkmcnt(0)
	s_barrier
	v_mfma_f32_16x16x128_f8f6f4 v[160:163], v[26:33], v[178:185], v[160:163]
	s_setprio 1
	v_mfma_f32_16x16x128_f8f6f4 v[156:159], v[18:25], v[178:185], v[156:159]
	v_mfma_f32_16x16x128_f8f6f4 v[148:151], v[18:25], v[204:211], v[148:151]
	v_mfma_f32_16x16x128_f8f6f4 v[152:155], v[26:33], v[204:211], v[152:155]
	v_mfma_f32_16x16x128_f8f6f4 v[144:147], v[26:33], v[212:219], v[144:147]
	v_mfma_f32_16x16x128_f8f6f4 v[140:143], v[18:25], v[212:219], v[140:143]
	v_mfma_f32_16x16x128_f8f6f4 v[132:135], v[18:25], v[222:229], v[132:135]
	v_mfma_f32_16x16x128_f8f6f4 v[136:139], v[26:33], v[222:229], v[136:139]
	s_setprio 0
	s_setprio 1
	v_mfma_f32_16x16x128_f8f6f4 v[128:131], v[10:17], v[178:185], v[128:131]
	v_mfma_f32_16x16x128_f8f6f4 v[124:127], v[2:9], v[178:185], v[124:127]
	v_mfma_f32_16x16x128_f8f6f4 v[116:119], v[2:9], v[204:211], v[116:119]
	v_mfma_f32_16x16x128_f8f6f4 v[120:123], v[10:17], v[204:211], v[120:123]
	v_mfma_f32_16x16x128_f8f6f4 v[112:115], v[10:17], v[212:219], v[112:115]
	v_mfma_f32_16x16x128_f8f6f4 v[108:111], v[2:9], v[212:219], v[108:111]
	v_mfma_f32_16x16x128_f8f6f4 v[100:103], v[2:9], v[222:229], v[100:103]
	v_mfma_f32_16x16x128_f8f6f4 v[104:107], v[10:17], v[222:229], v[104:107]
	s_barrier
	s_setprio 0
	s_add_i32 s50, s50, s82
	s_mov_b64 s[26:27], 0x180
	s_add_i32 s51, s50, 0x2000
	v_lshl_add_u64 v[194:195], v[194:195], 0, s[26:27]
	s_mov_b32 m0, s50
	s_add_u32 s30, s30, 0x20180
	ds_read_b128 v[178:181], v169 offset:49152
	ds_read_b128 v[182:185], v169 offset:50176
	ds_read_b128 v[204:207], v169 offset:51200
	ds_read_b128 v[208:211], v169 offset:52224
	ds_read_b128 v[212:215], v169 offset:53248
	ds_read_b128 v[216:219], v169 offset:54272
	ds_read_b128 v[222:225], v169 offset:55296
	ds_read_b128 v[226:229], v169 offset:56320
	global_load_lds_dwordx4 v[194:195], off
	v_lshl_add_u64 v[194:195], v[196:197], 0, s[26:27]
	s_mov_b32 m0, s51
	s_addc_u32 s31, s31, 0
	s_add_i32 s64, s64, s82
	global_load_lds_dwordx4 v[194:195], off
	v_lshl_add_u64 v[194:195], s[30:31], 0, v[170:171]
	s_mov_b32 m0, s64
	s_add_i32 s63, s64, 0x2000
	global_load_lds_dwordx4 v[194:195], off
	v_lshl_add_u64 v[194:195], s[30:31], 0, v[172:173]
	s_mov_b32 m0, s63
	v_readlane_b32 s26, v253, 39
	global_load_lds_dwordx4 v[194:195], off
	s_mov_b32 m0, s90
	v_readlane_b32 s27, v253, 40
	s_nop 4
	global_load_lds_dwordx4 v34, s[26:27]
	s_mov_b32 m0, s91
	s_nop 0
	global_load_lds_dwordx4 v192, s[26:27]
	s_waitcnt vmcnt(8)
	s_waitcnt lgkmcnt(0)
	s_barrier
	v_mfma_f32_16x16x128_f8f6f4 v[96:99], v[26:33], v[178:185], v[96:99]
	s_setprio 1
	v_mfma_f32_16x16x128_f8f6f4 v[92:95], v[18:25], v[178:185], v[92:95]
	v_mfma_f32_16x16x128_f8f6f4 v[84:87], v[18:25], v[204:211], v[84:87]
	v_mfma_f32_16x16x128_f8f6f4 v[88:91], v[26:33], v[204:211], v[88:91]
	v_mfma_f32_16x16x128_f8f6f4 v[80:83], v[26:33], v[212:219], v[80:83]
	v_mfma_f32_16x16x128_f8f6f4 v[76:79], v[18:25], v[212:219], v[76:79]
	v_mfma_f32_16x16x128_f8f6f4 v[68:71], v[18:25], v[222:229], v[68:71]
	v_mfma_f32_16x16x128_f8f6f4 v[72:75], v[26:33], v[222:229], v[72:75]
	s_setprio 0
	s_setprio 1
	v_mfma_f32_16x16x128_f8f6f4 v[64:67], v[10:17], v[178:185], v[64:67]
	v_mfma_f32_16x16x128_f8f6f4 v[60:63], v[2:9], v[178:185], v[60:63]
	v_mfma_f32_16x16x128_f8f6f4 v[52:55], v[2:9], v[204:211], v[52:55]
	v_mfma_f32_16x16x128_f8f6f4 v[56:59], v[10:17], v[204:211], v[56:59]
	v_mfma_f32_16x16x128_f8f6f4 v[48:51], v[10:17], v[212:219], v[48:51]
	v_mfma_f32_16x16x128_f8f6f4 v[44:47], v[2:9], v[212:219], v[44:47]
	v_mfma_f32_16x16x128_f8f6f4 v[36:39], v[2:9], v[222:229], v[36:39]
	v_mfma_f32_16x16x128_f8f6f4 v[40:43], v[10:17], v[222:229], v[40:43]
	s_barrier
	s_setprio 0
	v_lshl_add_u64 v[18:19], s[26:27], 0, v[174:175]
	v_lshl_add_u64 v[20:21], s[26:27], 0, v[190:191]
	s_mov_b32 s75, 0
	s_mov_b64 s[30:31], 0
	s_branch .LBB0_955
.LBB0_954:
	ds_read_b128 v[178:181], v200
	ds_read_b128 v[182:185], v200 offset:1024
	ds_read_b128 v[204:207], v200 offset:2048
	ds_read_b128 v[208:211], v200 offset:3072
	ds_read_b128 v[10:13], v199
	ds_read_b128 v[14:17], v199 offset:1024
	ds_read_b128 v[2:5], v199 offset:2048
	ds_read_b128 v[6:9], v199 offset:3072
	s_add_u32 s14, s30, 0x200
	s_addc_u32 vcc_lo, s31, 0
	s_and_b64 s[48:49], s[46:47], exec
	s_cselect_b32 s14, 0, s14
	s_cselect_b32 s49, 0, vcc_lo
	s_add_u32 s48, s20, s14
	s_addc_u32 s49, s21, s49
	s_add_u32 s14, s95, s30
	s_addc_u32 vcc_lo, s96, s31
	s_and_b64 s[46:47], s[46:47], exec
	s_cselect_b32 s47, s43, vcc_lo
	s_cselect_b32 s46, s42, s14
	s_mov_b32 m0, s83
	v_lshl_add_u64 v[30:31], v[20:21], 0, s[30:31]
	ds_read_b128 v[22:25], v169
	ds_read_b128 v[26:29], v169 offset:1024
	ds_read_b128 v[212:215], v169 offset:2048
	ds_read_b128 v[216:219], v169 offset:3072
	ds_read_b128 v[222:225], v169 offset:4096
	ds_read_b128 v[226:229], v169 offset:5120
	ds_read_b128 v[230:233], v169 offset:6144
	ds_read_b128 v[234:237], v169 offset:7168
	global_load_lds_dwordx4 v[30:31], off
	v_lshl_add_u64 v[30:31], v[18:19], 0, s[30:31]
	s_mov_b32 m0, s53
	s_nop 0
	global_load_lds_dwordx4 v[30:31], off
	s_waitcnt vmcnt(8)
	s_waitcnt lgkmcnt(0)
	s_barrier
	v_mfma_f32_16x16x128_f8f6f4 v[160:163], v[178:185], v[22:29], v[160:163]
	s_setprio 1
	v_mfma_f32_16x16x128_f8f6f4 v[156:159], v[204:211], v[22:29], v[156:159]
	v_mfma_f32_16x16x128_f8f6f4 v[148:151], v[204:211], v[212:219], v[148:151]
	v_mfma_f32_16x16x128_f8f6f4 v[152:155], v[178:185], v[212:219], v[152:155]
	v_mfma_f32_16x16x128_f8f6f4 v[144:147], v[178:185], v[222:229], v[144:147]
	v_mfma_f32_16x16x128_f8f6f4 v[140:143], v[204:211], v[222:229], v[140:143]
	v_mfma_f32_16x16x128_f8f6f4 v[132:135], v[204:211], v[230:237], v[132:135]
	v_mfma_f32_16x16x128_f8f6f4 v[136:139], v[178:185], v[230:237], v[136:139]
	s_setprio 0
	s_setprio 1
	v_mfma_f32_16x16x128_f8f6f4 v[128:131], v[10:17], v[22:29], v[128:131]
	v_mfma_f32_16x16x128_f8f6f4 v[124:127], v[2:9], v[22:29], v[124:127]
	v_mfma_f32_16x16x128_f8f6f4 v[116:119], v[2:9], v[212:219], v[116:119]
	v_mfma_f32_16x16x128_f8f6f4 v[120:123], v[10:17], v[212:219], v[120:123]
	v_mfma_f32_16x16x128_f8f6f4 v[112:115], v[10:17], v[222:229], v[112:115]
	v_mfma_f32_16x16x128_f8f6f4 v[108:111], v[2:9], v[222:229], v[108:111]
	v_mfma_f32_16x16x128_f8f6f4 v[100:103], v[2:9], v[230:237], v[100:103]
	v_mfma_f32_16x16x128_f8f6f4 v[104:107], v[10:17], v[230:237], v[104:107]
	s_barrier
	s_setprio 0
	s_mov_b32 m0, s67
	v_lshl_add_u64 v[22:23], s[46:47], 0, v[170:171]
	s_add_u32 vcc_lo, s46, 0x20000
	ds_read_b128 v[212:215], v169 offset:16384
	ds_read_b128 v[216:219], v169 offset:17408
	ds_read_b128 v[222:225], v169 offset:18432
	ds_read_b128 v[226:229], v169 offset:19456
	ds_read_b128 v[230:233], v169 offset:20480
	ds_read_b128 v[234:237], v169 offset:21504
	ds_read_b128 v[238:241], v169 offset:22528
	ds_read_b128 v[242:245], v169 offset:23552
	global_load_lds_dwordx4 v[22:23], off
	v_lshl_add_u64 v[24:25], s[46:47], 0, v[172:173]
	s_mov_b32 m0, s55
	s_addc_u32 vcc_hi, s47, 0
	global_load_lds_dwordx4 v[24:25], off
	v_lshl_add_u64 v[26:27], vcc, 0, v[170:171]
	s_mov_b32 m0, s65
	v_mov_b32_e32 v193, v35
	global_load_lds_dwordx4 v[26:27], off
	v_lshl_add_u64 v[26:27], vcc, 0, v[172:173]
	s_mov_b32 m0, s54
	v_lshl_add_u64 v[28:29], s[48:49], 0, v[34:35]
	global_load_lds_dwordx4 v[26:27], off
	s_mov_b32 m0, s52
	v_lshl_add_u64 v[26:27], s[48:49], 0, v[192:193]
	global_load_lds_dwordx4 v34, s[48:49]
	s_mov_b32 m0, s84
	s_nop 0
	global_load_lds_dwordx4 v192, s[48:49]
	s_waitcnt vmcnt(8)
	s_waitcnt lgkmcnt(0)
	s_barrier
	v_mfma_f32_16x16x128_f8f6f4 v[96:99], v[178:185], v[212:219], v[96:99]
	s_setprio 1
	v_mfma_f32_16x16x128_f8f6f4 v[92:95], v[204:211], v[212:219], v[92:95]
	v_mfma_f32_16x16x128_f8f6f4 v[84:87], v[204:211], v[222:229], v[84:87]
	v_mfma_f32_16x16x128_f8f6f4 v[88:91], v[178:185], v[222:229], v[88:91]
	v_mfma_f32_16x16x128_f8f6f4 v[80:83], v[178:185], v[230:237], v[80:83]
	v_mfma_f32_16x16x128_f8f6f4 v[76:79], v[204:211], v[230:237], v[76:79]
	v_mfma_f32_16x16x128_f8f6f4 v[68:71], v[204:211], v[238:245], v[68:71]
	v_mfma_f32_16x16x128_f8f6f4 v[72:75], v[178:185], v[238:245], v[72:75]
	s_setprio 0
	s_setprio 1
	v_mfma_f32_16x16x128_f8f6f4 v[64:67], v[10:17], v[212:219], v[64:67]
	v_mfma_f32_16x16x128_f8f6f4 v[60:63], v[2:9], v[212:219], v[60:63]
	v_mfma_f32_16x16x128_f8f6f4 v[52:55], v[2:9], v[222:229], v[52:55]
	v_mfma_f32_16x16x128_f8f6f4 v[56:59], v[10:17], v[222:229], v[56:59]
	v_mfma_f32_16x16x128_f8f6f4 v[48:51], v[10:17], v[230:237], v[48:51]
	v_mfma_f32_16x16x128_f8f6f4 v[44:47], v[2:9], v[230:237], v[44:47]
	v_mfma_f32_16x16x128_f8f6f4 v[36:39], v[2:9], v[238:245], v[36:39]
	v_mfma_f32_16x16x128_f8f6f4 v[40:43], v[10:17], v[238:245], v[40:43]
	s_barrier
	s_setprio 0
	ds_read_b128 v[178:181], v201
	ds_read_b128 v[182:185], v201 offset:1024
	ds_read_b128 v[204:207], v201 offset:2048
	ds_read_b128 v[208:211], v201 offset:3072
	ds_read_b128 v[10:13], v202
	ds_read_b128 v[14:17], v202 offset:1024
	ds_read_b128 v[2:5], v202 offset:2048
	ds_read_b128 v[6:9], v202 offset:3072
	s_mov_b32 m0, s85
	ds_read_b128 v[212:215], v169 offset:32768
	ds_read_b128 v[216:219], v169 offset:33792
	ds_read_b128 v[222:225], v169 offset:34816
	ds_read_b128 v[226:229], v169 offset:35840
	ds_read_b128 v[230:233], v169 offset:36864
	ds_read_b128 v[234:237], v169 offset:37888
	ds_read_b128 v[238:241], v169 offset:38912
	ds_read_b128 v[242:245], v169 offset:39936
	global_load_lds_dwordx4 v189, s[48:49]
	s_mov_b32 m0, s86
	s_nop 0
	global_load_lds_dwordx4 v198, s[48:49]
	s_waitcnt vmcnt(8)
	s_waitcnt lgkmcnt(0)
	s_barrier
	v_mfma_f32_16x16x128_f8f6f4 v[160:163], v[178:185], v[212:219], v[160:163]
	s_setprio 1
	v_mfma_f32_16x16x128_f8f6f4 v[156:159], v[204:211], v[212:219], v[156:159]
	v_mfma_f32_16x16x128_f8f6f4 v[148:151], v[204:211], v[222:229], v[148:151]
	v_mfma_f32_16x16x128_f8f6f4 v[152:155], v[178:185], v[222:229], v[152:155]
	v_mfma_f32_16x16x128_f8f6f4 v[144:147], v[178:185], v[230:237], v[144:147]
	v_mfma_f32_16x16x128_f8f6f4 v[140:143], v[204:211], v[230:237], v[140:143]
	v_mfma_f32_16x16x128_f8f6f4 v[132:135], v[204:211], v[238:245], v[132:135]
	v_mfma_f32_16x16x128_f8f6f4 v[136:139], v[178:185], v[238:245], v[136:139]
	s_setprio 0
	s_setprio 1
	v_mfma_f32_16x16x128_f8f6f4 v[128:131], v[10:17], v[212:219], v[128:131]
	v_mfma_f32_16x16x128_f8f6f4 v[124:127], v[2:9], v[212:219], v[124:127]
	v_mfma_f32_16x16x128_f8f6f4 v[116:119], v[2:9], v[222:229], v[116:119]
	v_mfma_f32_16x16x128_f8f6f4 v[120:123], v[10:17], v[222:229], v[120:123]
	v_mfma_f32_16x16x128_f8f6f4 v[112:115], v[10:17], v[230:237], v[112:115]
	v_mfma_f32_16x16x128_f8f6f4 v[108:111], v[2:9], v[230:237], v[108:111]
	v_mfma_f32_16x16x128_f8f6f4 v[100:103], v[2:9], v[238:245], v[100:103]
	v_mfma_f32_16x16x128_f8f6f4 v[104:107], v[10:17], v[238:245], v[104:107]
	s_barrier
	s_setprio 0
	s_mov_b32 m0, s50
	v_lshl_add_u64 v[22:23], v[22:23], 0, s[18:19]
	s_add_u32 s46, s46, 0x20080
	ds_read_b128 v[212:215], v169 offset:49152
	ds_read_b128 v[216:219], v169 offset:50176
	ds_read_b128 v[222:225], v169 offset:51200
	ds_read_b128 v[226:229], v169 offset:52224
	ds_read_b128 v[230:233], v169 offset:53248
	ds_read_b128 v[234:237], v169 offset:54272
	ds_read_b128 v[238:241], v169 offset:55296
	ds_read_b128 v[242:245], v169 offset:56320
	global_load_lds_dwordx4 v[22:23], off
	v_lshl_add_u64 v[22:23], v[24:25], 0, s[18:19]
	s_mov_b32 m0, s51
	s_addc_u32 s47, s47, 0
	global_load_lds_dwordx4 v[22:23], off
	v_lshl_add_u64 v[22:23], s[46:47], 0, v[170:171]
	s_mov_b32 m0, s64
	s_nop 0
	global_load_lds_dwordx4 v[22:23], off
	v_lshl_add_u64 v[22:23], s[46:47], 0, v[172:173]
	s_mov_b32 m0, s63
	s_nop 0
	global_load_lds_dwordx4 v[22:23], off
	v_lshl_add_u64 v[22:23], v[28:29], 0, s[18:19]
	s_mov_b32 m0, s90
	s_nop 0
	global_load_lds_dwordx4 v[22:23], off
	v_lshl_add_u64 v[22:23], v[26:27], 0, s[18:19]
	s_mov_b32 m0, s91
	s_nop 0
	global_load_lds_dwordx4 v[22:23], off
	s_waitcnt vmcnt(8)
	s_waitcnt lgkmcnt(0)
	s_barrier
	v_mfma_f32_16x16x128_f8f6f4 v[96:99], v[178:185], v[212:219], v[96:99]
	s_setprio 1
	v_mfma_f32_16x16x128_f8f6f4 v[92:95], v[204:211], v[212:219], v[92:95]
	v_mfma_f32_16x16x128_f8f6f4 v[84:87], v[204:211], v[222:229], v[84:87]
	v_mfma_f32_16x16x128_f8f6f4 v[88:91], v[178:185], v[222:229], v[88:91]
	v_mfma_f32_16x16x128_f8f6f4 v[80:83], v[178:185], v[230:237], v[80:83]
	v_mfma_f32_16x16x128_f8f6f4 v[76:79], v[204:211], v[230:237], v[76:79]
	v_mfma_f32_16x16x128_f8f6f4 v[68:71], v[204:211], v[238:245], v[68:71]
	v_mfma_f32_16x16x128_f8f6f4 v[72:75], v[178:185], v[238:245], v[72:75]
	s_setprio 0
	s_setprio 1
	v_mfma_f32_16x16x128_f8f6f4 v[64:67], v[10:17], v[212:219], v[64:67]
	v_mfma_f32_16x16x128_f8f6f4 v[60:63], v[2:9], v[212:219], v[60:63]
	v_mfma_f32_16x16x128_f8f6f4 v[52:55], v[2:9], v[222:229], v[52:55]
	v_mfma_f32_16x16x128_f8f6f4 v[56:59], v[10:17], v[222:229], v[56:59]
	v_mfma_f32_16x16x128_f8f6f4 v[48:51], v[10:17], v[230:237], v[48:51]
	v_mfma_f32_16x16x128_f8f6f4 v[44:47], v[2:9], v[230:237], v[44:47]
	v_mfma_f32_16x16x128_f8f6f4 v[36:39], v[2:9], v[238:245], v[36:39]
	v_mfma_f32_16x16x128_f8f6f4 v[40:43], v[10:17], v[238:245], v[40:43]
	s_barrier
	s_setprio 0
	s_add_i32 s75, s75, 2
	s_add_u32 s30, s30, 0x100
	s_addc_u32 s31, s31, 0
	s_cmp_gt_u32 s75, 5
	s_cbranch_scc1 .LBB0_957

.LBB0_1086:
	s_lshl_b32 s10, s51, 18
	s_add_u32 s10, s20, s10
	s_addc_u32 s11, s21, 0
	s_and_b64 s[16:17], s[4:5], exec
	s_cselect_b32 s54, s11, s31
	s_cselect_b32 s55, s10, s30
	s_lshl_b32 s14, s50, 18
	s_add_u32 s16, s15, s14
	s_addc_u32 s17, s26, 0
	s_and_b64 s[36:37], s[4:5], exec
	s_cselect_b32 s56, s17, s23
	s_cselect_b32 s57, s16, s22
	s_add_i32 s60, 0, 0x10000
	s_add_i32 s62, 0, 0x14000
	v_add_u32_e32 v198, s60, v196
	v_add_u32_e32 v199, s62, v196
	ds_read_b128 v[26:29], v198
	ds_read_b128 v[30:33], v198 offset:1024
	ds_read_b128 v[18:21], v198 offset:2048
	ds_read_b128 v[22:25], v198 offset:3072
	ds_read_b128 v[10:13], v199
	ds_read_b128 v[14:17], v199 offset:1024
	ds_read_b128 v[2:5], v199 offset:2048
	ds_read_b128 v[6:9], v199 offset:3072
	s_add_u32 s36, s30, 0x20080
	s_addc_u32 s37, s31, 0
	s_add_i32 s58, s41, 0xc000
	v_lshl_add_u64 v[174:175], s[36:37], 0, v[168:169]
	s_mov_b32 m0, s58
	s_add_i32 s59, s41, 0xe000
	ds_read_b128 v[200:203], v197
	ds_read_b128 v[204:207], v197 offset:1024
	ds_read_b128 v[222:225], v197 offset:2048
	ds_read_b128 v[226:229], v197 offset:3072
	ds_read_b128 v[230:233], v197 offset:4096
	ds_read_b128 v[234:237], v197 offset:5120
	ds_read_b128 v[238:241], v197 offset:6144
	ds_read_b128 v[242:245], v197 offset:7168
	global_load_lds_dwordx4 v[174:175], off
	v_lshl_add_u64 v[174:175], s[36:37], 0, v[166:167]
	s_mov_b32 m0, s59
	s_nop 0
	global_load_lds_dwordx4 v[174:175], off
	s_waitcnt vmcnt(8)
	s_waitcnt lgkmcnt(0)
	s_barrier
	v_mfma_f32_16x16x128_f8f6f4 v[160:163], v[26:33], v[200:207], 0
	s_setprio 1
	v_mfma_f32_16x16x128_f8f6f4 v[156:159], v[18:25], v[200:207], 0
	v_mfma_f32_16x16x128_f8f6f4 v[148:151], v[18:25], v[222:229], 0
	v_mfma_f32_16x16x128_f8f6f4 v[152:155], v[26:33], v[222:229], 0
	v_mfma_f32_16x16x128_f8f6f4 v[144:147], v[26:33], v[230:237], 0
	v_mfma_f32_16x16x128_f8f6f4 v[140:143], v[18:25], v[230:237], 0
	v_mfma_f32_16x16x128_f8f6f4 v[132:135], v[18:25], v[238:245], 0
	v_mfma_f32_16x16x128_f8f6f4 v[136:139], v[26:33], v[238:245], 0
	s_setprio 0
	s_setprio 1
	v_mfma_f32_16x16x128_f8f6f4 v[128:131], v[10:17], v[200:207], 0
	v_mfma_f32_16x16x128_f8f6f4 v[124:127], v[2:9], v[200:207], 0
	v_mfma_f32_16x16x128_f8f6f4 v[116:119], v[2:9], v[222:229], 0
	v_mfma_f32_16x16x128_f8f6f4 v[120:123], v[10:17], v[222:229], 0
	v_mfma_f32_16x16x128_f8f6f4 v[112:115], v[10:17], v[230:237], 0
	v_mfma_f32_16x16x128_f8f6f4 v[108:111], v[2:9], v[230:237], 0
	v_mfma_f32_16x16x128_f8f6f4 v[100:103], v[2:9], v[238:245], 0
	v_mfma_f32_16x16x128_f8f6f4 v[104:107], v[10:17], v[238:245], 0
	s_barrier
	s_setprio 0
	s_add_i32 s60, s60, s40
	v_lshl_add_u64 v[174:175], s[22:23], 0, v[34:35]
	s_add_i32 s61, s60, 0x2000
	v_lshl_add_u64 v[178:179], v[174:175], 0, s[28:29]
	s_mov_b32 m0, s60
	v_lshl_add_u64 v[190:191], s[22:23], 0, v[164:165]
	s_add_u32 s36, s22, 0x20100
	ds_read_b128 v[200:203], v197 offset:16384
	ds_read_b128 v[204:207], v197 offset:17408
	ds_read_b128 v[222:225], v197 offset:18432
	ds_read_b128 v[226:229], v197 offset:19456
	ds_read_b128 v[230:233], v197 offset:20480
	ds_read_b128 v[234:237], v197 offset:21504
	ds_read_b128 v[238:241], v197 offset:22528
	ds_read_b128 v[242:245], v197 offset:23552
	global_load_lds_dwordx4 v[178:179], off
	v_lshl_add_u64 v[178:179], v[190:191], 0, s[28:29]
	s_mov_b32 m0, s61
	s_addc_u32 s37, s23, 0
	s_add_i32 s62, s62, s40
	global_load_lds_dwordx4 v[178:179], off
	v_lshl_add_u64 v[178:179], s[36:37], 0, v[34:35]
	s_mov_b32 m0, s62
	s_add_i32 s63, s62, 0x2000
	global_load_lds_dwordx4 v[178:179], off
	v_lshl_add_u64 v[178:179], s[36:37], 0, v[164:165]
	s_mov_b32 m0, s63
	v_lshl_add_u64 v[192:193], s[30:31], 0, v[168:169]
	global_load_lds_dwordx4 v[178:179], off
	v_lshl_add_u64 v[178:179], v[192:193], 0, s[28:29]
	s_mov_b32 m0, s41
	v_lshl_add_u64 v[194:195], s[30:31], 0, v[166:167]
	global_load_lds_dwordx4 v[178:179], off
	v_lshl_add_u64 v[178:179], v[194:195], 0, s[28:29]
	s_mov_b32 m0, s42
	s_nop 0
	global_load_lds_dwordx4 v[178:179], off
	s_waitcnt vmcnt(8)
	s_waitcnt lgkmcnt(0)
	s_barrier
	v_mfma_f32_16x16x128_f8f6f4 v[96:99], v[26:33], v[200:207], 0
	s_setprio 1
	v_mfma_f32_16x16x128_f8f6f4 v[92:95], v[18:25], v[200:207], 0
	v_mfma_f32_16x16x128_f8f6f4 v[84:87], v[18:25], v[222:229], 0
	v_mfma_f32_16x16x128_f8f6f4 v[88:91], v[26:33], v[222:229], 0
	v_mfma_f32_16x16x128_f8f6f4 v[80:83], v[26:33], v[230:237], 0
	v_mfma_f32_16x16x128_f8f6f4 v[76:79], v[18:25], v[230:237], 0
	v_mfma_f32_16x16x128_f8f6f4 v[68:71], v[18:25], v[238:245], 0
	v_mfma_f32_16x16x128_f8f6f4 v[72:75], v[26:33], v[238:245], 0
	s_setprio 0
	s_setprio 1
	v_mfma_f32_16x16x128_f8f6f4 v[64:67], v[10:17], v[200:207], 0
	v_mfma_f32_16x16x128_f8f6f4 v[60:63], v[2:9], v[200:207], 0
	v_mfma_f32_16x16x128_f8f6f4 v[52:55], v[2:9], v[222:229], 0
	v_mfma_f32_16x16x128_f8f6f4 v[56:59], v[10:17], v[222:229], 0
	v_mfma_f32_16x16x128_f8f6f4 v[48:51], v[10:17], v[230:237], 0
	v_mfma_f32_16x16x128_f8f6f4 v[44:47], v[2:9], v[230:237], 0
	v_mfma_f32_16x16x128_f8f6f4 v[36:39], v[2:9], v[238:245], 0
	v_mfma_f32_16x16x128_f8f6f4 v[40:43], v[10:17], v[238:245], 0
	s_barrier
	s_setprio 0
	s_add_i32 s64, 0, 0x18000
	s_add_i32 s66, 0, 0x1c000
	v_add_u32_e32 v200, s64, v196
	v_add_u32_e32 v201, s66, v196
	ds_read_b128 v[26:29], v200
	ds_read_b128 v[30:33], v200 offset:1024
	ds_read_b128 v[18:21], v200 offset:2048
	ds_read_b128 v[22:25], v200 offset:3072
	ds_read_b128 v[10:13], v201
	ds_read_b128 v[14:17], v201 offset:1024
	ds_read_b128 v[2:5], v201 offset:2048
	ds_read_b128 v[6:9], v201 offset:3072
	s_add_u32 s36, s30, 0x20100
	s_addc_u32 s37, s31, 0
	s_mov_b32 m0, s43
	v_lshl_add_u64 v[178:179], s[36:37], 0, v[168:169]
	ds_read_b128 v[202:205], v197 offset:32768
	ds_read_b128 v[206:209], v197 offset:33792
	ds_read_b128 v[222:225], v197 offset:34816
	ds_read_b128 v[226:229], v197 offset:35840
	ds_read_b128 v[230:233], v197 offset:36864
	ds_read_b128 v[234:237], v197 offset:37888
	ds_read_b128 v[238:241], v197 offset:38912
	ds_read_b128 v[242:245], v197 offset:39936
	global_load_lds_dwordx4 v[178:179], off
	v_lshl_add_u64 v[178:179], s[36:37], 0, v[166:167]
	s_mov_b32 m0, s44
	s_nop 0
	global_load_lds_dwordx4 v[178:179], off
	s_waitcnt vmcnt(8)
	s_waitcnt lgkmcnt(0)
	s_barrier
	v_mfma_f32_16x16x128_f8f6f4 v[160:163], v[26:33], v[202:209], v[160:163]
	s_setprio 1
	v_mfma_f32_16x16x128_f8f6f4 v[156:159], v[18:25], v[202:209], v[156:159]
	v_mfma_f32_16x16x128_f8f6f4 v[148:151], v[18:25], v[222:229], v[148:151]
	v_mfma_f32_16x16x128_f8f6f4 v[152:155], v[26:33], v[222:229], v[152:155]
	v_mfma_f32_16x16x128_f8f6f4 v[144:147], v[26:33], v[230:237], v[144:147]
	v_mfma_f32_16x16x128_f8f6f4 v[140:143], v[18:25], v[230:237], v[140:143]
	v_mfma_f32_16x16x128_f8f6f4 v[132:135], v[18:25], v[238:245], v[132:135]
	v_mfma_f32_16x16x128_f8f6f4 v[136:139], v[26:33], v[238:245], v[136:139]
	s_setprio 0
	s_setprio 1
	v_mfma_f32_16x16x128_f8f6f4 v[128:131], v[10:17], v[202:209], v[128:131]
	v_mfma_f32_16x16x128_f8f6f4 v[124:127], v[2:9], v[202:209], v[124:127]
	v_mfma_f32_16x16x128_f8f6f4 v[116:119], v[2:9], v[222:229], v[116:119]
	v_mfma_f32_16x16x128_f8f6f4 v[120:123], v[10:17], v[222:229], v[120:123]
	v_mfma_f32_16x16x128_f8f6f4 v[112:115], v[10:17], v[230:237], v[112:115]
	v_mfma_f32_16x16x128_f8f6f4 v[108:111], v[2:9], v[230:237], v[108:111]
	v_mfma_f32_16x16x128_f8f6f4 v[100:103], v[2:9], v[238:245], v[100:103]
	v_mfma_f32_16x16x128_f8f6f4 v[104:107], v[10:17], v[238:245], v[104:107]
	s_barrier
	s_setprio 0
	s_add_i32 s64, s64, s40
	s_mov_b64 s[24:25], 0x180
	s_add_i32 s65, s64, 0x2000
	v_lshl_add_u64 v[174:175], v[174:175], 0, s[24:25]
	s_mov_b32 m0, s64
	s_add_u32 s36, s22, 0x20180
	ds_read_b128 v[202:205], v197 offset:49152
	ds_read_b128 v[206:209], v197 offset:50176
	ds_read_b128 v[222:225], v197 offset:51200
	ds_read_b128 v[226:229], v197 offset:52224
	ds_read_b128 v[230:233], v197 offset:53248
	ds_read_b128 v[234:237], v197 offset:54272
	ds_read_b128 v[238:241], v197 offset:55296
	ds_read_b128 v[242:245], v197 offset:56320
	global_load_lds_dwordx4 v[174:175], off
	v_lshl_add_u64 v[174:175], v[190:191], 0, s[24:25]
	s_mov_b32 m0, s65
	s_addc_u32 s37, s23, 0
	s_add_i32 s66, s66, s40
	global_load_lds_dwordx4 v[174:175], off
	v_lshl_add_u64 v[174:175], s[36:37], 0, v[34:35]
	s_mov_b32 m0, s66
	s_add_i32 s67, s66, 0x2000
	global_load_lds_dwordx4 v[174:175], off
	v_lshl_add_u64 v[174:175], s[36:37], 0, v[164:165]
	s_mov_b32 m0, s67
	s_nop 0
	global_load_lds_dwordx4 v[174:175], off
	v_lshl_add_u64 v[174:175], v[192:193], 0, s[24:25]
	s_mov_b32 m0, s47
	s_nop 0
	global_load_lds_dwordx4 v[174:175], off
	v_lshl_add_u64 v[174:175], v[194:195], 0, s[24:25]
	s_mov_b32 m0, s48
	s_nop 0
	global_load_lds_dwordx4 v[174:175], off
	s_waitcnt vmcnt(8)
	s_waitcnt lgkmcnt(0)
	s_barrier
	v_mfma_f32_16x16x128_f8f6f4 v[96:99], v[26:33], v[202:209], v[96:99]
	s_setprio 1
	v_mfma_f32_16x16x128_f8f6f4 v[92:95], v[18:25], v[202:209], v[92:95]
	v_mfma_f32_16x16x128_f8f6f4 v[84:87], v[18:25], v[222:229], v[84:87]
	v_mfma_f32_16x16x128_f8f6f4 v[88:91], v[26:33], v[222:229], v[88:91]
	v_mfma_f32_16x16x128_f8f6f4 v[80:83], v[26:33], v[230:237], v[80:83]
	v_mfma_f32_16x16x128_f8f6f4 v[76:79], v[18:25], v[230:237], v[76:79]
	v_mfma_f32_16x16x128_f8f6f4 v[68:71], v[18:25], v[238:245], v[68:71]
	v_mfma_f32_16x16x128_f8f6f4 v[72:75], v[26:33], v[238:245], v[72:75]
	s_setprio 0
	s_setprio 1
	v_mfma_f32_16x16x128_f8f6f4 v[64:67], v[10:17], v[202:209], v[64:67]
	v_mfma_f32_16x16x128_f8f6f4 v[60:63], v[2:9], v[202:209], v[60:63]
	v_mfma_f32_16x16x128_f8f6f4 v[52:55], v[2:9], v[222:229], v[52:55]
	v_mfma_f32_16x16x128_f8f6f4 v[56:59], v[10:17], v[222:229], v[56:59]
	v_mfma_f32_16x16x128_f8f6f4 v[48:51], v[10:17], v[230:237], v[48:51]
	v_mfma_f32_16x16x128_f8f6f4 v[44:47], v[2:9], v[230:237], v[44:47]
	v_mfma_f32_16x16x128_f8f6f4 v[36:39], v[2:9], v[238:245], v[36:39]
	v_mfma_f32_16x16x128_f8f6f4 v[40:43], v[10:17], v[238:245], v[40:43]
	s_barrier
	s_setprio 0
	s_add_u32 s30, s30, 0x20180
	s_addc_u32 s31, s31, 0
	s_add_u32 s68, s22, 0x200
	s_addc_u32 s69, s23, 0
	s_mov_b32 s70, 0
.LBB0_1087:
	ds_read_b128 v[2:5], v198
	ds_read_b128 v[6:9], v198 offset:1024
	ds_read_b128 v[10:13], v198 offset:2048
	ds_read_b128 v[14:17], v198 offset:3072
	ds_read_b128 v[18:21], v199
	ds_read_b128 v[22:25], v199 offset:1024
	ds_read_b128 v[26:29], v199 offset:2048
	ds_read_b128 v[30:33], v199 offset:3072
	s_add_u32 s14, s30, 0xfffe0080
	s_addc_u32 s22, s31, -1
	s_cmp_eq_u32 s70, 4
	s_cselect_b32 s37, s54, s22
	s_cselect_b32 s36, s55, s14
	s_cselect_b32 s23, s56, s69
	s_cselect_b32 s22, s57, s68
	s_mov_b32 m0, s58
	v_lshl_add_u64 v[174:175], s[30:31], 0, v[170:171]
	ds_read_b128 v[202:205], v197
	ds_read_b128 v[206:209], v197 offset:1024
	ds_read_b128 v[222:225], v197 offset:2048
	ds_read_b128 v[226:229], v197 offset:3072
	ds_read_b128 v[230:233], v197 offset:4096
	ds_read_b128 v[234:237], v197 offset:5120
	ds_read_b128 v[238:241], v197 offset:6144
	ds_read_b128 v[242:245], v197 offset:7168
	global_load_lds_dwordx4 v[174:175], off
	v_lshl_add_u64 v[174:175], s[30:31], 0, v[172:173]
	s_mov_b32 m0, s59
	s_nop 0
	global_load_lds_dwordx4 v[174:175], off
	s_waitcnt vmcnt(8)
	s_waitcnt lgkmcnt(0)
	s_barrier
	v_mfma_f32_16x16x128_f8f6f4 v[160:163], v[2:9], v[202:209], v[160:163]
	s_setprio 1
	v_mfma_f32_16x16x128_f8f6f4 v[156:159], v[10:17], v[202:209], v[156:159]
	v_mfma_f32_16x16x128_f8f6f4 v[148:151], v[10:17], v[222:229], v[148:151]
	v_mfma_f32_16x16x128_f8f6f4 v[152:155], v[2:9], v[222:229], v[152:155]
	v_mfma_f32_16x16x128_f8f6f4 v[144:147], v[2:9], v[230:237], v[144:147]
	v_mfma_f32_16x16x128_f8f6f4 v[140:143], v[10:17], v[230:237], v[140:143]
	v_mfma_f32_16x16x128_f8f6f4 v[132:135], v[10:17], v[238:245], v[132:135]
	v_mfma_f32_16x16x128_f8f6f4 v[136:139], v[2:9], v[238:245], v[136:139]
	s_setprio 0
	s_setprio 1
	v_mfma_f32_16x16x128_f8f6f4 v[128:131], v[18:25], v[202:209], v[128:131]
	v_mfma_f32_16x16x128_f8f6f4 v[124:127], v[26:33], v[202:209], v[124:127]
	v_mfma_f32_16x16x128_f8f6f4 v[116:119], v[26:33], v[222:229], v[116:119]
	v_mfma_f32_16x16x128_f8f6f4 v[120:123], v[18:25], v[222:229], v[120:123]
	v_mfma_f32_16x16x128_f8f6f4 v[112:115], v[18:25], v[230:237], v[112:115]
	v_mfma_f32_16x16x128_f8f6f4 v[108:111], v[26:33], v[230:237], v[108:111]
	v_mfma_f32_16x16x128_f8f6f4 v[100:103], v[26:33], v[238:245], v[100:103]
	v_mfma_f32_16x16x128_f8f6f4 v[104:107], v[18:25], v[238:245], v[104:107]
	s_barrier
	s_setprio 0
	s_mov_b32 m0, s60
	v_lshl_add_u64 v[174:175], s[22:23], 0, v[34:35]
	s_add_u32 s72, s22, 0x20000
	ds_read_b128 v[202:205], v197 offset:16384
	ds_read_b128 v[206:209], v197 offset:17408
	ds_read_b128 v[222:225], v197 offset:18432
	ds_read_b128 v[226:229], v197 offset:19456
	ds_read_b128 v[230:233], v197 offset:20480
	ds_read_b128 v[234:237], v197 offset:21504
	ds_read_b128 v[238:241], v197 offset:22528
	ds_read_b128 v[242:245], v197 offset:23552
	global_load_lds_dwordx4 v[174:175], off
	v_lshl_add_u64 v[190:191], s[22:23], 0, v[164:165]
	s_mov_b32 m0, s61
	s_addc_u32 s73, s23, 0
	global_load_lds_dwordx4 v[190:191], off
	v_lshl_add_u64 v[178:179], s[72:73], 0, v[34:35]
	s_mov_b32 m0, s62
	v_lshl_add_u64 v[192:193], s[36:37], 0, v[168:169]
	global_load_lds_dwordx4 v[178:179], off
	v_lshl_add_u64 v[178:179], s[72:73], 0, v[164:165]
	s_mov_b32 m0, s63
	v_lshl_add_u64 v[194:195], s[36:37], 0, v[166:167]
	global_load_lds_dwordx4 v[178:179], off
	s_mov_b32 m0, s41
	s_nop 0
	global_load_lds_dwordx4 v[192:193], off
	s_mov_b32 m0, s42
	s_nop 0
	global_load_lds_dwordx4 v[194:195], off
	s_waitcnt vmcnt(8)
	s_waitcnt lgkmcnt(0)
	s_barrier
	v_mfma_f32_16x16x128_f8f6f4 v[96:99], v[2:9], v[202:209], v[96:99]
	s_setprio 1
	v_mfma_f32_16x16x128_f8f6f4 v[92:95], v[10:17], v[202:209], v[92:95]
	v_mfma_f32_16x16x128_f8f6f4 v[84:87], v[10:17], v[222:229], v[84:87]
	v_mfma_f32_16x16x128_f8f6f4 v[88:91], v[2:9], v[222:229], v[88:91]
	v_mfma_f32_16x16x128_f8f6f4 v[80:83], v[2:9], v[230:237], v[80:83]
	v_mfma_f32_16x16x128_f8f6f4 v[76:79], v[10:17], v[230:237], v[76:79]
	v_mfma_f32_16x16x128_f8f6f4 v[68:71], v[10:17], v[238:245], v[68:71]
	v_mfma_f32_16x16x128_f8f6f4 v[72:75], v[2:9], v[238:245], v[72:75]
	s_setprio 0
	s_setprio 1
	v_mfma_f32_16x16x128_f8f6f4 v[64:67], v[18:25], v[202:209], v[64:67]
	v_mfma_f32_16x16x128_f8f6f4 v[60:63], v[26:33], v[202:209], v[60:63]
	v_mfma_f32_16x16x128_f8f6f4 v[52:55], v[26:33], v[222:229], v[52:55]
	v_mfma_f32_16x16x128_f8f6f4 v[56:59], v[18:25], v[222:229], v[56:59]
	v_mfma_f32_16x16x128_f8f6f4 v[48:51], v[18:25], v[230:237], v[48:51]
	v_mfma_f32_16x16x128_f8f6f4 v[44:47], v[26:33], v[230:237], v[44:47]
	v_mfma_f32_16x16x128_f8f6f4 v[36:39], v[26:33], v[238:245], v[36:39]
	v_mfma_f32_16x16x128_f8f6f4 v[40:43], v[18:25], v[238:245], v[40:43]
	s_barrier
	s_setprio 0
	ds_read_b128 v[26:29], v200
	ds_read_b128 v[30:33], v200 offset:1024
	ds_read_b128 v[18:21], v200 offset:2048
	ds_read_b128 v[22:25], v200 offset:3072
	ds_read_b128 v[10:13], v201
	ds_read_b128 v[14:17], v201 offset:1024
	ds_read_b128 v[2:5], v201 offset:2048
	ds_read_b128 v[6:9], v201 offset:3072
	s_add_u32 s36, s36, 0x20000
	s_addc_u32 s37, s37, 0
	s_mov_b32 m0, s43
	v_lshl_add_u64 v[178:179], s[36:37], 0, v[168:169]
	ds_read_b128 v[202:205], v197 offset:32768
	ds_read_b128 v[206:209], v197 offset:33792
	ds_read_b128 v[222:225], v197 offset:34816
	ds_read_b128 v[226:229], v197 offset:35840
	ds_read_b128 v[230:233], v197 offset:36864
	ds_read_b128 v[234:237], v197 offset:37888
	ds_read_b128 v[238:241], v197 offset:38912
	ds_read_b128 v[242:245], v197 offset:39936
	global_load_lds_dwordx4 v[178:179], off
	v_lshl_add_u64 v[178:179], s[36:37], 0, v[166:167]
	s_mov_b32 m0, s44
	s_nop 0
	global_load_lds_dwordx4 v[178:179], off
	s_waitcnt vmcnt(8)
	s_waitcnt lgkmcnt(0)
	s_barrier
	v_mfma_f32_16x16x128_f8f6f4 v[160:163], v[26:33], v[202:209], v[160:163]
	s_setprio 1
	v_mfma_f32_16x16x128_f8f6f4 v[156:159], v[18:25], v[202:209], v[156:159]
	v_mfma_f32_16x16x128_f8f6f4 v[148:151], v[18:25], v[222:229], v[148:151]
	v_mfma_f32_16x16x128_f8f6f4 v[152:155], v[26:33], v[222:229], v[152:155]
	v_mfma_f32_16x16x128_f8f6f4 v[144:147], v[26:33], v[230:237], v[144:147]
	v_mfma_f32_16x16x128_f8f6f4 v[140:143], v[18:25], v[230:237], v[140:143]
	v_mfma_f32_16x16x128_f8f6f4 v[132:135], v[18:25], v[238:245], v[132:135]
	v_mfma_f32_16x16x128_f8f6f4 v[136:139], v[26:33], v[238:245], v[136:139]
	s_setprio 0
	s_setprio 1
	v_mfma_f32_16x16x128_f8f6f4 v[128:131], v[10:17], v[202:209], v[128:131]
	v_mfma_f32_16x16x128_f8f6f4 v[124:127], v[2:9], v[202:209], v[124:127]
	v_mfma_f32_16x16x128_f8f6f4 v[116:119], v[2:9], v[222:229], v[116:119]
	v_mfma_f32_16x16x128_f8f6f4 v[120:123], v[10:17], v[222:229], v[120:123]
	v_mfma_f32_16x16x128_f8f6f4 v[112:115], v[10:17], v[230:237], v[112:115]
	v_mfma_f32_16x16x128_f8f6f4 v[108:111], v[2:9], v[230:237], v[108:111]
	v_mfma_f32_16x16x128_f8f6f4 v[100:103], v[2:9], v[238:245], v[100:103]
	v_mfma_f32_16x16x128_f8f6f4 v[104:107], v[10:17], v[238:245], v[104:107]
	s_barrier
	s_setprio 0
	s_mov_b32 m0, s64
	v_lshl_add_u64 v[174:175], v[174:175], 0, s[18:19]
	s_add_u32 s22, s22, 0x20080
	ds_read_b128 v[202:205], v197 offset:49152
	ds_read_b128 v[206:209], v197 offset:50176
	ds_read_b128 v[222:225], v197 offset:51200
	ds_read_b128 v[226:229], v197 offset:52224
	ds_read_b128 v[230:233], v197 offset:53248
	ds_read_b128 v[234:237], v197 offset:54272
	ds_read_b128 v[238:241], v197 offset:55296
	ds_read_b128 v[242:245], v197 offset:56320
	global_load_lds_dwordx4 v[174:175], off
	v_lshl_add_u64 v[174:175], v[190:191], 0, s[18:19]
	s_mov_b32 m0, s65
	s_addc_u32 s23, s23, 0
	global_load_lds_dwordx4 v[174:175], off
	v_lshl_add_u64 v[174:175], s[22:23], 0, v[34:35]
	s_mov_b32 m0, s66
	s_nop 0
	global_load_lds_dwordx4 v[174:175], off
	v_lshl_add_u64 v[174:175], s[22:23], 0, v[164:165]
	s_mov_b32 m0, s67
	s_nop 0
	global_load_lds_dwordx4 v[174:175], off
	v_lshl_add_u64 v[174:175], v[192:193], 0, s[18:19]
	s_mov_b32 m0, s47
	s_nop 0
	global_load_lds_dwordx4 v[174:175], off
	v_lshl_add_u64 v[174:175], v[194:195], 0, s[18:19]
	s_mov_b32 m0, s48
	s_nop 0
	global_load_lds_dwordx4 v[174:175], off
	s_waitcnt vmcnt(8)
	s_waitcnt lgkmcnt(0)
	s_barrier
	v_mfma_f32_16x16x128_f8f6f4 v[96:99], v[26:33], v[202:209], v[96:99]
	s_setprio 1
	v_mfma_f32_16x16x128_f8f6f4 v[92:95], v[18:25], v[202:209], v[92:95]
	v_mfma_f32_16x16x128_f8f6f4 v[84:87], v[18:25], v[222:229], v[84:87]
	v_mfma_f32_16x16x128_f8f6f4 v[88:91], v[26:33], v[222:229], v[88:91]
	v_mfma_f32_16x16x128_f8f6f4 v[80:83], v[26:33], v[230:237], v[80:83]
	v_mfma_f32_16x16x128_f8f6f4 v[76:79], v[18:25], v[230:237], v[76:79]
	v_mfma_f32_16x16x128_f8f6f4 v[68:71], v[18:25], v[238:245], v[68:71]
	v_mfma_f32_16x16x128_f8f6f4 v[72:75], v[26:33], v[238:245], v[72:75]
	s_setprio 0
	s_setprio 1
	v_mfma_f32_16x16x128_f8f6f4 v[64:67], v[10:17], v[202:209], v[64:67]
	v_mfma_f32_16x16x128_f8f6f4 v[60:63], v[2:9], v[202:209], v[60:63]
	v_mfma_f32_16x16x128_f8f6f4 v[52:55], v[2:9], v[222:229], v[52:55]
	v_mfma_f32_16x16x128_f8f6f4 v[56:59], v[10:17], v[222:229], v[56:59]
	v_mfma_f32_16x16x128_f8f6f4 v[48:51], v[10:17], v[230:237], v[48:51]
	v_mfma_f32_16x16x128_f8f6f4 v[44:47], v[2:9], v[230:237], v[44:47]
	v_mfma_f32_16x16x128_f8f6f4 v[36:39], v[2:9], v[238:245], v[36:39]
	v_mfma_f32_16x16x128_f8f6f4 v[40:43], v[10:17], v[238:245], v[40:43]
	s_barrier
	s_setprio 0
	s_add_i32 s70, s70, 2
	s_add_u32 s30, s30, 0x100
	s_addc_u32 s31, s31, 0
	s_add_u32 s68, s68, 0x100
	s_addc_u32 s69, s69, 0
	s_cmp_gt_u32 s70, 5
	s_cbranch_scc0 .LBB0_1087

.LBB0_1160:
	s_add_u32 s22, s30, 0x100
	s_addc_u32 s23, s31, 0
	s_add_i32 s65, 0, 0x10000
	s_cmp_eq_u32 s64, 18
	s_cselect_b32 s41, s58, s23
	s_cselect_b32 s40, s59, s22
	s_cselect_b32 s37, s60, s63
	s_cselect_b32 s36, s61, s62
	s_add_i32 s66, 0, 0x14000
	v_add_u32_e32 v2, s65, v222
	v_add_u32_e32 v6, s66, v222
	ds_read_b128 v[26:29], v2
	ds_read_b128 v[30:33], v2 offset:1024
	ds_read_b128 v[18:21], v2 offset:2048
	ds_read_b128 v[22:25], v2 offset:3072
	ds_read_b128 v[10:13], v6
	ds_read_b128 v[14:17], v6 offset:1024
	ds_read_b128 v[2:5], v6 offset:2048
	ds_read_b128 v[6:9], v6 offset:3072
	v_lshl_add_u64 v[174:175], s[30:31], 0, v[170:171]
	s_add_i32 m0, s43, 0xc000
	ds_read_b128 v[190:193], v223
	ds_read_b128 v[194:197], v223 offset:1024
	ds_read_b128 v[198:201], v223 offset:2048
	ds_read_b128 v[202:205], v223 offset:3072
	ds_read_b128 v[224:227], v223 offset:4096
	ds_read_b128 v[228:231], v223 offset:5120
	ds_read_b128 v[232:235], v223 offset:6144
	ds_read_b128 v[236:239], v223 offset:7168
	global_load_lds_dwordx4 v[174:175], off
	v_lshl_add_u64 v[174:175], s[30:31], 0, v[172:173]
	s_add_i32 m0, s43, 0xe000
	s_nop 0
	global_load_lds_dwordx4 v[174:175], off
	s_waitcnt vmcnt(8)
	s_waitcnt lgkmcnt(0)
	s_barrier
	v_mfma_f32_16x16x128_f8f6f4 v[160:163], v[26:33], v[190:197], v[160:163]
	s_setprio 1
	v_mfma_f32_16x16x128_f8f6f4 v[156:159], v[18:25], v[190:197], v[156:159]
	v_mfma_f32_16x16x128_f8f6f4 v[140:143], v[18:25], v[198:205], v[140:143]
	v_mfma_f32_16x16x128_f8f6f4 v[144:147], v[26:33], v[198:205], v[144:147]
	v_mfma_f32_16x16x128_f8f6f4 v[132:135], v[26:33], v[224:231], v[132:135]
	v_mfma_f32_16x16x128_f8f6f4 v[124:127], v[18:25], v[224:231], v[124:127]
	v_mfma_f32_16x16x128_f8f6f4 v[108:111], v[18:25], v[232:239], v[108:111]
	v_mfma_f32_16x16x128_f8f6f4 v[116:119], v[26:33], v[232:239], v[116:119]
	s_setprio 0
	s_setprio 1
	v_mfma_f32_16x16x128_f8f6f4 v[152:155], v[10:17], v[190:197], v[152:155]
	v_mfma_f32_16x16x128_f8f6f4 v[148:151], v[2:9], v[190:197], v[148:151]
	v_mfma_f32_16x16x128_f8f6f4 v[128:131], v[2:9], v[198:205], v[128:131]
	v_mfma_f32_16x16x128_f8f6f4 v[136:139], v[10:17], v[198:205], v[136:139]
	v_mfma_f32_16x16x128_f8f6f4 v[120:123], v[10:17], v[224:231], v[120:123]
	v_mfma_f32_16x16x128_f8f6f4 v[112:115], v[2:9], v[224:231], v[112:115]
	v_mfma_f32_16x16x128_f8f6f4 v[100:103], v[2:9], v[232:239], v[100:103]
	v_mfma_f32_16x16x128_f8f6f4 v[104:107], v[10:17], v[232:239], v[104:107]
	s_barrier
	s_setprio 0
	s_add_i32 s14, s65, s42
	v_lshl_add_u64 v[174:175], s[36:37], 0, v[34:35]
	s_mov_b32 m0, s14
	ds_read_b128 v[196:199], v223 offset:16384
	ds_read_b128 v[200:203], v223 offset:17408
	ds_read_b128 v[204:207], v223 offset:18432
	ds_read_b128 v[208:211], v223 offset:19456
	ds_read_b128 v[224:227], v223 offset:20480
	ds_read_b128 v[228:231], v223 offset:21504
	ds_read_b128 v[232:235], v223 offset:22528
	ds_read_b128 v[236:239], v223 offset:23552
	global_load_lds_dwordx4 v[174:175], off
	s_add_i32 m0, s14, 0x2000
	s_add_u32 s30, s36, 0x58000
	v_lshl_add_u64 v[190:191], s[36:37], 0, v[164:165]
	s_addc_u32 s31, s37, 0
	s_add_i32 s14, s66, s42
	global_load_lds_dwordx4 v[190:191], off
	v_lshl_add_u64 v[178:179], s[30:31], 0, v[34:35]
	s_mov_b32 m0, s14
	v_lshl_add_u64 v[192:193], s[40:41], 0, v[168:169]
	global_load_lds_dwordx4 v[178:179], off
	v_lshl_add_u64 v[178:179], s[30:31], 0, v[164:165]
	s_add_i32 m0, s14, 0x2000
	v_lshl_add_u64 v[194:195], s[40:41], 0, v[166:167]
	global_load_lds_dwordx4 v[178:179], off
	s_mov_b32 m0, s43
	s_nop 0
	global_load_lds_dwordx4 v[192:193], off
	s_mov_b32 m0, s44
	s_nop 0
	global_load_lds_dwordx4 v[194:195], off
	s_waitcnt vmcnt(8)
	s_waitcnt lgkmcnt(0)
	s_barrier
	v_mfma_f32_16x16x128_f8f6f4 v[96:99], v[26:33], v[196:203], v[96:99]
	s_setprio 1
	v_mfma_f32_16x16x128_f8f6f4 v[92:95], v[18:25], v[196:203], v[92:95]
	v_mfma_f32_16x16x128_f8f6f4 v[76:79], v[18:25], v[204:211], v[76:79]
	v_mfma_f32_16x16x128_f8f6f4 v[84:87], v[26:33], v[204:211], v[84:87]
	v_mfma_f32_16x16x128_f8f6f4 v[68:71], v[26:33], v[224:231], v[68:71]
	v_mfma_f32_16x16x128_f8f6f4 v[60:63], v[18:25], v[224:231], v[60:63]
	v_mfma_f32_16x16x128_f8f6f4 v[44:47], v[18:25], v[232:239], v[44:47]
	v_mfma_f32_16x16x128_f8f6f4 v[52:55], v[26:33], v[232:239], v[52:55]
	s_setprio 0
	s_setprio 1
	v_mfma_f32_16x16x128_f8f6f4 v[88:91], v[10:17], v[196:203], v[88:91]
	v_mfma_f32_16x16x128_f8f6f4 v[80:83], v[2:9], v[196:203], v[80:83]
	v_mfma_f32_16x16x128_f8f6f4 v[64:67], v[2:9], v[204:211], v[64:67]
	v_mfma_f32_16x16x128_f8f6f4 v[72:75], v[10:17], v[204:211], v[72:75]
	v_mfma_f32_16x16x128_f8f6f4 v[56:59], v[10:17], v[224:231], v[56:59]
	v_mfma_f32_16x16x128_f8f6f4 v[48:51], v[2:9], v[224:231], v[48:51]
	v_mfma_f32_16x16x128_f8f6f4 v[36:39], v[2:9], v[232:239], v[36:39]
	v_mfma_f32_16x16x128_f8f6f4 v[40:43], v[10:17], v[232:239], v[40:43]
	s_barrier
	s_setprio 0
	s_add_i32 s14, 0, 0x18000
	s_add_i32 s65, 0, 0x1c000
	v_add_u32_e32 v14, s14, v222
	v_add_u32_e32 v30, s65, v222
	ds_read_b128 v[2:5], v14
	ds_read_b128 v[6:9], v14 offset:1024
	ds_read_b128 v[10:13], v14 offset:2048
	ds_read_b128 v[14:17], v14 offset:3072
	ds_read_b128 v[18:21], v30
	ds_read_b128 v[22:25], v30 offset:1024
	ds_read_b128 v[26:29], v30 offset:2048
	ds_read_b128 v[30:33], v30 offset:3072
	s_add_u32 s30, s40, 0x58000
	s_addc_u32 s31, s41, 0
	s_mov_b32 m0, s45
	v_lshl_add_u64 v[178:179], s[30:31], 0, v[168:169]
	ds_read_b128 v[196:199], v223 offset:32768
	ds_read_b128 v[200:203], v223 offset:33792
	ds_read_b128 v[204:207], v223 offset:34816
	ds_read_b128 v[208:211], v223 offset:35840
	ds_read_b128 v[224:227], v223 offset:36864
	ds_read_b128 v[228:231], v223 offset:37888
	ds_read_b128 v[232:235], v223 offset:38912
	ds_read_b128 v[236:239], v223 offset:39936
	global_load_lds_dwordx4 v[178:179], off
	v_lshl_add_u64 v[178:179], s[30:31], 0, v[166:167]
	s_mov_b32 m0, s46
	s_nop 0
	global_load_lds_dwordx4 v[178:179], off
	s_waitcnt vmcnt(8)
	s_waitcnt lgkmcnt(0)
	s_barrier
	v_mfma_f32_16x16x128_f8f6f4 v[160:163], v[2:9], v[196:203], v[160:163]
	s_setprio 1
	v_mfma_f32_16x16x128_f8f6f4 v[156:159], v[10:17], v[196:203], v[156:159]
	v_mfma_f32_16x16x128_f8f6f4 v[140:143], v[10:17], v[204:211], v[140:143]
	v_mfma_f32_16x16x128_f8f6f4 v[144:147], v[2:9], v[204:211], v[144:147]
	v_mfma_f32_16x16x128_f8f6f4 v[132:135], v[2:9], v[224:231], v[132:135]
	v_mfma_f32_16x16x128_f8f6f4 v[124:127], v[10:17], v[224:231], v[124:127]
	v_mfma_f32_16x16x128_f8f6f4 v[108:111], v[10:17], v[232:239], v[108:111]
	v_mfma_f32_16x16x128_f8f6f4 v[116:119], v[2:9], v[232:239], v[116:119]
	s_setprio 0
	s_setprio 1
	v_mfma_f32_16x16x128_f8f6f4 v[152:155], v[18:25], v[196:203], v[152:155]
	v_mfma_f32_16x16x128_f8f6f4 v[148:151], v[26:33], v[196:203], v[148:151]
	v_mfma_f32_16x16x128_f8f6f4 v[128:131], v[26:33], v[204:211], v[128:131]
	v_mfma_f32_16x16x128_f8f6f4 v[136:139], v[18:25], v[204:211], v[136:139]
	v_mfma_f32_16x16x128_f8f6f4 v[120:123], v[18:25], v[224:231], v[120:123]
	v_mfma_f32_16x16x128_f8f6f4 v[112:115], v[26:33], v[224:231], v[112:115]
	v_mfma_f32_16x16x128_f8f6f4 v[100:103], v[26:33], v[232:239], v[100:103]
	v_mfma_f32_16x16x128_f8f6f4 v[104:107], v[18:25], v[232:239], v[104:107]
	s_barrier
	s_setprio 0
	s_add_i32 s14, s14, s42
	v_lshl_add_u64 v[174:175], v[174:175], 0, s[18:19]
	s_mov_b32 m0, s14
	ds_read_b128 v[196:199], v223 offset:49152
	ds_read_b128 v[200:203], v223 offset:50176
	ds_read_b128 v[204:207], v223 offset:51200
	ds_read_b128 v[208:211], v223 offset:52224
	ds_read_b128 v[224:227], v223 offset:53248
	ds_read_b128 v[228:231], v223 offset:54272
	ds_read_b128 v[232:235], v223 offset:55296
	ds_read_b128 v[236:239], v223 offset:56320
	global_load_lds_dwordx4 v[174:175], off
	s_add_i32 m0, s14, 0x2000
	s_add_u32 s30, s36, 0x58080
	v_lshl_add_u64 v[174:175], v[190:191], 0, s[18:19]
	s_addc_u32 s31, s37, 0
	s_add_i32 s14, s65, s42
	global_load_lds_dwordx4 v[174:175], off
	v_lshl_add_u64 v[174:175], s[30:31], 0, v[34:35]
	s_mov_b32 m0, s14
	s_nop 0
	global_load_lds_dwordx4 v[174:175], off
	v_lshl_add_u64 v[174:175], s[30:31], 0, v[164:165]
	s_add_i32 m0, s14, 0x2000
	s_nop 0
	global_load_lds_dwordx4 v[174:175], off
	v_lshl_add_u64 v[174:175], v[192:193], 0, s[18:19]
	s_mov_b32 m0, s51
	s_nop 0
	global_load_lds_dwordx4 v[174:175], off
	v_lshl_add_u64 v[174:175], v[194:195], 0, s[18:19]
	s_mov_b32 m0, s52
	s_nop 0
	global_load_lds_dwordx4 v[174:175], off
	s_waitcnt vmcnt(8)
	s_waitcnt lgkmcnt(0)
	s_barrier
	v_mfma_f32_16x16x128_f8f6f4 v[96:99], v[2:9], v[196:203], v[96:99]
	s_setprio 1
	v_mfma_f32_16x16x128_f8f6f4 v[92:95], v[10:17], v[196:203], v[92:95]
	v_mfma_f32_16x16x128_f8f6f4 v[76:79], v[10:17], v[204:211], v[76:79]
	v_mfma_f32_16x16x128_f8f6f4 v[84:87], v[2:9], v[204:211], v[84:87]
	v_mfma_f32_16x16x128_f8f6f4 v[68:71], v[2:9], v[224:231], v[68:71]
	v_mfma_f32_16x16x128_f8f6f4 v[60:63], v[10:17], v[224:231], v[60:63]
	v_mfma_f32_16x16x128_f8f6f4 v[44:47], v[10:17], v[232:239], v[44:47]
	v_mfma_f32_16x16x128_f8f6f4 v[52:55], v[2:9], v[232:239], v[52:55]
	s_setprio 0
	s_setprio 1
	v_mfma_f32_16x16x128_f8f6f4 v[88:91], v[18:25], v[196:203], v[88:91]
	v_mfma_f32_16x16x128_f8f6f4 v[80:83], v[26:33], v[196:203], v[80:83]
	v_mfma_f32_16x16x128_f8f6f4 v[64:67], v[26:33], v[204:211], v[64:67]
	v_mfma_f32_16x16x128_f8f6f4 v[72:75], v[18:25], v[204:211], v[72:75]
	v_mfma_f32_16x16x128_f8f6f4 v[56:59], v[18:25], v[224:231], v[56:59]
	v_mfma_f32_16x16x128_f8f6f4 v[48:51], v[26:33], v[224:231], v[48:51]
	v_mfma_f32_16x16x128_f8f6f4 v[36:39], v[26:33], v[232:239], v[36:39]
	v_mfma_f32_16x16x128_f8f6f4 v[40:43], v[18:25], v[232:239], v[40:43]
	s_barrier
	s_setprio 0
	s_add_i32 s64, s64, 2
	s_add_u32 s62, s62, 0x100
	s_addc_u32 s63, s63, 0
	s_cmp_gt_u32 s64, 19
	s_mov_b64 s[30:31], s[22:23]
	s_cbranch_scc0 .LBB0_1160
	s_and_b64 vcc, exec, s[8:9]
	s_mov_b32 s58, 0x19b00000
	v_readlane_b32 s59, v255, 10
	s_mov_b32 s60, 0xff61b1e6
	s_mov_b64 s[62:63], 0x800
	s_cbranch_vccz .LBB0_1163
	s_barrier
